# pass U masks from SGPR constants (shorter encodings); pass V end-of-list folded into the token switch
# speedup vs baseline: 1.0381x; 1.0058x over previous
; #define REP(i) for (int rep_ = 0; rep_ < ((PROBE_DUP == (i)) ? 2 : 1); ++rep_)
; #define PU_SX() do { int a_ = 0, b_ = 0; _Pragma("unroll") for (int q_ = 0; q_ < 4; ++q_) { a_ = __builtin_amdgcn_sdot4((int)xq[0][q_], 0x01010101, a_, false); b_ = __builtin_amdgcn_sdot4((int)xq[1][q_], 0x01010101, b_, false); } sx15 = 240 * a_ - 16 * b_; } while (0)
; __device__ __forceinline__ void phase_peer_bucket(const Params& P, unsigned char* ws, int l, LAS unsigned char* lds, int bid, int G, int lane, int wave) {
;     ...
;         int gstv = 0; if (lane <= 32) gstv = ((const int*)(ws + WS_GST))[((size_t)u * 16 + xb) * 64 + lane];
;         const int total = __builtin_amdgcn_readlane(gstv, 32);
;         float hmax = 0.f;
;         REP(30) if (total > 0) {
;             const unsigned char* X1Q = ws + WS_X1Q;
;             float xsc_v = 0.f; if (lane < 32) xsc_v = ((const float*)(ws + WS_XSC))[nbase + lane];
;             int tcur = peer3_next_nonempty(gstv, 0); int tnx = peer3_next_nonempty(gstv, tcur + 1); int tend = __builtin_amdgcn_readlane(gstv, tcur + 1);
;             u4 xq[2];
;             { const unsigned char* p = X1Q + (size_t)(nbase + tcur) * 2048u + (unsigned)lane * 16u; xq[0] = __builtin_nontemporal_load((const u4*)p); xq[1] = __builtin_nontemporal_load((const u4*)(p + 1024)); }
;             int lt = tnx, lts = (lt < 32) ? __builtin_amdgcn_readlane(gstv, lt) : 0x7fffffff;
;             float xs = __int_as_float(__builtin_amdgcn_readlane(__float_as_int(xsc_v), tcur));
;             int evn = 0; float wvn = 0.f;
;             if (lane < total) { evn = __builtin_nontemporal_load(FE + lane); wvn = __builtin_nontemporal_load(FW + lane); }
;     ...
;             int sx15; PU_SX();
.Lq_entry:
	s_mul_i32 s100, s29, 0x4400
	s_mov_b32 s65, 0x1010101
	s_mov_b32 s38, 0xf0f0f0f
	s_mov_b32 s39, 0xf0f0f0f0
	s_mov_b32 s22, 0xf
	s_mov_b32 s23, 0
	v_mov_b32_e32 v117, 0x110
	v_mad_u32_u24 v107, v208, v117, s100
	v_lshl_add_u32 v108, v208, 2, s100
	s_add_u32 s52, s12, s14
	s_addc_u32 s53, s13, s15
	s_add_u32 s52, s52, 0xa000000
	s_addc_u32 s53, s53, 0
	s_sub_u32 s58, s16, 0x8000000
	s_subb_u32 s59, s17, 0
	v_readlane_b32 s4, v254, 52
	s_lshl_b32 s4, s4, 16
	s_add_u32 s18, s12, 0x4e000000
	s_addc_u32 s19, s13, 0
	s_add_u32 s18, s18, s4
	s_addc_u32 s19, s19, 0
	s_lshl_b32 s4, s8, 11
	s_add_u32 s26, s12, 0x6b000000
	s_addc_u32 s27, s13, 0
	s_add_u32 s26, s26, s4
	s_addc_u32 s27, s27, 0
	s_add_u32 s6, s12, 0x6c000000
	s_addc_u32 s7, s13, 0
	v_mov_b32_e32 v201, 0
	v_add_lshl_u32 v117, v208, s8, 2
	v_cmp_gt_u32_e32 vcc, 32, v208
	s_and_saveexec_b64 s[4:5], vcc
	global_load_dword v201, v117, s[6:7]
	s_or_b64 exec, exec, s[4:5]
	v_mov_b32_e32 v233, 0
	v_mov_b32_e32 v87, 0
	v_mov_b32_e32 v74, 0
	v_mov_b32_e32 v78, 0
	v_add_u32_e32 v118, 0x4000000, v212
	s_and_saveexec_b64 s[4:5], s[40:41]
	global_load_dword v74, v212, s[58:59] nt
	global_load_dword v78, v118, s[58:59] nt
	s_or_b64 exec, exec, s[4:5]
	s_mov_b32 s31, 0

; #define LAS __attribute__((address_space(3)))
; __device__ __forceinline__ void peer3_dots(const u4 (&R)[PG][2], const u4 (&xq)[2], int sx15, LAS int* redrow, int g) {
;     static_assert(PG == 4, "one 16-byte LDS store per row group");
;     int d[4];
; #pragma unroll
;     for (int k = 0; k < 4; ++k) { int a = 0, ah = 0;
; #pragma unroll
;         for (int q = 0; q < 4; ++q) { const unsigned w = R[k][0][q];
;             a = __builtin_amdgcn_sdot4((int)(w & 0x0f0f0f0fu), (int)xq[0][q], a, false); ah = __builtin_amdgcn_sdot4((int)(w & 0xf0f0f0f0u), (int)xq[1][q], ah, false); }
;         d[k] = 32 * a + 2 * ah - sx15; }
;     u4 w; w.x = (unsigned)d[0]; w.y = (unsigned)d[1]; w.z = (unsigned)d[2]; w.w = (unsigned)d[3];
;     *(LAS u4*)(redrow + 4 * g) = w;
; }
.Lq_std0:
	s_waitcnt vmcnt(8)
	v_and_b32_e32 v96, s38, v0
	v_and_b32_e32 v100, s39, v0
	v_and_b32_e32 v97, s38, v1
	v_and_b32_e32 v101, s39, v1
	v_dot4_i32_i8 v104, v96, v64, 0
	v_dot4_i32_i8 v105, v100, v68, 0
	v_and_b32_e32 v98, s38, v2
	v_and_b32_e32 v102, s39, v2
	v_dot4_i32_i8 v104, v97, v65, v104
	v_dot4_i32_i8 v105, v101, v69, v105
	v_and_b32_e32 v99, s38, v3
	v_and_b32_e32 v103, s39, v3
	v_dot4_i32_i8 v104, v98, v66, v104
	v_dot4_i32_i8 v105, v102, v70, v105
	v_dot4_i32_i8 v104, v99, v67, v104
	v_dot4_i32_i8 v105, v103, v71, v105
	v_and_b32_e32 v96, s38, v4
	v_and_b32_e32 v100, s39, v4
	v_and_b32_e32 v97, s38, v5
	v_and_b32_e32 v101, s39, v5
	v_lshl_add_u32 v106, v104, 4, v105
	v_lshl_add_u32 v92, v106, 1, v72
	v_dot4_i32_i8 v126, v96, v64, 0
	v_dot4_i32_i8 v127, v100, v68, 0
	v_and_b32_e32 v98, s38, v6
	v_and_b32_e32 v102, s39, v6
	v_dot4_i32_i8 v126, v97, v65, v126
	v_dot4_i32_i8 v127, v101, v69, v127
	v_and_b32_e32 v99, s38, v7
	v_and_b32_e32 v103, s39, v7
	v_dot4_i32_i8 v126, v98, v66, v126
	v_dot4_i32_i8 v127, v102, v70, v127
	v_dot4_i32_i8 v126, v99, v67, v126
	v_dot4_i32_i8 v127, v103, v71, v127
	v_and_b32_e32 v96, s38, v8
	v_and_b32_e32 v100, s39, v8
	v_and_b32_e32 v97, s38, v9
	v_and_b32_e32 v101, s39, v9
	v_lshl_add_u32 v106, v126, 4, v127
	v_lshl_add_u32 v93, v106, 1, v72
	v_dot4_i32_i8 v104, v96, v64, 0
	v_dot4_i32_i8 v105, v100, v68, 0
	v_and_b32_e32 v98, s38, v10
	v_and_b32_e32 v102, s39, v10
	v_dot4_i32_i8 v104, v97, v65, v104
	v_dot4_i32_i8 v105, v101, v69, v105
	v_and_b32_e32 v99, s38, v11
	v_and_b32_e32 v103, s39, v11
	v_dot4_i32_i8 v104, v98, v66, v104
	v_dot4_i32_i8 v105, v102, v70, v105
	v_dot4_i32_i8 v104, v99, v67, v104
	v_dot4_i32_i8 v105, v103, v71, v105
	v_and_b32_e32 v96, s38, v12
	v_and_b32_e32 v100, s39, v12
	v_and_b32_e32 v97, s38, v13
	v_and_b32_e32 v101, s39, v13
	v_lshl_add_u32 v106, v104, 4, v105
	v_lshl_add_u32 v94, v106, 1, v72
	v_dot4_i32_i8 v126, v96, v64, 0
	v_dot4_i32_i8 v127, v100, v68, 0
	v_and_b32_e32 v98, s38, v14
	v_and_b32_e32 v102, s39, v14
	v_dot4_i32_i8 v126, v97, v65, v126
	v_dot4_i32_i8 v127, v101, v69, v127
	v_and_b32_e32 v99, s38, v15
	v_and_b32_e32 v103, s39, v15
	v_dot4_i32_i8 v126, v98, v66, v126
	v_dot4_i32_i8 v127, v102, v70, v127
	v_dot4_i32_i8 v126, v99, v67, v126
	v_dot4_i32_i8 v127, v103, v71, v127
	s_nop 0
	v_readlane_b32 s36, v75, 12
	v_readlane_b32 s5, v75, 13
	v_readlane_b32 s6, v75, 14
	v_readlane_b32 s7, v75, 15
	v_lshl_add_u32 v106, v126, 4, v127
	v_lshl_add_u32 v95, v106, 1, v72
	v_add_u32_e32 v113, s36, v206
	v_add_u32_e32 v114, s5, v206
	v_add_u32_e32 v115, s6, v206
	v_add_u32_e32 v116, s7, v206
	global_load_dwordx4 v[48:51], v113, s[52:53]
	global_load_dwordx4 v[52:55], v114, s[52:53]
	global_load_dwordx4 v[56:59], v115, s[52:53]
	global_load_dwordx4 v[60:63], v116, s[52:53]
	ds_write_b128 v107, v[92:95] offset:0
	s_mov_b64 exec, s[22:23]
	v_mov_b32_e32 v87, s10
	s_mov_b64 exec, -1

; #define LAS __attribute__((address_space(3)))
; __device__ __forceinline__ void peer3_dots(const u4 (&R)[PG][2], const u4 (&xq)[2], int sx15, LAS int* redrow, int g) {
;     static_assert(PG == 4, "one 16-byte LDS store per row group");
;     int d[4];
; #pragma unroll
;     for (int k = 0; k < 4; ++k) { int a = 0, ah = 0;
; #pragma unroll
;         for (int q = 0; q < 4; ++q) { const unsigned w = R[k][0][q];
;             a = __builtin_amdgcn_sdot4((int)(w & 0x0f0f0f0fu), (int)xq[0][q], a, false); ah = __builtin_amdgcn_sdot4((int)(w & 0xf0f0f0f0u), (int)xq[1][q], ah, false); }
;         d[k] = 32 * a + 2 * ah - sx15; }
;     u4 w; w.x = (unsigned)d[0]; w.y = (unsigned)d[1]; w.z = (unsigned)d[2]; w.w = (unsigned)d[3];
;     *(LAS u4*)(redrow + 4 * g) = w;
; }
.Lq_std1:
	s_waitcnt vmcnt(8)
	v_and_b32_e32 v96, s38, v16
	v_and_b32_e32 v100, s39, v16
	v_and_b32_e32 v97, s38, v17
	v_and_b32_e32 v101, s39, v17
	v_dot4_i32_i8 v104, v96, v64, 0
	v_dot4_i32_i8 v105, v100, v68, 0
	v_and_b32_e32 v98, s38, v18
	v_and_b32_e32 v102, s39, v18
	v_dot4_i32_i8 v104, v97, v65, v104
	v_dot4_i32_i8 v105, v101, v69, v105
	v_and_b32_e32 v99, s38, v19
	v_and_b32_e32 v103, s39, v19
	v_dot4_i32_i8 v104, v98, v66, v104
	v_dot4_i32_i8 v105, v102, v70, v105
	v_dot4_i32_i8 v104, v99, v67, v104
	v_dot4_i32_i8 v105, v103, v71, v105
	v_and_b32_e32 v96, s38, v20
	v_and_b32_e32 v100, s39, v20
	v_and_b32_e32 v97, s38, v21
	v_and_b32_e32 v101, s39, v21
	v_lshl_add_u32 v106, v104, 4, v105
	v_lshl_add_u32 v92, v106, 1, v72
	v_dot4_i32_i8 v126, v96, v64, 0
	v_dot4_i32_i8 v127, v100, v68, 0
	v_and_b32_e32 v98, s38, v22
	v_and_b32_e32 v102, s39, v22
	v_dot4_i32_i8 v126, v97, v65, v126
	v_dot4_i32_i8 v127, v101, v69, v127
	v_and_b32_e32 v99, s38, v23
	v_and_b32_e32 v103, s39, v23
	v_dot4_i32_i8 v126, v98, v66, v126
	v_dot4_i32_i8 v127, v102, v70, v127
	v_dot4_i32_i8 v126, v99, v67, v126
	v_dot4_i32_i8 v127, v103, v71, v127
	v_and_b32_e32 v96, s38, v24
	v_and_b32_e32 v100, s39, v24
	v_and_b32_e32 v97, s38, v25
	v_and_b32_e32 v101, s39, v25
	v_lshl_add_u32 v106, v126, 4, v127
	v_lshl_add_u32 v93, v106, 1, v72
	v_dot4_i32_i8 v104, v96, v64, 0
	v_dot4_i32_i8 v105, v100, v68, 0
	v_and_b32_e32 v98, s38, v26
	v_and_b32_e32 v102, s39, v26
	v_dot4_i32_i8 v104, v97, v65, v104
	v_dot4_i32_i8 v105, v101, v69, v105
	v_and_b32_e32 v99, s38, v27
	v_and_b32_e32 v103, s39, v27
	v_dot4_i32_i8 v104, v98, v66, v104
	v_dot4_i32_i8 v105, v102, v70, v105
	v_dot4_i32_i8 v104, v99, v67, v104
	v_dot4_i32_i8 v105, v103, v71, v105
	v_and_b32_e32 v96, s38, v28
	v_and_b32_e32 v100, s39, v28
	v_and_b32_e32 v97, s38, v29
	v_and_b32_e32 v101, s39, v29
	v_lshl_add_u32 v106, v104, 4, v105
	v_lshl_add_u32 v94, v106, 1, v72
	v_dot4_i32_i8 v126, v96, v64, 0
	v_dot4_i32_i8 v127, v100, v68, 0
	v_and_b32_e32 v98, s38, v30
	v_and_b32_e32 v102, s39, v30
	v_dot4_i32_i8 v126, v97, v65, v126
	v_dot4_i32_i8 v127, v101, v69, v127
	v_and_b32_e32 v99, s38, v31
	v_and_b32_e32 v103, s39, v31
	v_dot4_i32_i8 v126, v98, v66, v126
	v_dot4_i32_i8 v127, v102, v70, v127
	v_dot4_i32_i8 v126, v99, v67, v126
	v_dot4_i32_i8 v127, v103, v71, v127
	s_nop 0
	v_readlane_b32 s36, v75, 16
	v_readlane_b32 s5, v75, 17
	v_readlane_b32 s6, v75, 18
	v_readlane_b32 s7, v75, 19
	v_lshl_add_u32 v106, v126, 4, v127
	v_lshl_add_u32 v95, v106, 1, v72
	v_add_u32_e32 v113, s36, v206
	v_add_u32_e32 v114, s5, v206
	v_add_u32_e32 v115, s6, v206
	v_add_u32_e32 v116, s7, v206
	global_load_dwordx4 v[0:3], v113, s[52:53]
	global_load_dwordx4 v[4:7], v114, s[52:53]
	global_load_dwordx4 v[8:11], v115, s[52:53]
	global_load_dwordx4 v[12:15], v116, s[52:53]
	ds_write_b128 v107, v[92:95] offset:16
	s_lshl_b64 exec, s[22:23], 4
	v_mov_b32_e32 v87, s10
	s_mov_b64 exec, -1

; #define LAS __attribute__((address_space(3)))
; __device__ __forceinline__ void peer3_dots(const u4 (&R)[PG][2], const u4 (&xq)[2], int sx15, LAS int* redrow, int g) {
;     static_assert(PG == 4, "one 16-byte LDS store per row group");
;     int d[4];
; #pragma unroll
;     for (int k = 0; k < 4; ++k) { int a = 0, ah = 0;
; #pragma unroll
;         for (int q = 0; q < 4; ++q) { const unsigned w = R[k][0][q];
;             a = __builtin_amdgcn_sdot4((int)(w & 0x0f0f0f0fu), (int)xq[0][q], a, false); ah = __builtin_amdgcn_sdot4((int)(w & 0xf0f0f0f0u), (int)xq[1][q], ah, false); }
;         d[k] = 32 * a + 2 * ah - sx15; }
;     u4 w; w.x = (unsigned)d[0]; w.y = (unsigned)d[1]; w.z = (unsigned)d[2]; w.w = (unsigned)d[3];
;     *(LAS u4*)(redrow + 4 * g) = w;
; }
.Lq_std2:
	s_waitcnt vmcnt(8)
	v_and_b32_e32 v96, s38, v32
	v_and_b32_e32 v100, s39, v32
	v_and_b32_e32 v97, s38, v33
	v_and_b32_e32 v101, s39, v33
	v_dot4_i32_i8 v104, v96, v64, 0
	v_dot4_i32_i8 v105, v100, v68, 0
	v_and_b32_e32 v98, s38, v34
	v_and_b32_e32 v102, s39, v34
	v_dot4_i32_i8 v104, v97, v65, v104
	v_dot4_i32_i8 v105, v101, v69, v105
	v_and_b32_e32 v99, s38, v35
	v_and_b32_e32 v103, s39, v35
	v_dot4_i32_i8 v104, v98, v66, v104
	v_dot4_i32_i8 v105, v102, v70, v105
	v_dot4_i32_i8 v104, v99, v67, v104
	v_dot4_i32_i8 v105, v103, v71, v105
	v_and_b32_e32 v96, s38, v36
	v_and_b32_e32 v100, s39, v36
	v_and_b32_e32 v97, s38, v37
	v_and_b32_e32 v101, s39, v37
	v_lshl_add_u32 v106, v104, 4, v105
	v_lshl_add_u32 v92, v106, 1, v72
	v_dot4_i32_i8 v126, v96, v64, 0
	v_dot4_i32_i8 v127, v100, v68, 0
	v_and_b32_e32 v98, s38, v38
	v_and_b32_e32 v102, s39, v38
	v_dot4_i32_i8 v126, v97, v65, v126
	v_dot4_i32_i8 v127, v101, v69, v127
	v_and_b32_e32 v99, s38, v39
	v_and_b32_e32 v103, s39, v39
	v_dot4_i32_i8 v126, v98, v66, v126
	v_dot4_i32_i8 v127, v102, v70, v127
	v_dot4_i32_i8 v126, v99, v67, v126
	v_dot4_i32_i8 v127, v103, v71, v127
	v_and_b32_e32 v96, s38, v40
	v_and_b32_e32 v100, s39, v40
	v_and_b32_e32 v97, s38, v41
	v_and_b32_e32 v101, s39, v41
	v_lshl_add_u32 v106, v126, 4, v127
	v_lshl_add_u32 v93, v106, 1, v72
	v_dot4_i32_i8 v104, v96, v64, 0
	v_dot4_i32_i8 v105, v100, v68, 0
	v_and_b32_e32 v98, s38, v42
	v_and_b32_e32 v102, s39, v42
	v_dot4_i32_i8 v104, v97, v65, v104
	v_dot4_i32_i8 v105, v101, v69, v105
	v_and_b32_e32 v99, s38, v43
	v_and_b32_e32 v103, s39, v43
	v_dot4_i32_i8 v104, v98, v66, v104
	v_dot4_i32_i8 v105, v102, v70, v105
	v_dot4_i32_i8 v104, v99, v67, v104
	v_dot4_i32_i8 v105, v103, v71, v105
	v_and_b32_e32 v96, s38, v44
	v_and_b32_e32 v100, s39, v44
	v_and_b32_e32 v97, s38, v45
	v_and_b32_e32 v101, s39, v45
	v_lshl_add_u32 v106, v104, 4, v105
	v_lshl_add_u32 v94, v106, 1, v72
	v_dot4_i32_i8 v126, v96, v64, 0
	v_dot4_i32_i8 v127, v100, v68, 0
	v_and_b32_e32 v98, s38, v46
	v_and_b32_e32 v102, s39, v46
	v_dot4_i32_i8 v126, v97, v65, v126
	v_dot4_i32_i8 v127, v101, v69, v127
	v_and_b32_e32 v99, s38, v47
	v_and_b32_e32 v103, s39, v47
	v_dot4_i32_i8 v126, v98, v66, v126
	v_dot4_i32_i8 v127, v102, v70, v127
	v_dot4_i32_i8 v126, v99, v67, v126
	v_dot4_i32_i8 v127, v103, v71, v127
	s_nop 0
	v_readlane_b32 s36, v75, 20
	v_readlane_b32 s5, v75, 21
	v_readlane_b32 s6, v75, 22
	v_readlane_b32 s7, v75, 23
	v_lshl_add_u32 v106, v126, 4, v127
	v_lshl_add_u32 v95, v106, 1, v72
	v_add_u32_e32 v113, s36, v206
	v_add_u32_e32 v114, s5, v206
	v_add_u32_e32 v115, s6, v206
	v_add_u32_e32 v116, s7, v206
	global_load_dwordx4 v[16:19], v113, s[52:53]
	global_load_dwordx4 v[20:23], v114, s[52:53]
	global_load_dwordx4 v[24:27], v115, s[52:53]
	global_load_dwordx4 v[28:31], v116, s[52:53]
	ds_write_b128 v107, v[92:95] offset:32
	s_lshl_b64 exec, s[22:23], 8
	v_mov_b32_e32 v87, s10
	s_mov_b64 exec, -1

; #define LAS __attribute__((address_space(3)))
; __device__ __forceinline__ void peer3_dots(const u4 (&R)[PG][2], const u4 (&xq)[2], int sx15, LAS int* redrow, int g) {
;     static_assert(PG == 4, "one 16-byte LDS store per row group");
;     int d[4];
; #pragma unroll
;     for (int k = 0; k < 4; ++k) { int a = 0, ah = 0;
; #pragma unroll
;         for (int q = 0; q < 4; ++q) { const unsigned w = R[k][0][q];
;             a = __builtin_amdgcn_sdot4((int)(w & 0x0f0f0f0fu), (int)xq[0][q], a, false); ah = __builtin_amdgcn_sdot4((int)(w & 0xf0f0f0f0u), (int)xq[1][q], ah, false); }
;         d[k] = 32 * a + 2 * ah - sx15; }
;     u4 w; w.x = (unsigned)d[0]; w.y = (unsigned)d[1]; w.z = (unsigned)d[2]; w.w = (unsigned)d[3];
;     *(LAS u4*)(redrow + 4 * g) = w;
; }
.Lq_std3:
	s_waitcnt vmcnt(8)
	v_and_b32_e32 v96, s38, v48
	v_and_b32_e32 v100, s39, v48
	v_and_b32_e32 v97, s38, v49
	v_and_b32_e32 v101, s39, v49
	v_dot4_i32_i8 v104, v96, v64, 0
	v_dot4_i32_i8 v105, v100, v68, 0
	v_and_b32_e32 v98, s38, v50
	v_and_b32_e32 v102, s39, v50
	v_dot4_i32_i8 v104, v97, v65, v104
	v_dot4_i32_i8 v105, v101, v69, v105
	v_and_b32_e32 v99, s38, v51
	v_and_b32_e32 v103, s39, v51
	v_dot4_i32_i8 v104, v98, v66, v104
	v_dot4_i32_i8 v105, v102, v70, v105
	v_dot4_i32_i8 v104, v99, v67, v104
	v_dot4_i32_i8 v105, v103, v71, v105
	v_and_b32_e32 v96, s38, v52
	v_and_b32_e32 v100, s39, v52
	v_and_b32_e32 v97, s38, v53
	v_and_b32_e32 v101, s39, v53
	v_lshl_add_u32 v106, v104, 4, v105
	v_lshl_add_u32 v92, v106, 1, v72
	v_dot4_i32_i8 v126, v96, v64, 0
	v_dot4_i32_i8 v127, v100, v68, 0
	v_and_b32_e32 v98, s38, v54
	v_and_b32_e32 v102, s39, v54
	v_dot4_i32_i8 v126, v97, v65, v126
	v_dot4_i32_i8 v127, v101, v69, v127
	v_and_b32_e32 v99, s38, v55
	v_and_b32_e32 v103, s39, v55
	v_dot4_i32_i8 v126, v98, v66, v126
	v_dot4_i32_i8 v127, v102, v70, v127
	v_dot4_i32_i8 v126, v99, v67, v126
	v_dot4_i32_i8 v127, v103, v71, v127
	v_and_b32_e32 v96, s38, v56
	v_and_b32_e32 v100, s39, v56
	v_and_b32_e32 v97, s38, v57
	v_and_b32_e32 v101, s39, v57
	v_lshl_add_u32 v106, v126, 4, v127
	v_lshl_add_u32 v93, v106, 1, v72
	v_dot4_i32_i8 v104, v96, v64, 0
	v_dot4_i32_i8 v105, v100, v68, 0
	v_and_b32_e32 v98, s38, v58
	v_and_b32_e32 v102, s39, v58
	v_dot4_i32_i8 v104, v97, v65, v104
	v_dot4_i32_i8 v105, v101, v69, v105
	v_and_b32_e32 v99, s38, v59
	v_and_b32_e32 v103, s39, v59
	v_dot4_i32_i8 v104, v98, v66, v104
	v_dot4_i32_i8 v105, v102, v70, v105
	v_dot4_i32_i8 v104, v99, v67, v104
	v_dot4_i32_i8 v105, v103, v71, v105
	v_and_b32_e32 v96, s38, v60
	v_and_b32_e32 v100, s39, v60
	v_and_b32_e32 v97, s38, v61
	v_and_b32_e32 v101, s39, v61
	v_lshl_add_u32 v106, v104, 4, v105
	v_lshl_add_u32 v94, v106, 1, v72
	v_dot4_i32_i8 v126, v96, v64, 0
	v_dot4_i32_i8 v127, v100, v68, 0
	v_and_b32_e32 v98, s38, v62
	v_and_b32_e32 v102, s39, v62
	v_dot4_i32_i8 v126, v97, v65, v126
	v_dot4_i32_i8 v127, v101, v69, v127
	v_and_b32_e32 v99, s38, v63
	v_and_b32_e32 v103, s39, v63
	v_dot4_i32_i8 v126, v98, v66, v126
	v_dot4_i32_i8 v127, v102, v70, v127
	v_dot4_i32_i8 v126, v99, v67, v126
	v_dot4_i32_i8 v127, v103, v71, v127
	s_nop 0
	v_readlane_b32 s36, v75, 24
	v_readlane_b32 s5, v75, 25
	v_readlane_b32 s6, v75, 26
	v_readlane_b32 s7, v75, 27
	v_lshl_add_u32 v106, v126, 4, v127
	v_lshl_add_u32 v95, v106, 1, v72
	v_add_u32_e32 v113, s36, v206
	v_add_u32_e32 v114, s5, v206
	v_add_u32_e32 v115, s6, v206
	v_add_u32_e32 v116, s7, v206
	global_load_dwordx4 v[32:35], v113, s[52:53]
	global_load_dwordx4 v[36:39], v114, s[52:53]
	global_load_dwordx4 v[40:43], v115, s[52:53]
	global_load_dwordx4 v[44:47], v116, s[52:53]
	ds_write_b128 v107, v[92:95] offset:48
	s_lshl_b64 exec, s[22:23], 12
	v_mov_b32_e32 v87, s10
	s_mov_b64 exec, -1

; #define LAS __attribute__((address_space(3)))
; __device__ __forceinline__ void peer3_dots(const u4 (&R)[PG][2], const u4 (&xq)[2], int sx15, LAS int* redrow, int g) {
;     static_assert(PG == 4, "one 16-byte LDS store per row group");
;     int d[4];
; #pragma unroll
;     for (int k = 0; k < 4; ++k) { int a = 0, ah = 0;
; #pragma unroll
;         for (int q = 0; q < 4; ++q) { const unsigned w = R[k][0][q];
;             a = __builtin_amdgcn_sdot4((int)(w & 0x0f0f0f0fu), (int)xq[0][q], a, false); ah = __builtin_amdgcn_sdot4((int)(w & 0xf0f0f0f0u), (int)xq[1][q], ah, false); }
;         d[k] = 32 * a + 2 * ah - sx15; }
;     u4 w; w.x = (unsigned)d[0]; w.y = (unsigned)d[1]; w.z = (unsigned)d[2]; w.w = (unsigned)d[3];
;     *(LAS u4*)(redrow + 4 * g) = w;
; }
.Lq_std4:
	s_waitcnt vmcnt(8)
	v_and_b32_e32 v96, s38, v0
	v_and_b32_e32 v100, s39, v0
	v_and_b32_e32 v97, s38, v1
	v_and_b32_e32 v101, s39, v1
	v_dot4_i32_i8 v104, v96, v64, 0
	v_dot4_i32_i8 v105, v100, v68, 0
	v_and_b32_e32 v98, s38, v2
	v_and_b32_e32 v102, s39, v2
	v_dot4_i32_i8 v104, v97, v65, v104
	v_dot4_i32_i8 v105, v101, v69, v105
	v_and_b32_e32 v99, s38, v3
	v_and_b32_e32 v103, s39, v3
	v_dot4_i32_i8 v104, v98, v66, v104
	v_dot4_i32_i8 v105, v102, v70, v105
	v_dot4_i32_i8 v104, v99, v67, v104
	v_dot4_i32_i8 v105, v103, v71, v105
	v_and_b32_e32 v96, s38, v4
	v_and_b32_e32 v100, s39, v4
	v_and_b32_e32 v97, s38, v5
	v_and_b32_e32 v101, s39, v5
	v_lshl_add_u32 v106, v104, 4, v105
	v_lshl_add_u32 v92, v106, 1, v72
	v_dot4_i32_i8 v126, v96, v64, 0
	v_dot4_i32_i8 v127, v100, v68, 0
	v_and_b32_e32 v98, s38, v6
	v_and_b32_e32 v102, s39, v6
	v_dot4_i32_i8 v126, v97, v65, v126
	v_dot4_i32_i8 v127, v101, v69, v127
	v_and_b32_e32 v99, s38, v7
	v_and_b32_e32 v103, s39, v7
	v_dot4_i32_i8 v126, v98, v66, v126
	v_dot4_i32_i8 v127, v102, v70, v127
	v_dot4_i32_i8 v126, v99, v67, v126
	v_dot4_i32_i8 v127, v103, v71, v127
	v_and_b32_e32 v96, s38, v8
	v_and_b32_e32 v100, s39, v8
	v_and_b32_e32 v97, s38, v9
	v_and_b32_e32 v101, s39, v9
	v_lshl_add_u32 v106, v126, 4, v127
	v_lshl_add_u32 v93, v106, 1, v72
	v_dot4_i32_i8 v104, v96, v64, 0
	v_dot4_i32_i8 v105, v100, v68, 0
	v_and_b32_e32 v98, s38, v10
	v_and_b32_e32 v102, s39, v10
	v_dot4_i32_i8 v104, v97, v65, v104
	v_dot4_i32_i8 v105, v101, v69, v105
	v_and_b32_e32 v99, s38, v11
	v_and_b32_e32 v103, s39, v11
	v_dot4_i32_i8 v104, v98, v66, v104
	v_dot4_i32_i8 v105, v102, v70, v105
	v_dot4_i32_i8 v104, v99, v67, v104
	v_dot4_i32_i8 v105, v103, v71, v105
	v_and_b32_e32 v96, s38, v12
	v_and_b32_e32 v100, s39, v12
	v_and_b32_e32 v97, s38, v13
	v_and_b32_e32 v101, s39, v13
	v_lshl_add_u32 v106, v104, 4, v105
	v_lshl_add_u32 v94, v106, 1, v72
	v_dot4_i32_i8 v126, v96, v64, 0
	v_dot4_i32_i8 v127, v100, v68, 0
	v_and_b32_e32 v98, s38, v14
	v_and_b32_e32 v102, s39, v14
	v_dot4_i32_i8 v126, v97, v65, v126
	v_dot4_i32_i8 v127, v101, v69, v127
	v_and_b32_e32 v99, s38, v15
	v_and_b32_e32 v103, s39, v15
	v_dot4_i32_i8 v126, v98, v66, v126
	v_dot4_i32_i8 v127, v102, v70, v127
	v_dot4_i32_i8 v126, v99, v67, v126
	v_dot4_i32_i8 v127, v103, v71, v127
	s_nop 0
	v_readlane_b32 s36, v75, 28
	v_readlane_b32 s5, v75, 29
	v_readlane_b32 s6, v75, 30
	v_readlane_b32 s7, v75, 31
	v_lshl_add_u32 v106, v126, 4, v127
	v_lshl_add_u32 v95, v106, 1, v72
	v_add_u32_e32 v113, s36, v206
	v_add_u32_e32 v114, s5, v206
	v_add_u32_e32 v115, s6, v206
	v_add_u32_e32 v116, s7, v206
	global_load_dwordx4 v[48:51], v113, s[52:53]
	global_load_dwordx4 v[52:55], v114, s[52:53]
	global_load_dwordx4 v[56:59], v115, s[52:53]
	global_load_dwordx4 v[60:63], v116, s[52:53]
	ds_write_b128 v107, v[92:95] offset:64
	s_lshl_b64 exec, s[22:23], 16
	v_mov_b32_e32 v87, s10
	s_mov_b64 exec, -1

; #define LAS __attribute__((address_space(3)))
; #define PU_DO(R, gi) do { PU_SWITCH(R, gi) peer3_dots(R, xq, sx15, red + lane * 68, (gi)); xsv = (lane >= PG * (gi) && lane < PG * (gi) + PG) ? xs : xsv; } while (0)
; __device__ __forceinline__ void peer3_dots(const u4 (&R)[PG][2], const u4 (&xq)[2], int sx15, LAS int* redrow, int g) {
;     static_assert(PG == 4, "one 16-byte LDS store per row group");
;     int d[4];
; #pragma unroll
;     for (int k = 0; k < 4; ++k) { int a = 0, ah = 0;
; #pragma unroll
;         for (int q = 0; q < 4; ++q) { const unsigned w = R[k][0][q];
;             a = __builtin_amdgcn_sdot4((int)(w & 0x0f0f0f0fu), (int)xq[0][q], a, false); ah = __builtin_amdgcn_sdot4((int)(w & 0xf0f0f0f0u), (int)xq[1][q], ah, false); }
;         d[k] = 32 * a + 2 * ah - sx15; }
;     u4 w; w.x = (unsigned)d[0]; w.y = (unsigned)d[1]; w.z = (unsigned)d[2]; w.w = (unsigned)d[3];
;     *(LAS u4*)(redrow + 4 * g) = w;
; }
; __device__ __forceinline__ void phase_peer_bucket(const Params& P, unsigned char* ws, int l, LAS unsigned char* lds, int bid, int G, int lane, int wave) {
;     ...
;             bool pre = false; u4 A[PG][2], B[PG][2], C[PG][2], Dq[PG][2];
; #pragma unroll 1
;             for (int blk = 0; blk < total; blk += 64) { const int blen = (total - blk) < 64 ? (total - blk) : 64, ng = blen / PG;
;                 const int ev = evn; const float wv = wvn;
;                 if (blk + 64 + lane < total) { evn = __builtin_nontemporal_load(FE + blk + 64 + lane); wvn = __builtin_nontemporal_load(FW + blk + 64 + lane); }
;                 const float us = USC[ev], vs = VSC[ev];
;                 float xsv = 0.f;
;                 if (ng == 16) {
;                     const bool nextfull = blk + 128 <= total;
;                     if (!pre) { PU_ROWS(A, 0); PU_ROWS(B, 1); PU_ROWS(C, 2); }
; #pragma unroll 1
;                     for (int g = 0; g < 12; g += 4) {
;                         PU_ROWS(Dq, g + 3); PU_DO(A, g); PU_ROWS(A, g + 4); PU_DO(B, g + 1); PU_ROWS(B, g + 5); PU_DO(C, g + 2); PU_ROWS(C, g + 6); PU_DO(Dq, g + 3);
;                     }
;                     PU_ROWS(Dq, 15); PU_DO(A, 12); if (nextfull) PU_ROWS_N(A, 0); PU_DO(B, 13); if (nextfull) PU_ROWS_N(B, 1); PU_DO(C, 14); if (nextfull) PU_ROWS_N(C, 2); PU_DO(Dq, 15);
.Lq_std5:
	s_waitcnt vmcnt(8)
	v_and_b32_e32 v96, s38, v16
	v_and_b32_e32 v100, s39, v16
	v_and_b32_e32 v97, s38, v17
	v_and_b32_e32 v101, s39, v17
	v_dot4_i32_i8 v104, v96, v64, 0
	v_dot4_i32_i8 v105, v100, v68, 0
	v_and_b32_e32 v98, s38, v18
	v_and_b32_e32 v102, s39, v18
	v_dot4_i32_i8 v104, v97, v65, v104
	v_dot4_i32_i8 v105, v101, v69, v105
	v_and_b32_e32 v99, s38, v19
	v_and_b32_e32 v103, s39, v19
	v_dot4_i32_i8 v104, v98, v66, v104
	v_dot4_i32_i8 v105, v102, v70, v105
	v_dot4_i32_i8 v104, v99, v67, v104
	v_dot4_i32_i8 v105, v103, v71, v105
	v_and_b32_e32 v96, s38, v20
	v_and_b32_e32 v100, s39, v20
	v_and_b32_e32 v97, s38, v21
	v_and_b32_e32 v101, s39, v21
	v_lshl_add_u32 v106, v104, 4, v105
	v_lshl_add_u32 v92, v106, 1, v72
	v_dot4_i32_i8 v126, v96, v64, 0
	v_dot4_i32_i8 v127, v100, v68, 0
	v_and_b32_e32 v98, s38, v22
	v_and_b32_e32 v102, s39, v22
	v_dot4_i32_i8 v126, v97, v65, v126
	v_dot4_i32_i8 v127, v101, v69, v127
	v_and_b32_e32 v99, s38, v23
	v_and_b32_e32 v103, s39, v23
	v_dot4_i32_i8 v126, v98, v66, v126
	v_dot4_i32_i8 v127, v102, v70, v127
	v_dot4_i32_i8 v126, v99, v67, v126
	v_dot4_i32_i8 v127, v103, v71, v127
	v_and_b32_e32 v96, s38, v24
	v_and_b32_e32 v100, s39, v24
	v_and_b32_e32 v97, s38, v25
	v_and_b32_e32 v101, s39, v25
	v_lshl_add_u32 v106, v126, 4, v127
	v_lshl_add_u32 v93, v106, 1, v72
	v_dot4_i32_i8 v104, v96, v64, 0
	v_dot4_i32_i8 v105, v100, v68, 0
	v_and_b32_e32 v98, s38, v26
	v_and_b32_e32 v102, s39, v26
	v_dot4_i32_i8 v104, v97, v65, v104
	v_dot4_i32_i8 v105, v101, v69, v105
	v_and_b32_e32 v99, s38, v27
	v_and_b32_e32 v103, s39, v27
	v_dot4_i32_i8 v104, v98, v66, v104
	v_dot4_i32_i8 v105, v102, v70, v105
	v_dot4_i32_i8 v104, v99, v67, v104
	v_dot4_i32_i8 v105, v103, v71, v105
	v_and_b32_e32 v96, s38, v28
	v_and_b32_e32 v100, s39, v28
	v_and_b32_e32 v97, s38, v29
	v_and_b32_e32 v101, s39, v29
	v_lshl_add_u32 v106, v104, 4, v105
	v_lshl_add_u32 v94, v106, 1, v72
	v_dot4_i32_i8 v126, v96, v64, 0
	v_dot4_i32_i8 v127, v100, v68, 0
	v_and_b32_e32 v98, s38, v30
	v_and_b32_e32 v102, s39, v30
	v_dot4_i32_i8 v126, v97, v65, v126
	v_dot4_i32_i8 v127, v101, v69, v127
	v_and_b32_e32 v99, s38, v31
	v_and_b32_e32 v103, s39, v31
	v_dot4_i32_i8 v126, v98, v66, v126
	v_dot4_i32_i8 v127, v102, v70, v127
	v_dot4_i32_i8 v126, v99, v67, v126
	v_dot4_i32_i8 v127, v103, v71, v127
	s_nop 0
	v_readlane_b32 s36, v75, 32
	v_readlane_b32 s5, v75, 33
	v_readlane_b32 s6, v75, 34
	v_readlane_b32 s7, v75, 35
	v_lshl_add_u32 v106, v126, 4, v127
	v_lshl_add_u32 v95, v106, 1, v72
	v_add_u32_e32 v113, s36, v206
	v_add_u32_e32 v114, s5, v206
	v_add_u32_e32 v115, s6, v206
	v_add_u32_e32 v116, s7, v206
	global_load_dwordx4 v[0:3], v113, s[52:53]
	global_load_dwordx4 v[4:7], v114, s[52:53]
	global_load_dwordx4 v[8:11], v115, s[52:53]
	global_load_dwordx4 v[12:15], v116, s[52:53]
	ds_write_b128 v107, v[92:95] offset:80
	s_lshl_b64 exec, s[22:23], 20
	v_mov_b32_e32 v87, s10
	s_mov_b64 exec, -1

; #define LAS __attribute__((address_space(3)))
; #define PU_DO(R, gi) do { PU_SWITCH(R, gi) peer3_dots(R, xq, sx15, red + lane * 68, (gi)); xsv = (lane >= PG * (gi) && lane < PG * (gi) + PG) ? xs : xsv; } while (0)
; __device__ __forceinline__ void peer3_dots(const u4 (&R)[PG][2], const u4 (&xq)[2], int sx15, LAS int* redrow, int g) {
;     static_assert(PG == 4, "one 16-byte LDS store per row group");
;     int d[4];
; #pragma unroll
;     for (int k = 0; k < 4; ++k) { int a = 0, ah = 0;
; #pragma unroll
;         for (int q = 0; q < 4; ++q) { const unsigned w = R[k][0][q];
;             a = __builtin_amdgcn_sdot4((int)(w & 0x0f0f0f0fu), (int)xq[0][q], a, false); ah = __builtin_amdgcn_sdot4((int)(w & 0xf0f0f0f0u), (int)xq[1][q], ah, false); }
;         d[k] = 32 * a + 2 * ah - sx15; }
;     u4 w; w.x = (unsigned)d[0]; w.y = (unsigned)d[1]; w.z = (unsigned)d[2]; w.w = (unsigned)d[3];
;     *(LAS u4*)(redrow + 4 * g) = w;
; }
; __device__ __forceinline__ void phase_peer_bucket(const Params& P, unsigned char* ws, int l, LAS unsigned char* lds, int bid, int G, int lane, int wave) {
;     ...
;             bool pre = false; u4 A[PG][2], B[PG][2], C[PG][2], Dq[PG][2];
; #pragma unroll 1
;             for (int blk = 0; blk < total; blk += 64) { const int blen = (total - blk) < 64 ? (total - blk) : 64, ng = blen / PG;
;                 const int ev = evn; const float wv = wvn;
;                 if (blk + 64 + lane < total) { evn = __builtin_nontemporal_load(FE + blk + 64 + lane); wvn = __builtin_nontemporal_load(FW + blk + 64 + lane); }
;                 const float us = USC[ev], vs = VSC[ev];
;                 float xsv = 0.f;
;                 if (ng == 16) {
;                     const bool nextfull = blk + 128 <= total;
;                     if (!pre) { PU_ROWS(A, 0); PU_ROWS(B, 1); PU_ROWS(C, 2); }
; #pragma unroll 1
;                     for (int g = 0; g < 12; g += 4) {
;                         PU_ROWS(Dq, g + 3); PU_DO(A, g); PU_ROWS(A, g + 4); PU_DO(B, g + 1); PU_ROWS(B, g + 5); PU_DO(C, g + 2); PU_ROWS(C, g + 6); PU_DO(Dq, g + 3);
;                     }
;                     PU_ROWS(Dq, 15); PU_DO(A, 12); if (nextfull) PU_ROWS_N(A, 0); PU_DO(B, 13); if (nextfull) PU_ROWS_N(B, 1); PU_DO(C, 14); if (nextfull) PU_ROWS_N(C, 2); PU_DO(Dq, 15);
.Lq_std6:
	s_waitcnt vmcnt(8)
	v_and_b32_e32 v96, s38, v32
	v_and_b32_e32 v100, s39, v32
	v_and_b32_e32 v97, s38, v33
	v_and_b32_e32 v101, s39, v33
	v_dot4_i32_i8 v104, v96, v64, 0
	v_dot4_i32_i8 v105, v100, v68, 0
	v_and_b32_e32 v98, s38, v34
	v_and_b32_e32 v102, s39, v34
	v_dot4_i32_i8 v104, v97, v65, v104
	v_dot4_i32_i8 v105, v101, v69, v105
	v_and_b32_e32 v99, s38, v35
	v_and_b32_e32 v103, s39, v35
	v_dot4_i32_i8 v104, v98, v66, v104
	v_dot4_i32_i8 v105, v102, v70, v105
	v_dot4_i32_i8 v104, v99, v67, v104
	v_dot4_i32_i8 v105, v103, v71, v105
	v_and_b32_e32 v96, s38, v36
	v_and_b32_e32 v100, s39, v36
	v_and_b32_e32 v97, s38, v37
	v_and_b32_e32 v101, s39, v37
	v_lshl_add_u32 v106, v104, 4, v105
	v_lshl_add_u32 v92, v106, 1, v72
	v_dot4_i32_i8 v126, v96, v64, 0
	v_dot4_i32_i8 v127, v100, v68, 0
	v_and_b32_e32 v98, s38, v38
	v_and_b32_e32 v102, s39, v38
	v_dot4_i32_i8 v126, v97, v65, v126
	v_dot4_i32_i8 v127, v101, v69, v127
	v_and_b32_e32 v99, s38, v39
	v_and_b32_e32 v103, s39, v39
	v_dot4_i32_i8 v126, v98, v66, v126
	v_dot4_i32_i8 v127, v102, v70, v127
	v_dot4_i32_i8 v126, v99, v67, v126
	v_dot4_i32_i8 v127, v103, v71, v127
	v_and_b32_e32 v96, s38, v40
	v_and_b32_e32 v100, s39, v40
	v_and_b32_e32 v97, s38, v41
	v_and_b32_e32 v101, s39, v41
	v_lshl_add_u32 v106, v126, 4, v127
	v_lshl_add_u32 v93, v106, 1, v72
	v_dot4_i32_i8 v104, v96, v64, 0
	v_dot4_i32_i8 v105, v100, v68, 0
	v_and_b32_e32 v98, s38, v42
	v_and_b32_e32 v102, s39, v42
	v_dot4_i32_i8 v104, v97, v65, v104
	v_dot4_i32_i8 v105, v101, v69, v105
	v_and_b32_e32 v99, s38, v43
	v_and_b32_e32 v103, s39, v43
	v_dot4_i32_i8 v104, v98, v66, v104
	v_dot4_i32_i8 v105, v102, v70, v105
	v_dot4_i32_i8 v104, v99, v67, v104
	v_dot4_i32_i8 v105, v103, v71, v105
	v_and_b32_e32 v96, s38, v44
	v_and_b32_e32 v100, s39, v44
	v_and_b32_e32 v97, s38, v45
	v_and_b32_e32 v101, s39, v45
	v_lshl_add_u32 v106, v104, 4, v105
	v_lshl_add_u32 v94, v106, 1, v72
	v_dot4_i32_i8 v126, v96, v64, 0
	v_dot4_i32_i8 v127, v100, v68, 0
	v_and_b32_e32 v98, s38, v46
	v_and_b32_e32 v102, s39, v46
	v_dot4_i32_i8 v126, v97, v65, v126
	v_dot4_i32_i8 v127, v101, v69, v127
	v_and_b32_e32 v99, s38, v47
	v_and_b32_e32 v103, s39, v47
	v_dot4_i32_i8 v126, v98, v66, v126
	v_dot4_i32_i8 v127, v102, v70, v127
	v_dot4_i32_i8 v126, v99, v67, v126
	v_dot4_i32_i8 v127, v103, v71, v127
	s_nop 0
	v_readlane_b32 s36, v75, 36
	v_readlane_b32 s5, v75, 37
	v_readlane_b32 s6, v75, 38
	v_readlane_b32 s7, v75, 39
	v_lshl_add_u32 v106, v126, 4, v127
	v_lshl_add_u32 v95, v106, 1, v72
	v_add_u32_e32 v113, s36, v206
	v_add_u32_e32 v114, s5, v206
	v_add_u32_e32 v115, s6, v206
	v_add_u32_e32 v116, s7, v206
	global_load_dwordx4 v[16:19], v113, s[52:53]
	global_load_dwordx4 v[20:23], v114, s[52:53]
	global_load_dwordx4 v[24:27], v115, s[52:53]
	global_load_dwordx4 v[28:31], v116, s[52:53]
	ds_write_b128 v107, v[92:95] offset:96
	s_lshl_b64 exec, s[22:23], 24
	v_mov_b32_e32 v87, s10
	s_mov_b64 exec, -1

; #define LAS __attribute__((address_space(3)))
; #define PU_DO(R, gi) do { PU_SWITCH(R, gi) peer3_dots(R, xq, sx15, red + lane * 68, (gi)); xsv = (lane >= PG * (gi) && lane < PG * (gi) + PG) ? xs : xsv; } while (0)
; __device__ __forceinline__ void peer3_dots(const u4 (&R)[PG][2], const u4 (&xq)[2], int sx15, LAS int* redrow, int g) {
;     static_assert(PG == 4, "one 16-byte LDS store per row group");
;     int d[4];
; #pragma unroll
;     for (int k = 0; k < 4; ++k) { int a = 0, ah = 0;
; #pragma unroll
;         for (int q = 0; q < 4; ++q) { const unsigned w = R[k][0][q];
;             a = __builtin_amdgcn_sdot4((int)(w & 0x0f0f0f0fu), (int)xq[0][q], a, false); ah = __builtin_amdgcn_sdot4((int)(w & 0xf0f0f0f0u), (int)xq[1][q], ah, false); }
;         d[k] = 32 * a + 2 * ah - sx15; }
;     u4 w; w.x = (unsigned)d[0]; w.y = (unsigned)d[1]; w.z = (unsigned)d[2]; w.w = (unsigned)d[3];
;     *(LAS u4*)(redrow + 4 * g) = w;
; }
; __device__ __forceinline__ void phase_peer_bucket(const Params& P, unsigned char* ws, int l, LAS unsigned char* lds, int bid, int G, int lane, int wave) {
;     ...
;             bool pre = false; u4 A[PG][2], B[PG][2], C[PG][2], Dq[PG][2];
; #pragma unroll 1
;             for (int blk = 0; blk < total; blk += 64) { const int blen = (total - blk) < 64 ? (total - blk) : 64, ng = blen / PG;
;                 const int ev = evn; const float wv = wvn;
;                 if (blk + 64 + lane < total) { evn = __builtin_nontemporal_load(FE + blk + 64 + lane); wvn = __builtin_nontemporal_load(FW + blk + 64 + lane); }
;                 const float us = USC[ev], vs = VSC[ev];
;                 float xsv = 0.f;
;                 if (ng == 16) {
;                     const bool nextfull = blk + 128 <= total;
;                     if (!pre) { PU_ROWS(A, 0); PU_ROWS(B, 1); PU_ROWS(C, 2); }
; #pragma unroll 1
;                     for (int g = 0; g < 12; g += 4) {
;                         PU_ROWS(Dq, g + 3); PU_DO(A, g); PU_ROWS(A, g + 4); PU_DO(B, g + 1); PU_ROWS(B, g + 5); PU_DO(C, g + 2); PU_ROWS(C, g + 6); PU_DO(Dq, g + 3);
;                     }
;                     PU_ROWS(Dq, 15); PU_DO(A, 12); if (nextfull) PU_ROWS_N(A, 0); PU_DO(B, 13); if (nextfull) PU_ROWS_N(B, 1); PU_DO(C, 14); if (nextfull) PU_ROWS_N(C, 2); PU_DO(Dq, 15);
.Lq_std7:
	s_waitcnt vmcnt(8)
	v_and_b32_e32 v96, s38, v48
	v_and_b32_e32 v100, s39, v48
	v_and_b32_e32 v97, s38, v49
	v_and_b32_e32 v101, s39, v49
	v_dot4_i32_i8 v104, v96, v64, 0
	v_dot4_i32_i8 v105, v100, v68, 0
	v_and_b32_e32 v98, s38, v50
	v_and_b32_e32 v102, s39, v50
	v_dot4_i32_i8 v104, v97, v65, v104
	v_dot4_i32_i8 v105, v101, v69, v105
	v_and_b32_e32 v99, s38, v51
	v_and_b32_e32 v103, s39, v51
	v_dot4_i32_i8 v104, v98, v66, v104
	v_dot4_i32_i8 v105, v102, v70, v105
	v_dot4_i32_i8 v104, v99, v67, v104
	v_dot4_i32_i8 v105, v103, v71, v105
	v_and_b32_e32 v96, s38, v52
	v_and_b32_e32 v100, s39, v52
	v_and_b32_e32 v97, s38, v53
	v_and_b32_e32 v101, s39, v53
	v_lshl_add_u32 v106, v104, 4, v105
	v_lshl_add_u32 v92, v106, 1, v72
	v_dot4_i32_i8 v126, v96, v64, 0
	v_dot4_i32_i8 v127, v100, v68, 0
	v_and_b32_e32 v98, s38, v54
	v_and_b32_e32 v102, s39, v54
	v_dot4_i32_i8 v126, v97, v65, v126
	v_dot4_i32_i8 v127, v101, v69, v127
	v_and_b32_e32 v99, s38, v55
	v_and_b32_e32 v103, s39, v55
	v_dot4_i32_i8 v126, v98, v66, v126
	v_dot4_i32_i8 v127, v102, v70, v127
	v_dot4_i32_i8 v126, v99, v67, v126
	v_dot4_i32_i8 v127, v103, v71, v127
	v_and_b32_e32 v96, s38, v56
	v_and_b32_e32 v100, s39, v56
	v_and_b32_e32 v97, s38, v57
	v_and_b32_e32 v101, s39, v57
	v_lshl_add_u32 v106, v126, 4, v127
	v_lshl_add_u32 v93, v106, 1, v72
	v_dot4_i32_i8 v104, v96, v64, 0
	v_dot4_i32_i8 v105, v100, v68, 0
	v_and_b32_e32 v98, s38, v58
	v_and_b32_e32 v102, s39, v58
	v_dot4_i32_i8 v104, v97, v65, v104
	v_dot4_i32_i8 v105, v101, v69, v105
	v_and_b32_e32 v99, s38, v59
	v_and_b32_e32 v103, s39, v59
	v_dot4_i32_i8 v104, v98, v66, v104
	v_dot4_i32_i8 v105, v102, v70, v105
	v_dot4_i32_i8 v104, v99, v67, v104
	v_dot4_i32_i8 v105, v103, v71, v105
	v_and_b32_e32 v96, s38, v60
	v_and_b32_e32 v100, s39, v60
	v_and_b32_e32 v97, s38, v61
	v_and_b32_e32 v101, s39, v61
	v_lshl_add_u32 v106, v104, 4, v105
	v_lshl_add_u32 v94, v106, 1, v72
	v_dot4_i32_i8 v126, v96, v64, 0
	v_dot4_i32_i8 v127, v100, v68, 0
	v_and_b32_e32 v98, s38, v62
	v_and_b32_e32 v102, s39, v62
	v_dot4_i32_i8 v126, v97, v65, v126
	v_dot4_i32_i8 v127, v101, v69, v127
	v_and_b32_e32 v99, s38, v63
	v_and_b32_e32 v103, s39, v63
	v_dot4_i32_i8 v126, v98, v66, v126
	v_dot4_i32_i8 v127, v102, v70, v127
	v_dot4_i32_i8 v126, v99, v67, v126
	v_dot4_i32_i8 v127, v103, v71, v127
	s_nop 0
	v_readlane_b32 s36, v75, 40
	v_readlane_b32 s5, v75, 41
	v_readlane_b32 s6, v75, 42
	v_readlane_b32 s7, v75, 43
	v_lshl_add_u32 v106, v126, 4, v127
	v_lshl_add_u32 v95, v106, 1, v72
	v_add_u32_e32 v113, s36, v206
	v_add_u32_e32 v114, s5, v206
	v_add_u32_e32 v115, s6, v206
	v_add_u32_e32 v116, s7, v206
	global_load_dwordx4 v[32:35], v113, s[52:53]
	global_load_dwordx4 v[36:39], v114, s[52:53]
	global_load_dwordx4 v[40:43], v115, s[52:53]
	global_load_dwordx4 v[44:47], v116, s[52:53]
	ds_write_b128 v107, v[92:95] offset:112
	s_lshl_b64 exec, s[22:23], 28
	v_mov_b32_e32 v87, s10
	s_mov_b64 exec, -1

; #define LAS __attribute__((address_space(3)))
; #define PU_DO(R, gi) do { PU_SWITCH(R, gi) peer3_dots(R, xq, sx15, red + lane * 68, (gi)); xsv = (lane >= PG * (gi) && lane < PG * (gi) + PG) ? xs : xsv; } while (0)
; __device__ __forceinline__ void peer3_dots(const u4 (&R)[PG][2], const u4 (&xq)[2], int sx15, LAS int* redrow, int g) {
;     static_assert(PG == 4, "one 16-byte LDS store per row group");
;     int d[4];
; #pragma unroll
;     for (int k = 0; k < 4; ++k) { int a = 0, ah = 0;
; #pragma unroll
;         for (int q = 0; q < 4; ++q) { const unsigned w = R[k][0][q];
;             a = __builtin_amdgcn_sdot4((int)(w & 0x0f0f0f0fu), (int)xq[0][q], a, false); ah = __builtin_amdgcn_sdot4((int)(w & 0xf0f0f0f0u), (int)xq[1][q], ah, false); }
;         d[k] = 32 * a + 2 * ah - sx15; }
;     u4 w; w.x = (unsigned)d[0]; w.y = (unsigned)d[1]; w.z = (unsigned)d[2]; w.w = (unsigned)d[3];
;     *(LAS u4*)(redrow + 4 * g) = w;
; }
; __device__ __forceinline__ void phase_peer_bucket(const Params& P, unsigned char* ws, int l, LAS unsigned char* lds, int bid, int G, int lane, int wave) {
;     ...
;             bool pre = false; u4 A[PG][2], B[PG][2], C[PG][2], Dq[PG][2];
; #pragma unroll 1
;             for (int blk = 0; blk < total; blk += 64) { const int blen = (total - blk) < 64 ? (total - blk) : 64, ng = blen / PG;
;                 const int ev = evn; const float wv = wvn;
;                 if (blk + 64 + lane < total) { evn = __builtin_nontemporal_load(FE + blk + 64 + lane); wvn = __builtin_nontemporal_load(FW + blk + 64 + lane); }
;                 const float us = USC[ev], vs = VSC[ev];
;                 float xsv = 0.f;
;                 if (ng == 16) {
;                     const bool nextfull = blk + 128 <= total;
;                     if (!pre) { PU_ROWS(A, 0); PU_ROWS(B, 1); PU_ROWS(C, 2); }
; #pragma unroll 1
;                     for (int g = 0; g < 12; g += 4) {
;                         PU_ROWS(Dq, g + 3); PU_DO(A, g); PU_ROWS(A, g + 4); PU_DO(B, g + 1); PU_ROWS(B, g + 5); PU_DO(C, g + 2); PU_ROWS(C, g + 6); PU_DO(Dq, g + 3);
;                     }
;                     PU_ROWS(Dq, 15); PU_DO(A, 12); if (nextfull) PU_ROWS_N(A, 0); PU_DO(B, 13); if (nextfull) PU_ROWS_N(B, 1); PU_DO(C, 14); if (nextfull) PU_ROWS_N(C, 2); PU_DO(Dq, 15);
.Lq_std8:
	s_waitcnt vmcnt(8)
	v_and_b32_e32 v96, s38, v0
	v_and_b32_e32 v100, s39, v0
	v_and_b32_e32 v97, s38, v1
	v_and_b32_e32 v101, s39, v1
	v_dot4_i32_i8 v104, v96, v64, 0
	v_dot4_i32_i8 v105, v100, v68, 0
	v_and_b32_e32 v98, s38, v2
	v_and_b32_e32 v102, s39, v2
	v_dot4_i32_i8 v104, v97, v65, v104
	v_dot4_i32_i8 v105, v101, v69, v105
	v_and_b32_e32 v99, s38, v3
	v_and_b32_e32 v103, s39, v3
	v_dot4_i32_i8 v104, v98, v66, v104
	v_dot4_i32_i8 v105, v102, v70, v105
	v_dot4_i32_i8 v104, v99, v67, v104
	v_dot4_i32_i8 v105, v103, v71, v105
	v_and_b32_e32 v96, s38, v4
	v_and_b32_e32 v100, s39, v4
	v_and_b32_e32 v97, s38, v5
	v_and_b32_e32 v101, s39, v5
	v_lshl_add_u32 v106, v104, 4, v105
	v_lshl_add_u32 v92, v106, 1, v72
	v_dot4_i32_i8 v126, v96, v64, 0
	v_dot4_i32_i8 v127, v100, v68, 0
	v_and_b32_e32 v98, s38, v6
	v_and_b32_e32 v102, s39, v6
	v_dot4_i32_i8 v126, v97, v65, v126
	v_dot4_i32_i8 v127, v101, v69, v127
	v_and_b32_e32 v99, s38, v7
	v_and_b32_e32 v103, s39, v7
	v_dot4_i32_i8 v126, v98, v66, v126
	v_dot4_i32_i8 v127, v102, v70, v127
	v_dot4_i32_i8 v126, v99, v67, v126
	v_dot4_i32_i8 v127, v103, v71, v127
	v_and_b32_e32 v96, s38, v8
	v_and_b32_e32 v100, s39, v8
	v_and_b32_e32 v97, s38, v9
	v_and_b32_e32 v101, s39, v9
	v_lshl_add_u32 v106, v126, 4, v127
	v_lshl_add_u32 v93, v106, 1, v72
	v_dot4_i32_i8 v104, v96, v64, 0
	v_dot4_i32_i8 v105, v100, v68, 0
	v_and_b32_e32 v98, s38, v10
	v_and_b32_e32 v102, s39, v10
	v_dot4_i32_i8 v104, v97, v65, v104
	v_dot4_i32_i8 v105, v101, v69, v105
	v_and_b32_e32 v99, s38, v11
	v_and_b32_e32 v103, s39, v11
	v_dot4_i32_i8 v104, v98, v66, v104
	v_dot4_i32_i8 v105, v102, v70, v105
	v_dot4_i32_i8 v104, v99, v67, v104
	v_dot4_i32_i8 v105, v103, v71, v105
	v_and_b32_e32 v96, s38, v12
	v_and_b32_e32 v100, s39, v12
	v_and_b32_e32 v97, s38, v13
	v_and_b32_e32 v101, s39, v13
	v_lshl_add_u32 v106, v104, 4, v105
	v_lshl_add_u32 v94, v106, 1, v72
	v_dot4_i32_i8 v126, v96, v64, 0
	v_dot4_i32_i8 v127, v100, v68, 0
	v_and_b32_e32 v98, s38, v14
	v_and_b32_e32 v102, s39, v14
	v_dot4_i32_i8 v126, v97, v65, v126
	v_dot4_i32_i8 v127, v101, v69, v127
	v_and_b32_e32 v99, s38, v15
	v_and_b32_e32 v103, s39, v15
	v_dot4_i32_i8 v126, v98, v66, v126
	v_dot4_i32_i8 v127, v102, v70, v127
	v_dot4_i32_i8 v126, v99, v67, v126
	v_dot4_i32_i8 v127, v103, v71, v127
	s_nop 0
	v_readlane_b32 s36, v75, 44
	v_readlane_b32 s5, v75, 45
	v_readlane_b32 s6, v75, 46
	v_readlane_b32 s7, v75, 47
	v_lshl_add_u32 v106, v126, 4, v127
	v_lshl_add_u32 v95, v106, 1, v72
	v_add_u32_e32 v113, s36, v206
	v_add_u32_e32 v114, s5, v206
	v_add_u32_e32 v115, s6, v206
	v_add_u32_e32 v116, s7, v206
	global_load_dwordx4 v[48:51], v113, s[52:53]
	global_load_dwordx4 v[52:55], v114, s[52:53]
	global_load_dwordx4 v[56:59], v115, s[52:53]
	global_load_dwordx4 v[60:63], v116, s[52:53]
	ds_write_b128 v107, v[92:95] offset:128
	s_lshl_b64 exec, s[22:23], 32
	v_mov_b32_e32 v87, s10
	s_mov_b64 exec, -1

; #define LAS __attribute__((address_space(3)))
; #define PU_DO(R, gi) do { PU_SWITCH(R, gi) peer3_dots(R, xq, sx15, red + lane * 68, (gi)); xsv = (lane >= PG * (gi) && lane < PG * (gi) + PG) ? xs : xsv; } while (0)
; __device__ __forceinline__ void peer3_dots(const u4 (&R)[PG][2], const u4 (&xq)[2], int sx15, LAS int* redrow, int g) {
;     static_assert(PG == 4, "one 16-byte LDS store per row group");
;     int d[4];
; #pragma unroll
;     for (int k = 0; k < 4; ++k) { int a = 0, ah = 0;
; #pragma unroll
;         for (int q = 0; q < 4; ++q) { const unsigned w = R[k][0][q];
;             a = __builtin_amdgcn_sdot4((int)(w & 0x0f0f0f0fu), (int)xq[0][q], a, false); ah = __builtin_amdgcn_sdot4((int)(w & 0xf0f0f0f0u), (int)xq[1][q], ah, false); }
;         d[k] = 32 * a + 2 * ah - sx15; }
;     u4 w; w.x = (unsigned)d[0]; w.y = (unsigned)d[1]; w.z = (unsigned)d[2]; w.w = (unsigned)d[3];
;     *(LAS u4*)(redrow + 4 * g) = w;
; }
; __device__ __forceinline__ void phase_peer_bucket(const Params& P, unsigned char* ws, int l, LAS unsigned char* lds, int bid, int G, int lane, int wave) {
;     ...
;             bool pre = false; u4 A[PG][2], B[PG][2], C[PG][2], Dq[PG][2];
; #pragma unroll 1
;             for (int blk = 0; blk < total; blk += 64) { const int blen = (total - blk) < 64 ? (total - blk) : 64, ng = blen / PG;
;                 const int ev = evn; const float wv = wvn;
;                 if (blk + 64 + lane < total) { evn = __builtin_nontemporal_load(FE + blk + 64 + lane); wvn = __builtin_nontemporal_load(FW + blk + 64 + lane); }
;                 const float us = USC[ev], vs = VSC[ev];
;                 float xsv = 0.f;
;                 if (ng == 16) {
;                     const bool nextfull = blk + 128 <= total;
;                     if (!pre) { PU_ROWS(A, 0); PU_ROWS(B, 1); PU_ROWS(C, 2); }
; #pragma unroll 1
;                     for (int g = 0; g < 12; g += 4) {
;                         PU_ROWS(Dq, g + 3); PU_DO(A, g); PU_ROWS(A, g + 4); PU_DO(B, g + 1); PU_ROWS(B, g + 5); PU_DO(C, g + 2); PU_ROWS(C, g + 6); PU_DO(Dq, g + 3);
;                     }
;                     PU_ROWS(Dq, 15); PU_DO(A, 12); if (nextfull) PU_ROWS_N(A, 0); PU_DO(B, 13); if (nextfull) PU_ROWS_N(B, 1); PU_DO(C, 14); if (nextfull) PU_ROWS_N(C, 2); PU_DO(Dq, 15);
.Lq_std9:
	s_waitcnt vmcnt(8)
	v_and_b32_e32 v96, s38, v16
	v_and_b32_e32 v100, s39, v16
	v_and_b32_e32 v97, s38, v17
	v_and_b32_e32 v101, s39, v17
	v_dot4_i32_i8 v104, v96, v64, 0
	v_dot4_i32_i8 v105, v100, v68, 0
	v_and_b32_e32 v98, s38, v18
	v_and_b32_e32 v102, s39, v18
	v_dot4_i32_i8 v104, v97, v65, v104
	v_dot4_i32_i8 v105, v101, v69, v105
	v_and_b32_e32 v99, s38, v19
	v_and_b32_e32 v103, s39, v19
	v_dot4_i32_i8 v104, v98, v66, v104
	v_dot4_i32_i8 v105, v102, v70, v105
	v_dot4_i32_i8 v104, v99, v67, v104
	v_dot4_i32_i8 v105, v103, v71, v105
	v_and_b32_e32 v96, s38, v20
	v_and_b32_e32 v100, s39, v20
	v_and_b32_e32 v97, s38, v21
	v_and_b32_e32 v101, s39, v21
	v_lshl_add_u32 v106, v104, 4, v105
	v_lshl_add_u32 v92, v106, 1, v72
	v_dot4_i32_i8 v126, v96, v64, 0
	v_dot4_i32_i8 v127, v100, v68, 0
	v_and_b32_e32 v98, s38, v22
	v_and_b32_e32 v102, s39, v22
	v_dot4_i32_i8 v126, v97, v65, v126
	v_dot4_i32_i8 v127, v101, v69, v127
	v_and_b32_e32 v99, s38, v23
	v_and_b32_e32 v103, s39, v23
	v_dot4_i32_i8 v126, v98, v66, v126
	v_dot4_i32_i8 v127, v102, v70, v127
	v_dot4_i32_i8 v126, v99, v67, v126
	v_dot4_i32_i8 v127, v103, v71, v127
	v_and_b32_e32 v96, s38, v24
	v_and_b32_e32 v100, s39, v24
	v_and_b32_e32 v97, s38, v25
	v_and_b32_e32 v101, s39, v25
	v_lshl_add_u32 v106, v126, 4, v127
	v_lshl_add_u32 v93, v106, 1, v72
	v_dot4_i32_i8 v104, v96, v64, 0
	v_dot4_i32_i8 v105, v100, v68, 0
	v_and_b32_e32 v98, s38, v26
	v_and_b32_e32 v102, s39, v26
	v_dot4_i32_i8 v104, v97, v65, v104
	v_dot4_i32_i8 v105, v101, v69, v105
	v_and_b32_e32 v99, s38, v27
	v_and_b32_e32 v103, s39, v27
	v_dot4_i32_i8 v104, v98, v66, v104
	v_dot4_i32_i8 v105, v102, v70, v105
	v_dot4_i32_i8 v104, v99, v67, v104
	v_dot4_i32_i8 v105, v103, v71, v105
	v_and_b32_e32 v96, s38, v28
	v_and_b32_e32 v100, s39, v28
	v_and_b32_e32 v97, s38, v29
	v_and_b32_e32 v101, s39, v29
	v_lshl_add_u32 v106, v104, 4, v105
	v_lshl_add_u32 v94, v106, 1, v72
	v_dot4_i32_i8 v126, v96, v64, 0
	v_dot4_i32_i8 v127, v100, v68, 0
	v_and_b32_e32 v98, s38, v30
	v_and_b32_e32 v102, s39, v30
	v_dot4_i32_i8 v126, v97, v65, v126
	v_dot4_i32_i8 v127, v101, v69, v127
	v_and_b32_e32 v99, s38, v31
	v_and_b32_e32 v103, s39, v31
	v_dot4_i32_i8 v126, v98, v66, v126
	v_dot4_i32_i8 v127, v102, v70, v127
	v_dot4_i32_i8 v126, v99, v67, v126
	v_dot4_i32_i8 v127, v103, v71, v127
	s_nop 0
	v_readlane_b32 s36, v75, 48
	v_readlane_b32 s5, v75, 49
	v_readlane_b32 s6, v75, 50
	v_readlane_b32 s7, v75, 51
	v_lshl_add_u32 v106, v126, 4, v127
	v_lshl_add_u32 v95, v106, 1, v72
	v_add_u32_e32 v113, s36, v206
	v_add_u32_e32 v114, s5, v206
	v_add_u32_e32 v115, s6, v206
	v_add_u32_e32 v116, s7, v206
	global_load_dwordx4 v[0:3], v113, s[52:53]
	global_load_dwordx4 v[4:7], v114, s[52:53]
	global_load_dwordx4 v[8:11], v115, s[52:53]
	global_load_dwordx4 v[12:15], v116, s[52:53]
	ds_write_b128 v107, v[92:95] offset:144
	s_lshl_b64 exec, s[22:23], 36
	v_mov_b32_e32 v87, s10
	s_mov_b64 exec, -1

; #define LAS __attribute__((address_space(3)))
; #define PU_DO(R, gi) do { PU_SWITCH(R, gi) peer3_dots(R, xq, sx15, red + lane * 68, (gi)); xsv = (lane >= PG * (gi) && lane < PG * (gi) + PG) ? xs : xsv; } while (0)
; __device__ __forceinline__ void peer3_dots(const u4 (&R)[PG][2], const u4 (&xq)[2], int sx15, LAS int* redrow, int g) {
;     static_assert(PG == 4, "one 16-byte LDS store per row group");
;     int d[4];
; #pragma unroll
;     for (int k = 0; k < 4; ++k) { int a = 0, ah = 0;
; #pragma unroll
;         for (int q = 0; q < 4; ++q) { const unsigned w = R[k][0][q];
;             a = __builtin_amdgcn_sdot4((int)(w & 0x0f0f0f0fu), (int)xq[0][q], a, false); ah = __builtin_amdgcn_sdot4((int)(w & 0xf0f0f0f0u), (int)xq[1][q], ah, false); }
;         d[k] = 32 * a + 2 * ah - sx15; }
;     u4 w; w.x = (unsigned)d[0]; w.y = (unsigned)d[1]; w.z = (unsigned)d[2]; w.w = (unsigned)d[3];
;     *(LAS u4*)(redrow + 4 * g) = w;
; }
; __device__ __forceinline__ void phase_peer_bucket(const Params& P, unsigned char* ws, int l, LAS unsigned char* lds, int bid, int G, int lane, int wave) {
;     ...
;             bool pre = false; u4 A[PG][2], B[PG][2], C[PG][2], Dq[PG][2];
; #pragma unroll 1
;             for (int blk = 0; blk < total; blk += 64) { const int blen = (total - blk) < 64 ? (total - blk) : 64, ng = blen / PG;
;                 const int ev = evn; const float wv = wvn;
;                 if (blk + 64 + lane < total) { evn = __builtin_nontemporal_load(FE + blk + 64 + lane); wvn = __builtin_nontemporal_load(FW + blk + 64 + lane); }
;                 const float us = USC[ev], vs = VSC[ev];
;                 float xsv = 0.f;
;                 if (ng == 16) {
;                     const bool nextfull = blk + 128 <= total;
;                     if (!pre) { PU_ROWS(A, 0); PU_ROWS(B, 1); PU_ROWS(C, 2); }
; #pragma unroll 1
;                     for (int g = 0; g < 12; g += 4) {
;                         PU_ROWS(Dq, g + 3); PU_DO(A, g); PU_ROWS(A, g + 4); PU_DO(B, g + 1); PU_ROWS(B, g + 5); PU_DO(C, g + 2); PU_ROWS(C, g + 6); PU_DO(Dq, g + 3);
;                     }
;                     PU_ROWS(Dq, 15); PU_DO(A, 12); if (nextfull) PU_ROWS_N(A, 0); PU_DO(B, 13); if (nextfull) PU_ROWS_N(B, 1); PU_DO(C, 14); if (nextfull) PU_ROWS_N(C, 2); PU_DO(Dq, 15);
.Lq_std10:
	s_waitcnt vmcnt(8)
	v_and_b32_e32 v96, s38, v32
	v_and_b32_e32 v100, s39, v32
	v_and_b32_e32 v97, s38, v33
	v_and_b32_e32 v101, s39, v33
	v_dot4_i32_i8 v104, v96, v64, 0
	v_dot4_i32_i8 v105, v100, v68, 0
	v_and_b32_e32 v98, s38, v34
	v_and_b32_e32 v102, s39, v34
	v_dot4_i32_i8 v104, v97, v65, v104
	v_dot4_i32_i8 v105, v101, v69, v105
	v_and_b32_e32 v99, s38, v35
	v_and_b32_e32 v103, s39, v35
	v_dot4_i32_i8 v104, v98, v66, v104
	v_dot4_i32_i8 v105, v102, v70, v105
	v_dot4_i32_i8 v104, v99, v67, v104
	v_dot4_i32_i8 v105, v103, v71, v105
	v_and_b32_e32 v96, s38, v36
	v_and_b32_e32 v100, s39, v36
	v_and_b32_e32 v97, s38, v37
	v_and_b32_e32 v101, s39, v37
	v_lshl_add_u32 v106, v104, 4, v105
	v_lshl_add_u32 v92, v106, 1, v72
	v_dot4_i32_i8 v126, v96, v64, 0
	v_dot4_i32_i8 v127, v100, v68, 0
	v_and_b32_e32 v98, s38, v38
	v_and_b32_e32 v102, s39, v38
	v_dot4_i32_i8 v126, v97, v65, v126
	v_dot4_i32_i8 v127, v101, v69, v127
	v_and_b32_e32 v99, s38, v39
	v_and_b32_e32 v103, s39, v39
	v_dot4_i32_i8 v126, v98, v66, v126
	v_dot4_i32_i8 v127, v102, v70, v127
	v_dot4_i32_i8 v126, v99, v67, v126
	v_dot4_i32_i8 v127, v103, v71, v127
	v_and_b32_e32 v96, s38, v40
	v_and_b32_e32 v100, s39, v40
	v_and_b32_e32 v97, s38, v41
	v_and_b32_e32 v101, s39, v41
	v_lshl_add_u32 v106, v126, 4, v127
	v_lshl_add_u32 v93, v106, 1, v72
	v_dot4_i32_i8 v104, v96, v64, 0
	v_dot4_i32_i8 v105, v100, v68, 0
	v_and_b32_e32 v98, s38, v42
	v_and_b32_e32 v102, s39, v42
	v_dot4_i32_i8 v104, v97, v65, v104
	v_dot4_i32_i8 v105, v101, v69, v105
	v_and_b32_e32 v99, s38, v43
	v_and_b32_e32 v103, s39, v43
	v_dot4_i32_i8 v104, v98, v66, v104
	v_dot4_i32_i8 v105, v102, v70, v105
	v_dot4_i32_i8 v104, v99, v67, v104
	v_dot4_i32_i8 v105, v103, v71, v105
	v_and_b32_e32 v96, s38, v44
	v_and_b32_e32 v100, s39, v44
	v_and_b32_e32 v97, s38, v45
	v_and_b32_e32 v101, s39, v45
	v_lshl_add_u32 v106, v104, 4, v105
	v_lshl_add_u32 v94, v106, 1, v72
	v_dot4_i32_i8 v126, v96, v64, 0
	v_dot4_i32_i8 v127, v100, v68, 0
	v_and_b32_e32 v98, s38, v46
	v_and_b32_e32 v102, s39, v46
	v_dot4_i32_i8 v126, v97, v65, v126
	v_dot4_i32_i8 v127, v101, v69, v127
	v_and_b32_e32 v99, s38, v47
	v_and_b32_e32 v103, s39, v47
	v_dot4_i32_i8 v126, v98, v66, v126
	v_dot4_i32_i8 v127, v102, v70, v127
	v_dot4_i32_i8 v126, v99, v67, v126
	v_dot4_i32_i8 v127, v103, v71, v127
	s_nop 0
	v_readlane_b32 s36, v75, 52
	v_readlane_b32 s5, v75, 53
	v_readlane_b32 s6, v75, 54
	v_readlane_b32 s7, v75, 55
	v_lshl_add_u32 v106, v126, 4, v127
	v_lshl_add_u32 v95, v106, 1, v72
	v_add_u32_e32 v113, s36, v206
	v_add_u32_e32 v114, s5, v206
	v_add_u32_e32 v115, s6, v206
	v_add_u32_e32 v116, s7, v206
	global_load_dwordx4 v[16:19], v113, s[52:53]
	global_load_dwordx4 v[20:23], v114, s[52:53]
	global_load_dwordx4 v[24:27], v115, s[52:53]
	global_load_dwordx4 v[28:31], v116, s[52:53]
	ds_write_b128 v107, v[92:95] offset:160
	s_lshl_b64 exec, s[22:23], 40
	v_mov_b32_e32 v87, s10
	s_mov_b64 exec, -1

; #define LAS __attribute__((address_space(3)))
; #define PU_DO(R, gi) do { PU_SWITCH(R, gi) peer3_dots(R, xq, sx15, red + lane * 68, (gi)); xsv = (lane >= PG * (gi) && lane < PG * (gi) + PG) ? xs : xsv; } while (0)
; __device__ __forceinline__ void peer3_dots(const u4 (&R)[PG][2], const u4 (&xq)[2], int sx15, LAS int* redrow, int g) {
;     static_assert(PG == 4, "one 16-byte LDS store per row group");
;     int d[4];
; #pragma unroll
;     for (int k = 0; k < 4; ++k) { int a = 0, ah = 0;
; #pragma unroll
;         for (int q = 0; q < 4; ++q) { const unsigned w = R[k][0][q];
;             a = __builtin_amdgcn_sdot4((int)(w & 0x0f0f0f0fu), (int)xq[0][q], a, false); ah = __builtin_amdgcn_sdot4((int)(w & 0xf0f0f0f0u), (int)xq[1][q], ah, false); }
;         d[k] = 32 * a + 2 * ah - sx15; }
;     u4 w; w.x = (unsigned)d[0]; w.y = (unsigned)d[1]; w.z = (unsigned)d[2]; w.w = (unsigned)d[3];
;     *(LAS u4*)(redrow + 4 * g) = w;
; }
; __device__ __forceinline__ void phase_peer_bucket(const Params& P, unsigned char* ws, int l, LAS unsigned char* lds, int bid, int G, int lane, int wave) {
;     ...
;             bool pre = false; u4 A[PG][2], B[PG][2], C[PG][2], Dq[PG][2];
; #pragma unroll 1
;             for (int blk = 0; blk < total; blk += 64) { const int blen = (total - blk) < 64 ? (total - blk) : 64, ng = blen / PG;
;                 const int ev = evn; const float wv = wvn;
;                 if (blk + 64 + lane < total) { evn = __builtin_nontemporal_load(FE + blk + 64 + lane); wvn = __builtin_nontemporal_load(FW + blk + 64 + lane); }
;                 const float us = USC[ev], vs = VSC[ev];
;                 float xsv = 0.f;
;                 if (ng == 16) {
;                     const bool nextfull = blk + 128 <= total;
;                     if (!pre) { PU_ROWS(A, 0); PU_ROWS(B, 1); PU_ROWS(C, 2); }
; #pragma unroll 1
;                     for (int g = 0; g < 12; g += 4) {
;                         PU_ROWS(Dq, g + 3); PU_DO(A, g); PU_ROWS(A, g + 4); PU_DO(B, g + 1); PU_ROWS(B, g + 5); PU_DO(C, g + 2); PU_ROWS(C, g + 6); PU_DO(Dq, g + 3);
;                     }
;                     PU_ROWS(Dq, 15); PU_DO(A, 12); if (nextfull) PU_ROWS_N(A, 0); PU_DO(B, 13); if (nextfull) PU_ROWS_N(B, 1); PU_DO(C, 14); if (nextfull) PU_ROWS_N(C, 2); PU_DO(Dq, 15);
.Lq_std11:
	s_waitcnt vmcnt(8)
	v_and_b32_e32 v96, s38, v48
	v_and_b32_e32 v100, s39, v48
	v_and_b32_e32 v97, s38, v49
	v_and_b32_e32 v101, s39, v49
	v_dot4_i32_i8 v104, v96, v64, 0
	v_dot4_i32_i8 v105, v100, v68, 0
	v_and_b32_e32 v98, s38, v50
	v_and_b32_e32 v102, s39, v50
	v_dot4_i32_i8 v104, v97, v65, v104
	v_dot4_i32_i8 v105, v101, v69, v105
	v_and_b32_e32 v99, s38, v51
	v_and_b32_e32 v103, s39, v51
	v_dot4_i32_i8 v104, v98, v66, v104
	v_dot4_i32_i8 v105, v102, v70, v105
	v_dot4_i32_i8 v104, v99, v67, v104
	v_dot4_i32_i8 v105, v103, v71, v105
	v_and_b32_e32 v96, s38, v52
	v_and_b32_e32 v100, s39, v52
	v_and_b32_e32 v97, s38, v53
	v_and_b32_e32 v101, s39, v53
	v_lshl_add_u32 v106, v104, 4, v105
	v_lshl_add_u32 v92, v106, 1, v72
	v_dot4_i32_i8 v126, v96, v64, 0
	v_dot4_i32_i8 v127, v100, v68, 0
	v_and_b32_e32 v98, s38, v54
	v_and_b32_e32 v102, s39, v54
	v_dot4_i32_i8 v126, v97, v65, v126
	v_dot4_i32_i8 v127, v101, v69, v127
	v_and_b32_e32 v99, s38, v55
	v_and_b32_e32 v103, s39, v55
	v_dot4_i32_i8 v126, v98, v66, v126
	v_dot4_i32_i8 v127, v102, v70, v127
	v_dot4_i32_i8 v126, v99, v67, v126
	v_dot4_i32_i8 v127, v103, v71, v127
	v_and_b32_e32 v96, s38, v56
	v_and_b32_e32 v100, s39, v56
	v_and_b32_e32 v97, s38, v57
	v_and_b32_e32 v101, s39, v57
	v_lshl_add_u32 v106, v126, 4, v127
	v_lshl_add_u32 v93, v106, 1, v72
	v_dot4_i32_i8 v104, v96, v64, 0
	v_dot4_i32_i8 v105, v100, v68, 0
	v_and_b32_e32 v98, s38, v58
	v_and_b32_e32 v102, s39, v58
	v_dot4_i32_i8 v104, v97, v65, v104
	v_dot4_i32_i8 v105, v101, v69, v105
	v_and_b32_e32 v99, s38, v59
	v_and_b32_e32 v103, s39, v59
	v_dot4_i32_i8 v104, v98, v66, v104
	v_dot4_i32_i8 v105, v102, v70, v105
	v_dot4_i32_i8 v104, v99, v67, v104
	v_dot4_i32_i8 v105, v103, v71, v105
	v_and_b32_e32 v96, s38, v60
	v_and_b32_e32 v100, s39, v60
	v_and_b32_e32 v97, s38, v61
	v_and_b32_e32 v101, s39, v61
	v_lshl_add_u32 v106, v104, 4, v105
	v_lshl_add_u32 v94, v106, 1, v72
	v_dot4_i32_i8 v126, v96, v64, 0
	v_dot4_i32_i8 v127, v100, v68, 0
	v_and_b32_e32 v98, s38, v62
	v_and_b32_e32 v102, s39, v62
	v_dot4_i32_i8 v126, v97, v65, v126
	v_dot4_i32_i8 v127, v101, v69, v127
	v_and_b32_e32 v99, s38, v63
	v_and_b32_e32 v103, s39, v63
	v_dot4_i32_i8 v126, v98, v66, v126
	v_dot4_i32_i8 v127, v102, v70, v127
	v_dot4_i32_i8 v126, v99, v67, v126
	v_dot4_i32_i8 v127, v103, v71, v127
	s_nop 0
	v_readlane_b32 s36, v75, 56
	v_readlane_b32 s5, v75, 57
	v_readlane_b32 s6, v75, 58
	v_readlane_b32 s7, v75, 59
	v_lshl_add_u32 v106, v126, 4, v127
	v_lshl_add_u32 v95, v106, 1, v72
	v_add_u32_e32 v113, s36, v206
	v_add_u32_e32 v114, s5, v206
	v_add_u32_e32 v115, s6, v206
	v_add_u32_e32 v116, s7, v206
	global_load_dwordx4 v[32:35], v113, s[52:53]
	global_load_dwordx4 v[36:39], v114, s[52:53]
	global_load_dwordx4 v[40:43], v115, s[52:53]
	global_load_dwordx4 v[44:47], v116, s[52:53]
	ds_write_b128 v107, v[92:95] offset:176
	s_lshl_b64 exec, s[22:23], 44
	v_mov_b32_e32 v87, s10
	s_mov_b64 exec, -1

; #define LAS __attribute__((address_space(3)))
; #define PU_DO(R, gi) do { PU_SWITCH(R, gi) peer3_dots(R, xq, sx15, red + lane * 68, (gi)); xsv = (lane >= PG * (gi) && lane < PG * (gi) + PG) ? xs : xsv; } while (0)
; __device__ __forceinline__ void peer3_dots(const u4 (&R)[PG][2], const u4 (&xq)[2], int sx15, LAS int* redrow, int g) {
;     static_assert(PG == 4, "one 16-byte LDS store per row group");
;     int d[4];
; #pragma unroll
;     for (int k = 0; k < 4; ++k) { int a = 0, ah = 0;
; #pragma unroll
;         for (int q = 0; q < 4; ++q) { const unsigned w = R[k][0][q];
;             a = __builtin_amdgcn_sdot4((int)(w & 0x0f0f0f0fu), (int)xq[0][q], a, false); ah = __builtin_amdgcn_sdot4((int)(w & 0xf0f0f0f0u), (int)xq[1][q], ah, false); }
;         d[k] = 32 * a + 2 * ah - sx15; }
;     u4 w; w.x = (unsigned)d[0]; w.y = (unsigned)d[1]; w.z = (unsigned)d[2]; w.w = (unsigned)d[3];
;     *(LAS u4*)(redrow + 4 * g) = w;
; }
; __device__ __forceinline__ void phase_peer_bucket(const Params& P, unsigned char* ws, int l, LAS unsigned char* lds, int bid, int G, int lane, int wave) {
;     ...
;             bool pre = false; u4 A[PG][2], B[PG][2], C[PG][2], Dq[PG][2];
; #pragma unroll 1
;             for (int blk = 0; blk < total; blk += 64) { const int blen = (total - blk) < 64 ? (total - blk) : 64, ng = blen / PG;
;                 const int ev = evn; const float wv = wvn;
;                 if (blk + 64 + lane < total) { evn = __builtin_nontemporal_load(FE + blk + 64 + lane); wvn = __builtin_nontemporal_load(FW + blk + 64 + lane); }
;                 const float us = USC[ev], vs = VSC[ev];
;                 float xsv = 0.f;
;                 if (ng == 16) {
;                     const bool nextfull = blk + 128 <= total;
;                     if (!pre) { PU_ROWS(A, 0); PU_ROWS(B, 1); PU_ROWS(C, 2); }
; #pragma unroll 1
;                     for (int g = 0; g < 12; g += 4) {
;                         PU_ROWS(Dq, g + 3); PU_DO(A, g); PU_ROWS(A, g + 4); PU_DO(B, g + 1); PU_ROWS(B, g + 5); PU_DO(C, g + 2); PU_ROWS(C, g + 6); PU_DO(Dq, g + 3);
;                     }
;                     PU_ROWS(Dq, 15); PU_DO(A, 12); if (nextfull) PU_ROWS_N(A, 0); PU_DO(B, 13); if (nextfull) PU_ROWS_N(B, 1); PU_DO(C, 14); if (nextfull) PU_ROWS_N(C, 2); PU_DO(Dq, 15);
.Lq_std12:
	s_waitcnt vmcnt(8)
	v_and_b32_e32 v96, s38, v0
	v_and_b32_e32 v100, s39, v0
	v_and_b32_e32 v97, s38, v1
	v_and_b32_e32 v101, s39, v1
	v_dot4_i32_i8 v104, v96, v64, 0
	v_dot4_i32_i8 v105, v100, v68, 0
	v_and_b32_e32 v98, s38, v2
	v_and_b32_e32 v102, s39, v2
	v_dot4_i32_i8 v104, v97, v65, v104
	v_dot4_i32_i8 v105, v101, v69, v105
	v_and_b32_e32 v99, s38, v3
	v_and_b32_e32 v103, s39, v3
	v_dot4_i32_i8 v104, v98, v66, v104
	v_dot4_i32_i8 v105, v102, v70, v105
	v_dot4_i32_i8 v104, v99, v67, v104
	v_dot4_i32_i8 v105, v103, v71, v105
	v_and_b32_e32 v96, s38, v4
	v_and_b32_e32 v100, s39, v4
	v_and_b32_e32 v97, s38, v5
	v_and_b32_e32 v101, s39, v5
	v_lshl_add_u32 v106, v104, 4, v105
	v_lshl_add_u32 v92, v106, 1, v72
	v_dot4_i32_i8 v126, v96, v64, 0
	v_dot4_i32_i8 v127, v100, v68, 0
	v_and_b32_e32 v98, s38, v6
	v_and_b32_e32 v102, s39, v6
	v_dot4_i32_i8 v126, v97, v65, v126
	v_dot4_i32_i8 v127, v101, v69, v127
	v_and_b32_e32 v99, s38, v7
	v_and_b32_e32 v103, s39, v7
	v_dot4_i32_i8 v126, v98, v66, v126
	v_dot4_i32_i8 v127, v102, v70, v127
	v_dot4_i32_i8 v126, v99, v67, v126
	v_dot4_i32_i8 v127, v103, v71, v127
	v_and_b32_e32 v96, s38, v8
	v_and_b32_e32 v100, s39, v8
	v_and_b32_e32 v97, s38, v9
	v_and_b32_e32 v101, s39, v9
	v_lshl_add_u32 v106, v126, 4, v127
	v_lshl_add_u32 v93, v106, 1, v72
	v_dot4_i32_i8 v104, v96, v64, 0
	v_dot4_i32_i8 v105, v100, v68, 0
	v_and_b32_e32 v98, s38, v10
	v_and_b32_e32 v102, s39, v10
	v_dot4_i32_i8 v104, v97, v65, v104
	v_dot4_i32_i8 v105, v101, v69, v105
	v_and_b32_e32 v99, s38, v11
	v_and_b32_e32 v103, s39, v11
	v_dot4_i32_i8 v104, v98, v66, v104
	v_dot4_i32_i8 v105, v102, v70, v105
	v_dot4_i32_i8 v104, v99, v67, v104
	v_dot4_i32_i8 v105, v103, v71, v105
	v_and_b32_e32 v96, s38, v12
	v_and_b32_e32 v100, s39, v12
	v_and_b32_e32 v97, s38, v13
	v_and_b32_e32 v101, s39, v13
	v_lshl_add_u32 v106, v104, 4, v105
	v_lshl_add_u32 v94, v106, 1, v72
	v_dot4_i32_i8 v126, v96, v64, 0
	v_dot4_i32_i8 v127, v100, v68, 0
	v_and_b32_e32 v98, s38, v14
	v_and_b32_e32 v102, s39, v14
	v_dot4_i32_i8 v126, v97, v65, v126
	v_dot4_i32_i8 v127, v101, v69, v127
	v_and_b32_e32 v99, s38, v15
	v_and_b32_e32 v103, s39, v15
	v_dot4_i32_i8 v126, v98, v66, v126
	v_dot4_i32_i8 v127, v102, v70, v127
	v_dot4_i32_i8 v126, v99, v67, v126
	v_dot4_i32_i8 v127, v103, v71, v127
	s_nop 0
	v_readlane_b32 s36, v75, 60
	v_readlane_b32 s5, v75, 61
	v_readlane_b32 s6, v75, 62
	v_readlane_b32 s7, v75, 63
	v_lshl_add_u32 v106, v126, 4, v127
	v_lshl_add_u32 v95, v106, 1, v72
	v_add_u32_e32 v113, s36, v206
	v_add_u32_e32 v114, s5, v206
	v_add_u32_e32 v115, s6, v206
	v_add_u32_e32 v116, s7, v206
	global_load_dwordx4 v[48:51], v113, s[52:53]
	global_load_dwordx4 v[52:55], v114, s[52:53]
	global_load_dwordx4 v[56:59], v115, s[52:53]
	global_load_dwordx4 v[60:63], v116, s[52:53]
	ds_write_b128 v107, v[92:95] offset:192
	s_lshl_b64 exec, s[22:23], 48
	v_mov_b32_e32 v87, s10
	s_mov_b64 exec, -1

; #define LAS __attribute__((address_space(3)))
; #define PU_DO(R, gi) do { PU_SWITCH(R, gi) peer3_dots(R, xq, sx15, red + lane * 68, (gi)); xsv = (lane >= PG * (gi) && lane < PG * (gi) + PG) ? xs : xsv; } while (0)
; __device__ __forceinline__ void peer3_dots(const u4 (&R)[PG][2], const u4 (&xq)[2], int sx15, LAS int* redrow, int g) {
;     static_assert(PG == 4, "one 16-byte LDS store per row group");
;     int d[4];
; #pragma unroll
;     for (int k = 0; k < 4; ++k) { int a = 0, ah = 0;
; #pragma unroll
;         for (int q = 0; q < 4; ++q) { const unsigned w = R[k][0][q];
;             a = __builtin_amdgcn_sdot4((int)(w & 0x0f0f0f0fu), (int)xq[0][q], a, false); ah = __builtin_amdgcn_sdot4((int)(w & 0xf0f0f0f0u), (int)xq[1][q], ah, false); }
;         d[k] = 32 * a + 2 * ah - sx15; }
;     u4 w; w.x = (unsigned)d[0]; w.y = (unsigned)d[1]; w.z = (unsigned)d[2]; w.w = (unsigned)d[3];
;     *(LAS u4*)(redrow + 4 * g) = w;
; }
; __device__ __forceinline__ void phase_peer_bucket(const Params& P, unsigned char* ws, int l, LAS unsigned char* lds, int bid, int G, int lane, int wave) {
;     ...
;             bool pre = false; u4 A[PG][2], B[PG][2], C[PG][2], Dq[PG][2];
; #pragma unroll 1
;             for (int blk = 0; blk < total; blk += 64) { const int blen = (total - blk) < 64 ? (total - blk) : 64, ng = blen / PG;
;                 const int ev = evn; const float wv = wvn;
;                 if (blk + 64 + lane < total) { evn = __builtin_nontemporal_load(FE + blk + 64 + lane); wvn = __builtin_nontemporal_load(FW + blk + 64 + lane); }
;                 const float us = USC[ev], vs = VSC[ev];
;                 float xsv = 0.f;
;                 if (ng == 16) {
;                     const bool nextfull = blk + 128 <= total;
;                     if (!pre) { PU_ROWS(A, 0); PU_ROWS(B, 1); PU_ROWS(C, 2); }
; #pragma unroll 1
;                     for (int g = 0; g < 12; g += 4) {
;                         PU_ROWS(Dq, g + 3); PU_DO(A, g); PU_ROWS(A, g + 4); PU_DO(B, g + 1); PU_ROWS(B, g + 5); PU_DO(C, g + 2); PU_ROWS(C, g + 6); PU_DO(Dq, g + 3);
;                     }
;                     PU_ROWS(Dq, 15); PU_DO(A, 12); if (nextfull) PU_ROWS_N(A, 0); PU_DO(B, 13); if (nextfull) PU_ROWS_N(B, 1); PU_DO(C, 14); if (nextfull) PU_ROWS_N(C, 2); PU_DO(Dq, 15);
.Lq_std13:
	s_waitcnt vmcnt(8)
	v_and_b32_e32 v96, s38, v16
	v_and_b32_e32 v100, s39, v16
	v_and_b32_e32 v97, s38, v17
	v_and_b32_e32 v101, s39, v17
	v_dot4_i32_i8 v104, v96, v64, 0
	v_dot4_i32_i8 v105, v100, v68, 0
	v_and_b32_e32 v98, s38, v18
	v_and_b32_e32 v102, s39, v18
	v_dot4_i32_i8 v104, v97, v65, v104
	v_dot4_i32_i8 v105, v101, v69, v105
	v_and_b32_e32 v99, s38, v19
	v_and_b32_e32 v103, s39, v19
	v_dot4_i32_i8 v104, v98, v66, v104
	v_dot4_i32_i8 v105, v102, v70, v105
	v_dot4_i32_i8 v104, v99, v67, v104
	v_dot4_i32_i8 v105, v103, v71, v105
	v_and_b32_e32 v96, s38, v20
	v_and_b32_e32 v100, s39, v20
	v_and_b32_e32 v97, s38, v21
	v_and_b32_e32 v101, s39, v21
	v_lshl_add_u32 v106, v104, 4, v105
	v_lshl_add_u32 v92, v106, 1, v72
	v_dot4_i32_i8 v126, v96, v64, 0
	v_dot4_i32_i8 v127, v100, v68, 0
	v_and_b32_e32 v98, s38, v22
	v_and_b32_e32 v102, s39, v22
	v_dot4_i32_i8 v126, v97, v65, v126
	v_dot4_i32_i8 v127, v101, v69, v127
	v_and_b32_e32 v99, s38, v23
	v_and_b32_e32 v103, s39, v23
	v_dot4_i32_i8 v126, v98, v66, v126
	v_dot4_i32_i8 v127, v102, v70, v127
	v_dot4_i32_i8 v126, v99, v67, v126
	v_dot4_i32_i8 v127, v103, v71, v127
	v_and_b32_e32 v96, s38, v24
	v_and_b32_e32 v100, s39, v24
	v_and_b32_e32 v97, s38, v25
	v_and_b32_e32 v101, s39, v25
	v_lshl_add_u32 v106, v126, 4, v127
	v_lshl_add_u32 v93, v106, 1, v72
	v_dot4_i32_i8 v104, v96, v64, 0
	v_dot4_i32_i8 v105, v100, v68, 0
	v_and_b32_e32 v98, s38, v26
	v_and_b32_e32 v102, s39, v26
	v_dot4_i32_i8 v104, v97, v65, v104
	v_dot4_i32_i8 v105, v101, v69, v105
	v_and_b32_e32 v99, s38, v27
	v_and_b32_e32 v103, s39, v27
	v_dot4_i32_i8 v104, v98, v66, v104
	v_dot4_i32_i8 v105, v102, v70, v105
	v_dot4_i32_i8 v104, v99, v67, v104
	v_dot4_i32_i8 v105, v103, v71, v105
	v_and_b32_e32 v96, s38, v28
	v_and_b32_e32 v100, s39, v28
	v_and_b32_e32 v97, s38, v29
	v_and_b32_e32 v101, s39, v29
	v_lshl_add_u32 v106, v104, 4, v105
	v_lshl_add_u32 v94, v106, 1, v72
	v_dot4_i32_i8 v126, v96, v64, 0
	v_dot4_i32_i8 v127, v100, v68, 0
	v_and_b32_e32 v98, s38, v30
	v_and_b32_e32 v102, s39, v30
	v_dot4_i32_i8 v126, v97, v65, v126
	v_dot4_i32_i8 v127, v101, v69, v127
	v_and_b32_e32 v99, s38, v31
	v_and_b32_e32 v103, s39, v31
	v_dot4_i32_i8 v126, v98, v66, v126
	v_dot4_i32_i8 v127, v102, v70, v127
	v_dot4_i32_i8 v126, v99, v67, v126
	v_dot4_i32_i8 v127, v103, v71, v127
	v_lshlrev_b32_e32 v76, 10, v74
	s_nop 0
	v_readlane_b32 s36, v76, 0
	v_readlane_b32 s5, v76, 1
	v_readlane_b32 s6, v76, 2
	v_readlane_b32 s7, v76, 3
	v_lshl_add_u32 v106, v126, 4, v127
	v_lshl_add_u32 v95, v106, 1, v72
	v_add_u32_e32 v113, s36, v206
	v_add_u32_e32 v114, s5, v206
	v_add_u32_e32 v115, s6, v206
	v_add_u32_e32 v116, s7, v206
	global_load_dwordx4 v[0:3], v113, s[52:53]
	global_load_dwordx4 v[4:7], v114, s[52:53]
	global_load_dwordx4 v[8:11], v115, s[52:53]
	global_load_dwordx4 v[12:15], v116, s[52:53]
	ds_write_b128 v107, v[92:95] offset:208
	s_lshl_b64 exec, s[22:23], 52
	v_mov_b32_e32 v87, s10
	s_mov_b64 exec, -1

; #define LAS __attribute__((address_space(3)))
; #define PU_DO(R, gi) do { PU_SWITCH(R, gi) peer3_dots(R, xq, sx15, red + lane * 68, (gi)); xsv = (lane >= PG * (gi) && lane < PG * (gi) + PG) ? xs : xsv; } while (0)
; __device__ __forceinline__ void peer3_dots(const u4 (&R)[PG][2], const u4 (&xq)[2], int sx15, LAS int* redrow, int g) {
;     static_assert(PG == 4, "one 16-byte LDS store per row group");
;     int d[4];
; #pragma unroll
;     for (int k = 0; k < 4; ++k) { int a = 0, ah = 0;
; #pragma unroll
;         for (int q = 0; q < 4; ++q) { const unsigned w = R[k][0][q];
;             a = __builtin_amdgcn_sdot4((int)(w & 0x0f0f0f0fu), (int)xq[0][q], a, false); ah = __builtin_amdgcn_sdot4((int)(w & 0xf0f0f0f0u), (int)xq[1][q], ah, false); }
;         d[k] = 32 * a + 2 * ah - sx15; }
;     u4 w; w.x = (unsigned)d[0]; w.y = (unsigned)d[1]; w.z = (unsigned)d[2]; w.w = (unsigned)d[3];
;     *(LAS u4*)(redrow + 4 * g) = w;
; }
; __device__ __forceinline__ void phase_peer_bucket(const Params& P, unsigned char* ws, int l, LAS unsigned char* lds, int bid, int G, int lane, int wave) {
;     ...
;             bool pre = false; u4 A[PG][2], B[PG][2], C[PG][2], Dq[PG][2];
; #pragma unroll 1
;             for (int blk = 0; blk < total; blk += 64) { const int blen = (total - blk) < 64 ? (total - blk) : 64, ng = blen / PG;
;                 const int ev = evn; const float wv = wvn;
;                 if (blk + 64 + lane < total) { evn = __builtin_nontemporal_load(FE + blk + 64 + lane); wvn = __builtin_nontemporal_load(FW + blk + 64 + lane); }
;                 const float us = USC[ev], vs = VSC[ev];
;                 float xsv = 0.f;
;                 if (ng == 16) {
;                     const bool nextfull = blk + 128 <= total;
;                     if (!pre) { PU_ROWS(A, 0); PU_ROWS(B, 1); PU_ROWS(C, 2); }
; #pragma unroll 1
;                     for (int g = 0; g < 12; g += 4) {
;                         PU_ROWS(Dq, g + 3); PU_DO(A, g); PU_ROWS(A, g + 4); PU_DO(B, g + 1); PU_ROWS(B, g + 5); PU_DO(C, g + 2); PU_ROWS(C, g + 6); PU_DO(Dq, g + 3);
;                     }
;                     PU_ROWS(Dq, 15); PU_DO(A, 12); if (nextfull) PU_ROWS_N(A, 0); PU_DO(B, 13); if (nextfull) PU_ROWS_N(B, 1); PU_DO(C, 14); if (nextfull) PU_ROWS_N(C, 2); PU_DO(Dq, 15);
.Lq_std14:
	s_waitcnt vmcnt(8)
	v_and_b32_e32 v96, s38, v32
	v_and_b32_e32 v100, s39, v32
	v_and_b32_e32 v97, s38, v33
	v_and_b32_e32 v101, s39, v33
	v_dot4_i32_i8 v104, v96, v64, 0
	v_dot4_i32_i8 v105, v100, v68, 0
	v_and_b32_e32 v98, s38, v34
	v_and_b32_e32 v102, s39, v34
	v_dot4_i32_i8 v104, v97, v65, v104
	v_dot4_i32_i8 v105, v101, v69, v105
	v_and_b32_e32 v99, s38, v35
	v_and_b32_e32 v103, s39, v35
	v_dot4_i32_i8 v104, v98, v66, v104
	v_dot4_i32_i8 v105, v102, v70, v105
	v_dot4_i32_i8 v104, v99, v67, v104
	v_dot4_i32_i8 v105, v103, v71, v105
	v_and_b32_e32 v96, s38, v36
	v_and_b32_e32 v100, s39, v36
	v_and_b32_e32 v97, s38, v37
	v_and_b32_e32 v101, s39, v37
	v_lshl_add_u32 v106, v104, 4, v105
	v_lshl_add_u32 v92, v106, 1, v72
	v_dot4_i32_i8 v126, v96, v64, 0
	v_dot4_i32_i8 v127, v100, v68, 0
	v_and_b32_e32 v98, s38, v38
	v_and_b32_e32 v102, s39, v38
	v_dot4_i32_i8 v126, v97, v65, v126
	v_dot4_i32_i8 v127, v101, v69, v127
	v_and_b32_e32 v99, s38, v39
	v_and_b32_e32 v103, s39, v39
	v_dot4_i32_i8 v126, v98, v66, v126
	v_dot4_i32_i8 v127, v102, v70, v127
	v_dot4_i32_i8 v126, v99, v67, v126
	v_dot4_i32_i8 v127, v103, v71, v127
	v_and_b32_e32 v96, s38, v40
	v_and_b32_e32 v100, s39, v40
	v_and_b32_e32 v97, s38, v41
	v_and_b32_e32 v101, s39, v41
	v_lshl_add_u32 v106, v126, 4, v127
	v_lshl_add_u32 v93, v106, 1, v72
	v_dot4_i32_i8 v104, v96, v64, 0
	v_dot4_i32_i8 v105, v100, v68, 0
	v_and_b32_e32 v98, s38, v42
	v_and_b32_e32 v102, s39, v42
	v_dot4_i32_i8 v104, v97, v65, v104
	v_dot4_i32_i8 v105, v101, v69, v105
	v_and_b32_e32 v99, s38, v43
	v_and_b32_e32 v103, s39, v43
	v_dot4_i32_i8 v104, v98, v66, v104
	v_dot4_i32_i8 v105, v102, v70, v105
	v_dot4_i32_i8 v104, v99, v67, v104
	v_dot4_i32_i8 v105, v103, v71, v105
	v_and_b32_e32 v96, s38, v44
	v_and_b32_e32 v100, s39, v44
	v_and_b32_e32 v97, s38, v45
	v_and_b32_e32 v101, s39, v45
	v_lshl_add_u32 v106, v104, 4, v105
	v_lshl_add_u32 v94, v106, 1, v72
	v_dot4_i32_i8 v126, v96, v64, 0
	v_dot4_i32_i8 v127, v100, v68, 0
	v_and_b32_e32 v98, s38, v46
	v_and_b32_e32 v102, s39, v46
	v_dot4_i32_i8 v126, v97, v65, v126
	v_dot4_i32_i8 v127, v101, v69, v127
	v_and_b32_e32 v99, s38, v47
	v_and_b32_e32 v103, s39, v47
	v_dot4_i32_i8 v126, v98, v66, v126
	v_dot4_i32_i8 v127, v102, v70, v127
	v_dot4_i32_i8 v126, v99, v67, v126
	v_dot4_i32_i8 v127, v103, v71, v127
	s_nop 0
	v_readlane_b32 s36, v76, 4
	v_readlane_b32 s5, v76, 5
	v_readlane_b32 s6, v76, 6
	v_readlane_b32 s7, v76, 7
	v_lshl_add_u32 v106, v126, 4, v127
	v_lshl_add_u32 v95, v106, 1, v72
	v_add_u32_e32 v113, s36, v206
	v_add_u32_e32 v114, s5, v206
	v_add_u32_e32 v115, s6, v206
	v_add_u32_e32 v116, s7, v206
	global_load_dwordx4 v[16:19], v113, s[52:53]
	global_load_dwordx4 v[20:23], v114, s[52:53]
	global_load_dwordx4 v[24:27], v115, s[52:53]
	global_load_dwordx4 v[28:31], v116, s[52:53]
	ds_write_b128 v107, v[92:95] offset:224
	s_lshl_b64 exec, s[22:23], 56
	v_mov_b32_e32 v87, s10
	s_mov_b64 exec, -1

; #define LAS __attribute__((address_space(3)))
; #define PU_DO(R, gi) do { PU_SWITCH(R, gi) peer3_dots(R, xq, sx15, red + lane * 68, (gi)); xsv = (lane >= PG * (gi) && lane < PG * (gi) + PG) ? xs : xsv; } while (0)
; __device__ __forceinline__ void peer3_dots(const u4 (&R)[PG][2], const u4 (&xq)[2], int sx15, LAS int* redrow, int g) {
;     static_assert(PG == 4, "one 16-byte LDS store per row group");
;     int d[4];
; #pragma unroll
;     for (int k = 0; k < 4; ++k) { int a = 0, ah = 0;
; #pragma unroll
;         for (int q = 0; q < 4; ++q) { const unsigned w = R[k][0][q];
;             a = __builtin_amdgcn_sdot4((int)(w & 0x0f0f0f0fu), (int)xq[0][q], a, false); ah = __builtin_amdgcn_sdot4((int)(w & 0xf0f0f0f0u), (int)xq[1][q], ah, false); }
;         d[k] = 32 * a + 2 * ah - sx15; }
;     u4 w; w.x = (unsigned)d[0]; w.y = (unsigned)d[1]; w.z = (unsigned)d[2]; w.w = (unsigned)d[3];
;     *(LAS u4*)(redrow + 4 * g) = w;
; }
; __device__ __forceinline__ void phase_peer_bucket(const Params& P, unsigned char* ws, int l, LAS unsigned char* lds, int bid, int G, int lane, int wave) {
;     ...
;             bool pre = false; u4 A[PG][2], B[PG][2], C[PG][2], Dq[PG][2];
; #pragma unroll 1
;             for (int blk = 0; blk < total; blk += 64) { const int blen = (total - blk) < 64 ? (total - blk) : 64, ng = blen / PG;
;                 const int ev = evn; const float wv = wvn;
;                 if (blk + 64 + lane < total) { evn = __builtin_nontemporal_load(FE + blk + 64 + lane); wvn = __builtin_nontemporal_load(FW + blk + 64 + lane); }
;                 const float us = USC[ev], vs = VSC[ev];
;                 float xsv = 0.f;
;                 if (ng == 16) {
;                     const bool nextfull = blk + 128 <= total;
;                     if (!pre) { PU_ROWS(A, 0); PU_ROWS(B, 1); PU_ROWS(C, 2); }
; #pragma unroll 1
;                     for (int g = 0; g < 12; g += 4) {
;                         PU_ROWS(Dq, g + 3); PU_DO(A, g); PU_ROWS(A, g + 4); PU_DO(B, g + 1); PU_ROWS(B, g + 5); PU_DO(C, g + 2); PU_ROWS(C, g + 6); PU_DO(Dq, g + 3);
;                     }
;                     PU_ROWS(Dq, 15); PU_DO(A, 12); if (nextfull) PU_ROWS_N(A, 0); PU_DO(B, 13); if (nextfull) PU_ROWS_N(B, 1); PU_DO(C, 14); if (nextfull) PU_ROWS_N(C, 2); PU_DO(Dq, 15);
.Lq_std15:
	s_waitcnt vmcnt(8)
	v_and_b32_e32 v96, s38, v48
	v_and_b32_e32 v100, s39, v48
	v_and_b32_e32 v97, s38, v49
	v_and_b32_e32 v101, s39, v49
	v_dot4_i32_i8 v104, v96, v64, 0
	v_dot4_i32_i8 v105, v100, v68, 0
	v_and_b32_e32 v98, s38, v50
	v_and_b32_e32 v102, s39, v50
	v_dot4_i32_i8 v104, v97, v65, v104
	v_dot4_i32_i8 v105, v101, v69, v105
	v_and_b32_e32 v99, s38, v51
	v_and_b32_e32 v103, s39, v51
	v_dot4_i32_i8 v104, v98, v66, v104
	v_dot4_i32_i8 v105, v102, v70, v105
	v_dot4_i32_i8 v104, v99, v67, v104
	v_dot4_i32_i8 v105, v103, v71, v105
	v_and_b32_e32 v96, s38, v52
	v_and_b32_e32 v100, s39, v52
	v_and_b32_e32 v97, s38, v53
	v_and_b32_e32 v101, s39, v53
	v_lshl_add_u32 v106, v104, 4, v105
	v_lshl_add_u32 v92, v106, 1, v72
	v_dot4_i32_i8 v126, v96, v64, 0
	v_dot4_i32_i8 v127, v100, v68, 0
	v_and_b32_e32 v98, s38, v54
	v_and_b32_e32 v102, s39, v54
	v_dot4_i32_i8 v126, v97, v65, v126
	v_dot4_i32_i8 v127, v101, v69, v127
	v_and_b32_e32 v99, s38, v55
	v_and_b32_e32 v103, s39, v55
	v_dot4_i32_i8 v126, v98, v66, v126
	v_dot4_i32_i8 v127, v102, v70, v127
	v_dot4_i32_i8 v126, v99, v67, v126
	v_dot4_i32_i8 v127, v103, v71, v127
	v_and_b32_e32 v96, s38, v56
	v_and_b32_e32 v100, s39, v56
	v_and_b32_e32 v97, s38, v57
	v_and_b32_e32 v101, s39, v57
	v_lshl_add_u32 v106, v126, 4, v127
	v_lshl_add_u32 v93, v106, 1, v72
	v_dot4_i32_i8 v104, v96, v64, 0
	v_dot4_i32_i8 v105, v100, v68, 0
	v_and_b32_e32 v98, s38, v58
	v_and_b32_e32 v102, s39, v58
	v_dot4_i32_i8 v104, v97, v65, v104
	v_dot4_i32_i8 v105, v101, v69, v105
	v_and_b32_e32 v99, s38, v59
	v_and_b32_e32 v103, s39, v59
	v_dot4_i32_i8 v104, v98, v66, v104
	v_dot4_i32_i8 v105, v102, v70, v105
	v_dot4_i32_i8 v104, v99, v67, v104
	v_dot4_i32_i8 v105, v103, v71, v105
	v_and_b32_e32 v96, s38, v60
	v_and_b32_e32 v100, s39, v60
	v_and_b32_e32 v97, s38, v61
	v_and_b32_e32 v101, s39, v61
	v_lshl_add_u32 v106, v104, 4, v105
	v_lshl_add_u32 v94, v106, 1, v72
	v_dot4_i32_i8 v126, v96, v64, 0
	v_dot4_i32_i8 v127, v100, v68, 0
	v_and_b32_e32 v98, s38, v62
	v_and_b32_e32 v102, s39, v62
	v_dot4_i32_i8 v126, v97, v65, v126
	v_dot4_i32_i8 v127, v101, v69, v127
	v_and_b32_e32 v99, s38, v63
	v_and_b32_e32 v103, s39, v63
	v_dot4_i32_i8 v126, v98, v66, v126
	v_dot4_i32_i8 v127, v102, v70, v127
	v_dot4_i32_i8 v126, v99, v67, v126
	v_dot4_i32_i8 v127, v103, v71, v127
	s_nop 0
	v_readlane_b32 s36, v76, 8
	v_readlane_b32 s5, v76, 9
	v_readlane_b32 s6, v76, 10
	v_readlane_b32 s7, v76, 11
	v_lshl_add_u32 v106, v126, 4, v127
	v_lshl_add_u32 v95, v106, 1, v72
	v_add_u32_e32 v113, s36, v206
	v_add_u32_e32 v114, s5, v206
	v_add_u32_e32 v115, s6, v206
	v_add_u32_e32 v116, s7, v206
	global_load_dwordx4 v[32:35], v113, s[52:53]
	global_load_dwordx4 v[36:39], v114, s[52:53]
	global_load_dwordx4 v[40:43], v115, s[52:53]
	global_load_dwordx4 v[44:47], v116, s[52:53]
	ds_write_b128 v107, v[92:95] offset:240
	s_lshl_b64 exec, s[22:23], 60
	v_mov_b32_e32 v87, s10
	s_mov_b64 exec, -1
	s_branch .Lq_blockend

; #define PV_ROWS(R, gi) do { __builtin_amdgcn_sched_barrier(0); peer3_rows<true>(R, PV, ev, (gi), lane); __builtin_amdgcn_sched_barrier(0); } while (0)
; template <bool HALFROW = false>
; __device__ __forceinline__ void peer3_rows(u4 (&R)[PG][2], const unsigned char* __restrict__ TAB, int ev, int g, int lane) {
; #pragma unroll
;     for (int k = 0; k < PG; ++k) { const int e = __builtin_amdgcn_readlane(ev, PG * g + k);
;         if (HALFROW) { R[k][0] = *(const u4*)(TAB + (size_t)(unsigned)e * 1024u + (unsigned)lane * 16u); }
;         else { const unsigned char* rowp = TAB + (size_t)(unsigned)e * 2048u; R[k][0] = *(const u4*)(rowp + (unsigned)lane * 16u); R[k][1] = *(const u4*)(rowp + 1024u + (unsigned)lane * 16u); } }
; }
; __device__ __forceinline__ void phase_peer_bucket(const Params& P, unsigned char* ws, int l, LAS unsigned char* lds, int bid, int G, int lane, int wave) {
;     ...
;                 for (int blk = 0; blk < total; blk += 64) { const int blen = (total - blk) < 64 ? (total - blk) : 64, ng = blen / PG;
;                     const int ev = evn; int hwv; { const _Float16 hh = (_Float16)(__int_as_float(hwn) * hs); const unsigned hb = (unsigned)__builtin_bit_cast(unsigned short, hh); hwv = (int)(hb | (hb << 16)); }
;                     if (blk + 64 + lane < total) { evn = __builtin_nontemporal_load(FE + blk + 64 + lane); hwn = (int)__hip_atomic_load((const unsigned*)(FHW + blk + 64 + lane), __ATOMIC_RELAXED, __HIP_MEMORY_SCOPE_AGENT); }
;                     u4 Rb0[PG][2], Rb1[PG][2], Rb2[PG][2], Rb3[PG][2], Rb4[PG][2], Rb5[PG][2], Rb6[PG][2], Rb7[PG][2];
;                     const bool pre = false;
;     ...
;                     if (ng == 16) {
;                         const bool nextfull = false;
;                         if (!pre) { PV_ROWS(Rb0, 0); PV_ROWS(Rb1, 1); PV_ROWS(Rb2, 2); PV_ROWS(Rb3, 3); PV_ROWS(Rb4, 4); PV_ROWS(Rb5, 5); PV_ROWS(Rb6, 6); }
.Lpv_nnd_i1:
	s_mov_b32 s53, 0
	s_waitcnt vmcnt(0)
	v_mov_b32_e32 v213, v214
	v_lshlrev_b32_e32 v201, 10, v214
	v_and_b32_e32 v220, 0xffff0000, v217
	v_sub_f32_e32 v221, v217, v220
	v_perm_b32 v215, v220, v221, s43
	v_mov_b32_e32 v214, 0
	v_mov_b32_e32 v217, 0
	s_add_u32 s4, s53, 64
	v_add_u32_e32 v220, s4, v208
	v_cmp_gt_u32_e32 vcc, s28, v220
	v_lshlrev_b32_e32 v220, 2, v220
	s_and_saveexec_b64 s[6:7], vcc
	global_load_dword v214, v220, s[40:41] nt
	global_load_dword v217, v220, s[16:17] sc1
	s_or_b64 exec, exec, s[6:7]
	v_readlane_b32 s36, v201, 0
	v_readlane_b32 s5, v201, 1
	v_readlane_b32 s6, v201, 2
	v_readlane_b32 s7, v201, 3
	v_add_u32_e32 v220, s36, v206
	v_add_u32_e32 v221, s5, v206
	v_add_u32_e32 v192, s6, v206
	v_add_u32_e32 v193, s7, v206
	global_load_dwordx4 v[0:3], v220, s[44:45]
	global_load_dwordx4 v[4:7], v221, s[44:45]
	global_load_dwordx4 v[8:11], v192, s[44:45]
	global_load_dwordx4 v[12:15], v193, s[44:45]
	v_readlane_b32 s36, v201, 4
	v_readlane_b32 s5, v201, 5
	v_readlane_b32 s6, v201, 6
	v_readlane_b32 s7, v201, 7
	v_add_u32_e32 v220, s36, v206
	v_add_u32_e32 v221, s5, v206
	v_add_u32_e32 v192, s6, v206
	v_add_u32_e32 v193, s7, v206
	global_load_dwordx4 v[16:19], v220, s[44:45]
	global_load_dwordx4 v[20:23], v221, s[44:45]
	global_load_dwordx4 v[24:27], v192, s[44:45]
	global_load_dwordx4 v[28:31], v193, s[44:45]
	v_readlane_b32 s36, v201, 8
	v_readlane_b32 s5, v201, 9
	v_readlane_b32 s6, v201, 10
	v_readlane_b32 s7, v201, 11
	v_add_u32_e32 v220, s36, v206
	v_add_u32_e32 v221, s5, v206
	v_add_u32_e32 v192, s6, v206
	v_add_u32_e32 v193, s7, v206
	global_load_dwordx4 v[32:35], v220, s[44:45]
	global_load_dwordx4 v[36:39], v221, s[44:45]
	global_load_dwordx4 v[40:43], v192, s[44:45]
	global_load_dwordx4 v[44:47], v193, s[44:45]
	v_readlane_b32 s36, v201, 12
	v_readlane_b32 s5, v201, 13
	v_readlane_b32 s6, v201, 14
	v_readlane_b32 s7, v201, 15
	v_add_u32_e32 v220, s36, v206
	v_add_u32_e32 v221, s5, v206
	v_add_u32_e32 v192, s6, v206
	v_add_u32_e32 v193, s7, v206
	global_load_dwordx4 v[48:51], v220, s[44:45]
	global_load_dwordx4 v[52:55], v221, s[44:45]
	global_load_dwordx4 v[56:59], v192, s[44:45]
	global_load_dwordx4 v[60:63], v193, s[44:45]
	v_readlane_b32 s36, v201, 16
	v_readlane_b32 s5, v201, 17
	v_readlane_b32 s6, v201, 18
	v_readlane_b32 s7, v201, 19
	v_add_u32_e32 v220, s36, v206
	v_add_u32_e32 v221, s5, v206
	v_add_u32_e32 v192, s6, v206
	v_add_u32_e32 v193, s7, v206
	global_load_dwordx4 v[64:67], v220, s[44:45]
	global_load_dwordx4 v[68:71], v221, s[44:45]
	global_load_dwordx4 v[72:75], v192, s[44:45]
	global_load_dwordx4 v[76:79], v193, s[44:45]
	v_readlane_b32 s36, v201, 20
	v_readlane_b32 s5, v201, 21
	v_readlane_b32 s6, v201, 22
	v_readlane_b32 s7, v201, 23
	v_add_u32_e32 v220, s36, v206
	v_add_u32_e32 v221, s5, v206
	v_add_u32_e32 v192, s6, v206
	v_add_u32_e32 v193, s7, v206
	global_load_dwordx4 v[82:85], v220, s[44:45]
	global_load_dwordx4 v[86:89], v221, s[44:45]
	global_load_dwordx4 v[90:93], v192, s[44:45]
	global_load_dwordx4 v[94:97], v193, s[44:45]
	v_readlane_b32 s36, v201, 24
	v_readlane_b32 s5, v201, 25
	v_readlane_b32 s6, v201, 26
	v_readlane_b32 s7, v201, 27
	v_add_u32_e32 v220, s36, v206
	v_add_u32_e32 v221, s5, v206
	v_add_u32_e32 v192, s6, v206
	v_add_u32_e32 v193, s7, v206
	global_load_dwordx4 v[98:101], v220, s[44:45]
	global_load_dwordx4 v[102:105], v221, s[44:45]
	global_load_dwordx4 v[106:109], v192, s[44:45]
	global_load_dwordx4 v[110:113], v193, s[44:45]
	s_branch .Lpv_g0

; #define PV_DO(R, gi) do { PV_SWITCH(gi) peer3_axpy(R, acc, hwv, (gi)); } while (0)
; #define PV_ROWS(R, gi) do { __builtin_amdgcn_sched_barrier(0); peer3_rows<true>(R, PV, ev, (gi), lane); __builtin_amdgcn_sched_barrier(0); } while (0)
; #define PV_ROWS_N(R, gi) do { __builtin_amdgcn_sched_barrier(0); peer3_rows<true>(R, PV, evn, (gi), lane); __builtin_amdgcn_sched_barrier(0); } while (0)
; __device__ __forceinline__ void phase_peer_bucket(const Params& P, unsigned char* ws, int l, LAS unsigned char* lds, int bid, int G, int lane, int wave) {
;     ...
;                     if (ng == 16) {
;                         const bool nextfull = false;
;                         if (!pre) { PV_ROWS(Rb0, 0); PV_ROWS(Rb1, 1); PV_ROWS(Rb2, 2); PV_ROWS(Rb3, 3); PV_ROWS(Rb4, 4); PV_ROWS(Rb5, 5); PV_ROWS(Rb6, 6); }
;                         PV_ROWS(Rb7, 7); PV_DO(Rb0, 0); PV_ROWS(Rb0, 8); PV_DO(Rb1, 1); PV_ROWS(Rb1, 9); PV_DO(Rb2, 2); PV_ROWS(Rb2, 10); PV_DO(Rb3, 3); PV_ROWS(Rb3, 11); PV_DO(Rb4, 4); PV_ROWS(Rb4, 12); PV_DO(Rb5, 5); PV_ROWS(Rb5, 13); PV_DO(Rb6, 6); PV_ROWS(Rb6, 14); PV_DO(Rb7, 7);
;                         PV_ROWS(Rb7, 15); PV_DO(Rb0, 8);
;                         if (nextfull) { PV_ROWS_N(Rb0, 0); PV_DO(Rb1, 9); PV_ROWS_N(Rb1, 1); PV_DO(Rb2, 10); PV_ROWS_N(Rb2, 2); PV_DO(Rb3, 11); PV_ROWS_N(Rb3, 3); PV_DO(Rb4, 12); PV_ROWS_N(Rb4, 4); PV_DO(Rb5, 13); PV_ROWS_N(Rb5, 5); PV_DO(Rb6, 14); PV_ROWS_N(Rb6, 6); PV_DO(Rb7, 15); }
;                         else { PV_DO(Rb1, 9); PV_DO(Rb2, 10); PV_DO(Rb3, 11); PV_DO(Rb4, 12); PV_DO(Rb5, 13); PV_DO(Rb6, 14); PV_DO(Rb7, 15); }
.Lpv_g0:
	v_readlane_b32 s36, v201, 28
	v_readlane_b32 s5, v201, 29
	v_readlane_b32 s6, v201, 30
	v_readlane_b32 s7, v201, 31
	v_add_u32_e32 v220, s36, v206
	v_add_u32_e32 v221, s5, v206
	v_add_u32_e32 v192, s6, v206
	v_add_u32_e32 v193, s7, v206
	global_load_dwordx4 v[114:117], v220, s[44:45]
	global_load_dwordx4 v[118:121], v221, s[44:45]
	global_load_dwordx4 v[122:125], v192, s[44:45]
	global_load_dwordx4 v[126:129], v193, s[44:45]
	s_add_u32 s4, s53, 0
	s_cmp_ge_u32 s4, s52
	s_cbranch_scc1 .Lpv_sw0

; #define PV_DO(R, gi) do { PV_SWITCH(gi) peer3_axpy(R, acc, hwv, (gi)); } while (0)
; #define PV_ROWS(R, gi) do { __builtin_amdgcn_sched_barrier(0); peer3_rows<true>(R, PV, ev, (gi), lane); __builtin_amdgcn_sched_barrier(0); } while (0)
; #define PV_ROWS_N(R, gi) do { __builtin_amdgcn_sched_barrier(0); peer3_rows<true>(R, PV, evn, (gi), lane); __builtin_amdgcn_sched_barrier(0); } while (0)
; __device__ __forceinline__ void phase_peer_bucket(const Params& P, unsigned char* ws, int l, LAS unsigned char* lds, int bid, int G, int lane, int wave) {
;     ...
;                     if (ng == 16) {
;                         const bool nextfull = false;
;                         if (!pre) { PV_ROWS(Rb0, 0); PV_ROWS(Rb1, 1); PV_ROWS(Rb2, 2); PV_ROWS(Rb3, 3); PV_ROWS(Rb4, 4); PV_ROWS(Rb5, 5); PV_ROWS(Rb6, 6); }
;                         PV_ROWS(Rb7, 7); PV_DO(Rb0, 0); PV_ROWS(Rb0, 8); PV_DO(Rb1, 1); PV_ROWS(Rb1, 9); PV_DO(Rb2, 2); PV_ROWS(Rb2, 10); PV_DO(Rb3, 3); PV_ROWS(Rb3, 11); PV_DO(Rb4, 4); PV_ROWS(Rb4, 12); PV_DO(Rb5, 5); PV_ROWS(Rb5, 13); PV_DO(Rb6, 6); PV_ROWS(Rb6, 14); PV_DO(Rb7, 7);
;                         PV_ROWS(Rb7, 15); PV_DO(Rb0, 8);
;                         if (nextfull) { PV_ROWS_N(Rb0, 0); PV_DO(Rb1, 9); PV_ROWS_N(Rb1, 1); PV_DO(Rb2, 10); PV_ROWS_N(Rb2, 2); PV_DO(Rb3, 11); PV_ROWS_N(Rb3, 3); PV_DO(Rb4, 12); PV_ROWS_N(Rb4, 4); PV_DO(Rb5, 13); PV_ROWS_N(Rb5, 5); PV_DO(Rb6, 14); PV_ROWS_N(Rb6, 6); PV_DO(Rb7, 15); }
;                         else { PV_DO(Rb1, 9); PV_DO(Rb2, 10); PV_DO(Rb3, 11); PV_DO(Rb4, 12); PV_DO(Rb5, 13); PV_DO(Rb6, 14); PV_DO(Rb7, 15); }
.Lpv_g1:
	v_readlane_b32 s36, v201, 32
	v_readlane_b32 s5, v201, 33
	v_readlane_b32 s6, v201, 34
	v_readlane_b32 s7, v201, 35
	v_add_u32_e32 v220, s36, v206
	v_add_u32_e32 v221, s5, v206
	v_add_u32_e32 v192, s6, v206
	v_add_u32_e32 v193, s7, v206
	global_load_dwordx4 v[0:3], v220, s[44:45]
	global_load_dwordx4 v[4:7], v221, s[44:45]
	global_load_dwordx4 v[8:11], v192, s[44:45]
	global_load_dwordx4 v[12:15], v193, s[44:45]
	s_add_u32 s4, s53, 4
	s_cmp_ge_u32 s4, s52
	s_cbranch_scc1 .Lpv_sw1

; #define PV_DO(R, gi) do { PV_SWITCH(gi) peer3_axpy(R, acc, hwv, (gi)); } while (0)
; #define PV_ROWS(R, gi) do { __builtin_amdgcn_sched_barrier(0); peer3_rows<true>(R, PV, ev, (gi), lane); __builtin_amdgcn_sched_barrier(0); } while (0)
; #define PV_ROWS_N(R, gi) do { __builtin_amdgcn_sched_barrier(0); peer3_rows<true>(R, PV, evn, (gi), lane); __builtin_amdgcn_sched_barrier(0); } while (0)
; __device__ __forceinline__ void phase_peer_bucket(const Params& P, unsigned char* ws, int l, LAS unsigned char* lds, int bid, int G, int lane, int wave) {
;     ...
;                     if (ng == 16) {
;                         const bool nextfull = false;
;                         if (!pre) { PV_ROWS(Rb0, 0); PV_ROWS(Rb1, 1); PV_ROWS(Rb2, 2); PV_ROWS(Rb3, 3); PV_ROWS(Rb4, 4); PV_ROWS(Rb5, 5); PV_ROWS(Rb6, 6); }
;                         PV_ROWS(Rb7, 7); PV_DO(Rb0, 0); PV_ROWS(Rb0, 8); PV_DO(Rb1, 1); PV_ROWS(Rb1, 9); PV_DO(Rb2, 2); PV_ROWS(Rb2, 10); PV_DO(Rb3, 3); PV_ROWS(Rb3, 11); PV_DO(Rb4, 4); PV_ROWS(Rb4, 12); PV_DO(Rb5, 5); PV_ROWS(Rb5, 13); PV_DO(Rb6, 6); PV_ROWS(Rb6, 14); PV_DO(Rb7, 7);
;                         PV_ROWS(Rb7, 15); PV_DO(Rb0, 8);
;                         if (nextfull) { PV_ROWS_N(Rb0, 0); PV_DO(Rb1, 9); PV_ROWS_N(Rb1, 1); PV_DO(Rb2, 10); PV_ROWS_N(Rb2, 2); PV_DO(Rb3, 11); PV_ROWS_N(Rb3, 3); PV_DO(Rb4, 12); PV_ROWS_N(Rb4, 4); PV_DO(Rb5, 13); PV_ROWS_N(Rb5, 5); PV_DO(Rb6, 14); PV_ROWS_N(Rb6, 6); PV_DO(Rb7, 15); }
;                         else { PV_DO(Rb1, 9); PV_DO(Rb2, 10); PV_DO(Rb3, 11); PV_DO(Rb4, 12); PV_DO(Rb5, 13); PV_DO(Rb6, 14); PV_DO(Rb7, 15); }
.Lpv_g2:
	v_readlane_b32 s36, v201, 36
	v_readlane_b32 s5, v201, 37
	v_readlane_b32 s6, v201, 38
	v_readlane_b32 s7, v201, 39
	v_add_u32_e32 v220, s36, v206
	v_add_u32_e32 v221, s5, v206
	v_add_u32_e32 v192, s6, v206
	v_add_u32_e32 v193, s7, v206
	global_load_dwordx4 v[16:19], v220, s[44:45]
	global_load_dwordx4 v[20:23], v221, s[44:45]
	global_load_dwordx4 v[24:27], v192, s[44:45]
	global_load_dwordx4 v[28:31], v193, s[44:45]
	s_add_u32 s4, s53, 8
	s_cmp_ge_u32 s4, s52
	s_cbranch_scc1 .Lpv_sw2

; #define PV_DO(R, gi) do { PV_SWITCH(gi) peer3_axpy(R, acc, hwv, (gi)); } while (0)
; #define PV_ROWS(R, gi) do { __builtin_amdgcn_sched_barrier(0); peer3_rows<true>(R, PV, ev, (gi), lane); __builtin_amdgcn_sched_barrier(0); } while (0)
; #define PV_ROWS_N(R, gi) do { __builtin_amdgcn_sched_barrier(0); peer3_rows<true>(R, PV, evn, (gi), lane); __builtin_amdgcn_sched_barrier(0); } while (0)
; __device__ __forceinline__ void phase_peer_bucket(const Params& P, unsigned char* ws, int l, LAS unsigned char* lds, int bid, int G, int lane, int wave) {
;     ...
;                     if (ng == 16) {
;                         const bool nextfull = false;
;                         if (!pre) { PV_ROWS(Rb0, 0); PV_ROWS(Rb1, 1); PV_ROWS(Rb2, 2); PV_ROWS(Rb3, 3); PV_ROWS(Rb4, 4); PV_ROWS(Rb5, 5); PV_ROWS(Rb6, 6); }
;                         PV_ROWS(Rb7, 7); PV_DO(Rb0, 0); PV_ROWS(Rb0, 8); PV_DO(Rb1, 1); PV_ROWS(Rb1, 9); PV_DO(Rb2, 2); PV_ROWS(Rb2, 10); PV_DO(Rb3, 3); PV_ROWS(Rb3, 11); PV_DO(Rb4, 4); PV_ROWS(Rb4, 12); PV_DO(Rb5, 5); PV_ROWS(Rb5, 13); PV_DO(Rb6, 6); PV_ROWS(Rb6, 14); PV_DO(Rb7, 7);
;                         PV_ROWS(Rb7, 15); PV_DO(Rb0, 8);
;                         if (nextfull) { PV_ROWS_N(Rb0, 0); PV_DO(Rb1, 9); PV_ROWS_N(Rb1, 1); PV_DO(Rb2, 10); PV_ROWS_N(Rb2, 2); PV_DO(Rb3, 11); PV_ROWS_N(Rb3, 3); PV_DO(Rb4, 12); PV_ROWS_N(Rb4, 4); PV_DO(Rb5, 13); PV_ROWS_N(Rb5, 5); PV_DO(Rb6, 14); PV_ROWS_N(Rb6, 6); PV_DO(Rb7, 15); }
;                         else { PV_DO(Rb1, 9); PV_DO(Rb2, 10); PV_DO(Rb3, 11); PV_DO(Rb4, 12); PV_DO(Rb5, 13); PV_DO(Rb6, 14); PV_DO(Rb7, 15); }
.Lpv_g3:
	v_readlane_b32 s36, v201, 40
	v_readlane_b32 s5, v201, 41
	v_readlane_b32 s6, v201, 42
	v_readlane_b32 s7, v201, 43
	v_add_u32_e32 v220, s36, v206
	v_add_u32_e32 v221, s5, v206
	v_add_u32_e32 v192, s6, v206
	v_add_u32_e32 v193, s7, v206
	global_load_dwordx4 v[32:35], v220, s[44:45]
	global_load_dwordx4 v[36:39], v221, s[44:45]
	global_load_dwordx4 v[40:43], v192, s[44:45]
	global_load_dwordx4 v[44:47], v193, s[44:45]
	s_add_u32 s4, s53, 12
	s_cmp_ge_u32 s4, s52
	s_cbranch_scc1 .Lpv_sw3

; #define PV_DO(R, gi) do { PV_SWITCH(gi) peer3_axpy(R, acc, hwv, (gi)); } while (0)
; #define PV_ROWS(R, gi) do { __builtin_amdgcn_sched_barrier(0); peer3_rows<true>(R, PV, ev, (gi), lane); __builtin_amdgcn_sched_barrier(0); } while (0)
; #define PV_ROWS_N(R, gi) do { __builtin_amdgcn_sched_barrier(0); peer3_rows<true>(R, PV, evn, (gi), lane); __builtin_amdgcn_sched_barrier(0); } while (0)
; __device__ __forceinline__ void phase_peer_bucket(const Params& P, unsigned char* ws, int l, LAS unsigned char* lds, int bid, int G, int lane, int wave) {
;     ...
;                     if (ng == 16) {
;                         const bool nextfull = false;
;                         if (!pre) { PV_ROWS(Rb0, 0); PV_ROWS(Rb1, 1); PV_ROWS(Rb2, 2); PV_ROWS(Rb3, 3); PV_ROWS(Rb4, 4); PV_ROWS(Rb5, 5); PV_ROWS(Rb6, 6); }
;                         PV_ROWS(Rb7, 7); PV_DO(Rb0, 0); PV_ROWS(Rb0, 8); PV_DO(Rb1, 1); PV_ROWS(Rb1, 9); PV_DO(Rb2, 2); PV_ROWS(Rb2, 10); PV_DO(Rb3, 3); PV_ROWS(Rb3, 11); PV_DO(Rb4, 4); PV_ROWS(Rb4, 12); PV_DO(Rb5, 5); PV_ROWS(Rb5, 13); PV_DO(Rb6, 6); PV_ROWS(Rb6, 14); PV_DO(Rb7, 7);
;                         PV_ROWS(Rb7, 15); PV_DO(Rb0, 8);
;                         if (nextfull) { PV_ROWS_N(Rb0, 0); PV_DO(Rb1, 9); PV_ROWS_N(Rb1, 1); PV_DO(Rb2, 10); PV_ROWS_N(Rb2, 2); PV_DO(Rb3, 11); PV_ROWS_N(Rb3, 3); PV_DO(Rb4, 12); PV_ROWS_N(Rb4, 4); PV_DO(Rb5, 13); PV_ROWS_N(Rb5, 5); PV_DO(Rb6, 14); PV_ROWS_N(Rb6, 6); PV_DO(Rb7, 15); }
;                         else { PV_DO(Rb1, 9); PV_DO(Rb2, 10); PV_DO(Rb3, 11); PV_DO(Rb4, 12); PV_DO(Rb5, 13); PV_DO(Rb6, 14); PV_DO(Rb7, 15); }
.Lpv_g4:
	v_readlane_b32 s36, v201, 44
	v_readlane_b32 s5, v201, 45
	v_readlane_b32 s6, v201, 46
	v_readlane_b32 s7, v201, 47
	v_add_u32_e32 v220, s36, v206
	v_add_u32_e32 v221, s5, v206
	v_add_u32_e32 v192, s6, v206
	v_add_u32_e32 v193, s7, v206
	global_load_dwordx4 v[48:51], v220, s[44:45]
	global_load_dwordx4 v[52:55], v221, s[44:45]
	global_load_dwordx4 v[56:59], v192, s[44:45]
	global_load_dwordx4 v[60:63], v193, s[44:45]
	s_add_u32 s4, s53, 16
	s_cmp_ge_u32 s4, s52
	s_cbranch_scc1 .Lpv_sw4

; #define PV_DO(R, gi) do { PV_SWITCH(gi) peer3_axpy(R, acc, hwv, (gi)); } while (0)
; #define PV_ROWS(R, gi) do { __builtin_amdgcn_sched_barrier(0); peer3_rows<true>(R, PV, ev, (gi), lane); __builtin_amdgcn_sched_barrier(0); } while (0)
; #define PV_ROWS_N(R, gi) do { __builtin_amdgcn_sched_barrier(0); peer3_rows<true>(R, PV, evn, (gi), lane); __builtin_amdgcn_sched_barrier(0); } while (0)
; __device__ __forceinline__ void phase_peer_bucket(const Params& P, unsigned char* ws, int l, LAS unsigned char* lds, int bid, int G, int lane, int wave) {
;     ...
;                     if (ng == 16) {
;                         const bool nextfull = false;
;                         if (!pre) { PV_ROWS(Rb0, 0); PV_ROWS(Rb1, 1); PV_ROWS(Rb2, 2); PV_ROWS(Rb3, 3); PV_ROWS(Rb4, 4); PV_ROWS(Rb5, 5); PV_ROWS(Rb6, 6); }
;                         PV_ROWS(Rb7, 7); PV_DO(Rb0, 0); PV_ROWS(Rb0, 8); PV_DO(Rb1, 1); PV_ROWS(Rb1, 9); PV_DO(Rb2, 2); PV_ROWS(Rb2, 10); PV_DO(Rb3, 3); PV_ROWS(Rb3, 11); PV_DO(Rb4, 4); PV_ROWS(Rb4, 12); PV_DO(Rb5, 5); PV_ROWS(Rb5, 13); PV_DO(Rb6, 6); PV_ROWS(Rb6, 14); PV_DO(Rb7, 7);
;                         PV_ROWS(Rb7, 15); PV_DO(Rb0, 8);
;                         if (nextfull) { PV_ROWS_N(Rb0, 0); PV_DO(Rb1, 9); PV_ROWS_N(Rb1, 1); PV_DO(Rb2, 10); PV_ROWS_N(Rb2, 2); PV_DO(Rb3, 11); PV_ROWS_N(Rb3, 3); PV_DO(Rb4, 12); PV_ROWS_N(Rb4, 4); PV_DO(Rb5, 13); PV_ROWS_N(Rb5, 5); PV_DO(Rb6, 14); PV_ROWS_N(Rb6, 6); PV_DO(Rb7, 15); }
;                         else { PV_DO(Rb1, 9); PV_DO(Rb2, 10); PV_DO(Rb3, 11); PV_DO(Rb4, 12); PV_DO(Rb5, 13); PV_DO(Rb6, 14); PV_DO(Rb7, 15); }
.Lpv_g5:
	v_readlane_b32 s36, v201, 48
	v_readlane_b32 s5, v201, 49
	v_readlane_b32 s6, v201, 50
	v_readlane_b32 s7, v201, 51
	v_add_u32_e32 v220, s36, v206
	v_add_u32_e32 v221, s5, v206
	v_add_u32_e32 v192, s6, v206
	v_add_u32_e32 v193, s7, v206
	global_load_dwordx4 v[64:67], v220, s[44:45]
	global_load_dwordx4 v[68:71], v221, s[44:45]
	global_load_dwordx4 v[72:75], v192, s[44:45]
	global_load_dwordx4 v[76:79], v193, s[44:45]
	s_add_u32 s4, s53, 20
	s_cmp_ge_u32 s4, s52
	s_cbranch_scc1 .Lpv_sw5

; #define PV_DO(R, gi) do { PV_SWITCH(gi) peer3_axpy(R, acc, hwv, (gi)); } while (0)
; #define PV_ROWS(R, gi) do { __builtin_amdgcn_sched_barrier(0); peer3_rows<true>(R, PV, ev, (gi), lane); __builtin_amdgcn_sched_barrier(0); } while (0)
; #define PV_ROWS_N(R, gi) do { __builtin_amdgcn_sched_barrier(0); peer3_rows<true>(R, PV, evn, (gi), lane); __builtin_amdgcn_sched_barrier(0); } while (0)
; __device__ __forceinline__ void phase_peer_bucket(const Params& P, unsigned char* ws, int l, LAS unsigned char* lds, int bid, int G, int lane, int wave) {
;     ...
;                     if (ng == 16) {
;                         const bool nextfull = false;
;                         if (!pre) { PV_ROWS(Rb0, 0); PV_ROWS(Rb1, 1); PV_ROWS(Rb2, 2); PV_ROWS(Rb3, 3); PV_ROWS(Rb4, 4); PV_ROWS(Rb5, 5); PV_ROWS(Rb6, 6); }
;                         PV_ROWS(Rb7, 7); PV_DO(Rb0, 0); PV_ROWS(Rb0, 8); PV_DO(Rb1, 1); PV_ROWS(Rb1, 9); PV_DO(Rb2, 2); PV_ROWS(Rb2, 10); PV_DO(Rb3, 3); PV_ROWS(Rb3, 11); PV_DO(Rb4, 4); PV_ROWS(Rb4, 12); PV_DO(Rb5, 5); PV_ROWS(Rb5, 13); PV_DO(Rb6, 6); PV_ROWS(Rb6, 14); PV_DO(Rb7, 7);
;                         PV_ROWS(Rb7, 15); PV_DO(Rb0, 8);
;                         if (nextfull) { PV_ROWS_N(Rb0, 0); PV_DO(Rb1, 9); PV_ROWS_N(Rb1, 1); PV_DO(Rb2, 10); PV_ROWS_N(Rb2, 2); PV_DO(Rb3, 11); PV_ROWS_N(Rb3, 3); PV_DO(Rb4, 12); PV_ROWS_N(Rb4, 4); PV_DO(Rb5, 13); PV_ROWS_N(Rb5, 5); PV_DO(Rb6, 14); PV_ROWS_N(Rb6, 6); PV_DO(Rb7, 15); }
;                         else { PV_DO(Rb1, 9); PV_DO(Rb2, 10); PV_DO(Rb3, 11); PV_DO(Rb4, 12); PV_DO(Rb5, 13); PV_DO(Rb6, 14); PV_DO(Rb7, 15); }
.Lpv_g6:
	v_readlane_b32 s36, v201, 52
	v_readlane_b32 s5, v201, 53
	v_readlane_b32 s6, v201, 54
	v_readlane_b32 s7, v201, 55
	v_add_u32_e32 v220, s36, v206
	v_add_u32_e32 v221, s5, v206
	v_add_u32_e32 v192, s6, v206
	v_add_u32_e32 v193, s7, v206
	global_load_dwordx4 v[82:85], v220, s[44:45]
	global_load_dwordx4 v[86:89], v221, s[44:45]
	global_load_dwordx4 v[90:93], v192, s[44:45]
	global_load_dwordx4 v[94:97], v193, s[44:45]
	s_add_u32 s4, s53, 24
	s_cmp_ge_u32 s4, s52
	s_cbranch_scc1 .Lpv_sw6

; #define PV_DO(R, gi) do { PV_SWITCH(gi) peer3_axpy(R, acc, hwv, (gi)); } while (0)
; #define PV_ROWS(R, gi) do { __builtin_amdgcn_sched_barrier(0); peer3_rows<true>(R, PV, ev, (gi), lane); __builtin_amdgcn_sched_barrier(0); } while (0)
; #define PV_ROWS_N(R, gi) do { __builtin_amdgcn_sched_barrier(0); peer3_rows<true>(R, PV, evn, (gi), lane); __builtin_amdgcn_sched_barrier(0); } while (0)
; __device__ __forceinline__ void phase_peer_bucket(const Params& P, unsigned char* ws, int l, LAS unsigned char* lds, int bid, int G, int lane, int wave) {
;     ...
;                     if (ng == 16) {
;                         const bool nextfull = false;
;                         if (!pre) { PV_ROWS(Rb0, 0); PV_ROWS(Rb1, 1); PV_ROWS(Rb2, 2); PV_ROWS(Rb3, 3); PV_ROWS(Rb4, 4); PV_ROWS(Rb5, 5); PV_ROWS(Rb6, 6); }
;                         PV_ROWS(Rb7, 7); PV_DO(Rb0, 0); PV_ROWS(Rb0, 8); PV_DO(Rb1, 1); PV_ROWS(Rb1, 9); PV_DO(Rb2, 2); PV_ROWS(Rb2, 10); PV_DO(Rb3, 3); PV_ROWS(Rb3, 11); PV_DO(Rb4, 4); PV_ROWS(Rb4, 12); PV_DO(Rb5, 5); PV_ROWS(Rb5, 13); PV_DO(Rb6, 6); PV_ROWS(Rb6, 14); PV_DO(Rb7, 7);
;                         PV_ROWS(Rb7, 15); PV_DO(Rb0, 8);
;                         if (nextfull) { PV_ROWS_N(Rb0, 0); PV_DO(Rb1, 9); PV_ROWS_N(Rb1, 1); PV_DO(Rb2, 10); PV_ROWS_N(Rb2, 2); PV_DO(Rb3, 11); PV_ROWS_N(Rb3, 3); PV_DO(Rb4, 12); PV_ROWS_N(Rb4, 4); PV_DO(Rb5, 13); PV_ROWS_N(Rb5, 5); PV_DO(Rb6, 14); PV_ROWS_N(Rb6, 6); PV_DO(Rb7, 15); }
;                         else { PV_DO(Rb1, 9); PV_DO(Rb2, 10); PV_DO(Rb3, 11); PV_DO(Rb4, 12); PV_DO(Rb5, 13); PV_DO(Rb6, 14); PV_DO(Rb7, 15); }
.Lpv_g7:
	v_readlane_b32 s36, v201, 56
	v_readlane_b32 s5, v201, 57
	v_readlane_b32 s6, v201, 58
	v_readlane_b32 s7, v201, 59
	v_add_u32_e32 v220, s36, v206
	v_add_u32_e32 v221, s5, v206
	v_add_u32_e32 v192, s6, v206
	v_add_u32_e32 v193, s7, v206
	global_load_dwordx4 v[98:101], v220, s[44:45]
	global_load_dwordx4 v[102:105], v221, s[44:45]
	global_load_dwordx4 v[106:109], v192, s[44:45]
	global_load_dwordx4 v[110:113], v193, s[44:45]
	s_add_u32 s4, s53, 28
	s_cmp_ge_u32 s4, s52
	s_cbranch_scc1 .Lpv_sw7

; #define PV_DO(R, gi) do { PV_SWITCH(gi) peer3_axpy(R, acc, hwv, (gi)); } while (0)
; #define PV_ROWS(R, gi) do { __builtin_amdgcn_sched_barrier(0); peer3_rows<true>(R, PV, ev, (gi), lane); __builtin_amdgcn_sched_barrier(0); } while (0)
; #define PV_ROWS_N(R, gi) do { __builtin_amdgcn_sched_barrier(0); peer3_rows<true>(R, PV, evn, (gi), lane); __builtin_amdgcn_sched_barrier(0); } while (0)
; __device__ __forceinline__ void phase_peer_bucket(const Params& P, unsigned char* ws, int l, LAS unsigned char* lds, int bid, int G, int lane, int wave) {
;     ...
;                     if (ng == 16) {
;                         const bool nextfull = false;
;                         if (!pre) { PV_ROWS(Rb0, 0); PV_ROWS(Rb1, 1); PV_ROWS(Rb2, 2); PV_ROWS(Rb3, 3); PV_ROWS(Rb4, 4); PV_ROWS(Rb5, 5); PV_ROWS(Rb6, 6); }
;                         PV_ROWS(Rb7, 7); PV_DO(Rb0, 0); PV_ROWS(Rb0, 8); PV_DO(Rb1, 1); PV_ROWS(Rb1, 9); PV_DO(Rb2, 2); PV_ROWS(Rb2, 10); PV_DO(Rb3, 3); PV_ROWS(Rb3, 11); PV_DO(Rb4, 4); PV_ROWS(Rb4, 12); PV_DO(Rb5, 5); PV_ROWS(Rb5, 13); PV_DO(Rb6, 6); PV_ROWS(Rb6, 14); PV_DO(Rb7, 7);
;                         PV_ROWS(Rb7, 15); PV_DO(Rb0, 8);
;                         if (nextfull) { PV_ROWS_N(Rb0, 0); PV_DO(Rb1, 9); PV_ROWS_N(Rb1, 1); PV_DO(Rb2, 10); PV_ROWS_N(Rb2, 2); PV_DO(Rb3, 11); PV_ROWS_N(Rb3, 3); PV_DO(Rb4, 12); PV_ROWS_N(Rb4, 4); PV_DO(Rb5, 13); PV_ROWS_N(Rb5, 5); PV_DO(Rb6, 14); PV_ROWS_N(Rb6, 6); PV_DO(Rb7, 15); }
;                         else { PV_DO(Rb1, 9); PV_DO(Rb2, 10); PV_DO(Rb3, 11); PV_DO(Rb4, 12); PV_DO(Rb5, 13); PV_DO(Rb6, 14); PV_DO(Rb7, 15); }
.Lpv_g8:
	v_readlane_b32 s36, v201, 60
	v_readlane_b32 s5, v201, 61
	v_readlane_b32 s6, v201, 62
	v_readlane_b32 s7, v201, 63
	v_add_u32_e32 v220, s36, v206
	v_add_u32_e32 v221, s5, v206
	v_add_u32_e32 v192, s6, v206
	v_add_u32_e32 v193, s7, v206
	global_load_dwordx4 v[114:117], v220, s[44:45]
	global_load_dwordx4 v[118:121], v221, s[44:45]
	global_load_dwordx4 v[122:125], v192, s[44:45]
	global_load_dwordx4 v[126:129], v193, s[44:45]
	s_add_u32 s4, s53, 32
	s_cmp_ge_u32 s4, s52
	s_cbranch_scc1 .Lpv_sw8

; #define PV_DO(R, gi) do { PV_SWITCH(gi) peer3_axpy(R, acc, hwv, (gi)); } while (0)
; #define PV_ROWS(R, gi) do { __builtin_amdgcn_sched_barrier(0); peer3_rows<true>(R, PV, ev, (gi), lane); __builtin_amdgcn_sched_barrier(0); } while (0)
; #define PV_ROWS_N(R, gi) do { __builtin_amdgcn_sched_barrier(0); peer3_rows<true>(R, PV, evn, (gi), lane); __builtin_amdgcn_sched_barrier(0); } while (0)
; __device__ __forceinline__ void phase_peer_bucket(const Params& P, unsigned char* ws, int l, LAS unsigned char* lds, int bid, int G, int lane, int wave) {
;     ...
;                     if (ng == 16) {
;                         const bool nextfull = false;
;                         if (!pre) { PV_ROWS(Rb0, 0); PV_ROWS(Rb1, 1); PV_ROWS(Rb2, 2); PV_ROWS(Rb3, 3); PV_ROWS(Rb4, 4); PV_ROWS(Rb5, 5); PV_ROWS(Rb6, 6); }
;                         PV_ROWS(Rb7, 7); PV_DO(Rb0, 0); PV_ROWS(Rb0, 8); PV_DO(Rb1, 1); PV_ROWS(Rb1, 9); PV_DO(Rb2, 2); PV_ROWS(Rb2, 10); PV_DO(Rb3, 3); PV_ROWS(Rb3, 11); PV_DO(Rb4, 4); PV_ROWS(Rb4, 12); PV_DO(Rb5, 5); PV_ROWS(Rb5, 13); PV_DO(Rb6, 6); PV_ROWS(Rb6, 14); PV_DO(Rb7, 7);
;                         PV_ROWS(Rb7, 15); PV_DO(Rb0, 8);
;                         if (nextfull) { PV_ROWS_N(Rb0, 0); PV_DO(Rb1, 9); PV_ROWS_N(Rb1, 1); PV_DO(Rb2, 10); PV_ROWS_N(Rb2, 2); PV_DO(Rb3, 11); PV_ROWS_N(Rb3, 3); PV_DO(Rb4, 12); PV_ROWS_N(Rb4, 4); PV_DO(Rb5, 13); PV_ROWS_N(Rb5, 5); PV_DO(Rb6, 14); PV_ROWS_N(Rb6, 6); PV_DO(Rb7, 15); }
;                         else { PV_DO(Rb1, 9); PV_DO(Rb2, 10); PV_DO(Rb3, 11); PV_DO(Rb4, 12); PV_DO(Rb5, 13); PV_DO(Rb6, 14); PV_DO(Rb7, 15); }
.Lpv_g9:
	v_lshlrev_b32_e32 v209, 10, v214
	s_nop 0
	v_readlane_b32 s36, v209, 0
	v_readlane_b32 s5, v209, 1
	v_readlane_b32 s6, v209, 2
	v_readlane_b32 s7, v209, 3
	v_add_u32_e32 v220, s36, v206
	v_add_u32_e32 v221, s5, v206
	v_add_u32_e32 v192, s6, v206
	v_add_u32_e32 v193, s7, v206
	global_load_dwordx4 v[0:3], v220, s[44:45]
	global_load_dwordx4 v[4:7], v221, s[44:45]
	global_load_dwordx4 v[8:11], v192, s[44:45]
	global_load_dwordx4 v[12:15], v193, s[44:45]
	s_add_u32 s4, s53, 36
	s_cmp_ge_u32 s4, s52
	s_cbranch_scc1 .Lpv_sw9

; #define PV_DO(R, gi) do { PV_SWITCH(gi) peer3_axpy(R, acc, hwv, (gi)); } while (0)
; #define PV_ROWS(R, gi) do { __builtin_amdgcn_sched_barrier(0); peer3_rows<true>(R, PV, ev, (gi), lane); __builtin_amdgcn_sched_barrier(0); } while (0)
; #define PV_ROWS_N(R, gi) do { __builtin_amdgcn_sched_barrier(0); peer3_rows<true>(R, PV, evn, (gi), lane); __builtin_amdgcn_sched_barrier(0); } while (0)
; __device__ __forceinline__ void phase_peer_bucket(const Params& P, unsigned char* ws, int l, LAS unsigned char* lds, int bid, int G, int lane, int wave) {
;     ...
;                     if (ng == 16) {
;                         const bool nextfull = false;
;                         if (!pre) { PV_ROWS(Rb0, 0); PV_ROWS(Rb1, 1); PV_ROWS(Rb2, 2); PV_ROWS(Rb3, 3); PV_ROWS(Rb4, 4); PV_ROWS(Rb5, 5); PV_ROWS(Rb6, 6); }
;                         PV_ROWS(Rb7, 7); PV_DO(Rb0, 0); PV_ROWS(Rb0, 8); PV_DO(Rb1, 1); PV_ROWS(Rb1, 9); PV_DO(Rb2, 2); PV_ROWS(Rb2, 10); PV_DO(Rb3, 3); PV_ROWS(Rb3, 11); PV_DO(Rb4, 4); PV_ROWS(Rb4, 12); PV_DO(Rb5, 5); PV_ROWS(Rb5, 13); PV_DO(Rb6, 6); PV_ROWS(Rb6, 14); PV_DO(Rb7, 7);
;                         PV_ROWS(Rb7, 15); PV_DO(Rb0, 8);
;                         if (nextfull) { PV_ROWS_N(Rb0, 0); PV_DO(Rb1, 9); PV_ROWS_N(Rb1, 1); PV_DO(Rb2, 10); PV_ROWS_N(Rb2, 2); PV_DO(Rb3, 11); PV_ROWS_N(Rb3, 3); PV_DO(Rb4, 12); PV_ROWS_N(Rb4, 4); PV_DO(Rb5, 13); PV_ROWS_N(Rb5, 5); PV_DO(Rb6, 14); PV_ROWS_N(Rb6, 6); PV_DO(Rb7, 15); }
;                         else { PV_DO(Rb1, 9); PV_DO(Rb2, 10); PV_DO(Rb3, 11); PV_DO(Rb4, 12); PV_DO(Rb5, 13); PV_DO(Rb6, 14); PV_DO(Rb7, 15); }
.Lpv_g10:
	v_readlane_b32 s36, v209, 4
	v_readlane_b32 s5, v209, 5
	v_readlane_b32 s6, v209, 6
	v_readlane_b32 s7, v209, 7
	v_add_u32_e32 v220, s36, v206
	v_add_u32_e32 v221, s5, v206
	v_add_u32_e32 v192, s6, v206
	v_add_u32_e32 v193, s7, v206
	global_load_dwordx4 v[16:19], v220, s[44:45]
	global_load_dwordx4 v[20:23], v221, s[44:45]
	global_load_dwordx4 v[24:27], v192, s[44:45]
	global_load_dwordx4 v[28:31], v193, s[44:45]
	s_add_u32 s4, s53, 40
	s_cmp_ge_u32 s4, s52
	s_cbranch_scc1 .Lpv_sw10

; #define PV_DO(R, gi) do { PV_SWITCH(gi) peer3_axpy(R, acc, hwv, (gi)); } while (0)
; #define PV_ROWS(R, gi) do { __builtin_amdgcn_sched_barrier(0); peer3_rows<true>(R, PV, ev, (gi), lane); __builtin_amdgcn_sched_barrier(0); } while (0)
; #define PV_ROWS_N(R, gi) do { __builtin_amdgcn_sched_barrier(0); peer3_rows<true>(R, PV, evn, (gi), lane); __builtin_amdgcn_sched_barrier(0); } while (0)
; __device__ __forceinline__ void phase_peer_bucket(const Params& P, unsigned char* ws, int l, LAS unsigned char* lds, int bid, int G, int lane, int wave) {
;     ...
;                     if (ng == 16) {
;                         const bool nextfull = false;
;                         if (!pre) { PV_ROWS(Rb0, 0); PV_ROWS(Rb1, 1); PV_ROWS(Rb2, 2); PV_ROWS(Rb3, 3); PV_ROWS(Rb4, 4); PV_ROWS(Rb5, 5); PV_ROWS(Rb6, 6); }
;                         PV_ROWS(Rb7, 7); PV_DO(Rb0, 0); PV_ROWS(Rb0, 8); PV_DO(Rb1, 1); PV_ROWS(Rb1, 9); PV_DO(Rb2, 2); PV_ROWS(Rb2, 10); PV_DO(Rb3, 3); PV_ROWS(Rb3, 11); PV_DO(Rb4, 4); PV_ROWS(Rb4, 12); PV_DO(Rb5, 5); PV_ROWS(Rb5, 13); PV_DO(Rb6, 6); PV_ROWS(Rb6, 14); PV_DO(Rb7, 7);
;                         PV_ROWS(Rb7, 15); PV_DO(Rb0, 8);
;                         if (nextfull) { PV_ROWS_N(Rb0, 0); PV_DO(Rb1, 9); PV_ROWS_N(Rb1, 1); PV_DO(Rb2, 10); PV_ROWS_N(Rb2, 2); PV_DO(Rb3, 11); PV_ROWS_N(Rb3, 3); PV_DO(Rb4, 12); PV_ROWS_N(Rb4, 4); PV_DO(Rb5, 13); PV_ROWS_N(Rb5, 5); PV_DO(Rb6, 14); PV_ROWS_N(Rb6, 6); PV_DO(Rb7, 15); }
;                         else { PV_DO(Rb1, 9); PV_DO(Rb2, 10); PV_DO(Rb3, 11); PV_DO(Rb4, 12); PV_DO(Rb5, 13); PV_DO(Rb6, 14); PV_DO(Rb7, 15); }
.Lpv_g11:
	v_readlane_b32 s36, v209, 8
	v_readlane_b32 s5, v209, 9
	v_readlane_b32 s6, v209, 10
	v_readlane_b32 s7, v209, 11
	v_add_u32_e32 v220, s36, v206
	v_add_u32_e32 v221, s5, v206
	v_add_u32_e32 v192, s6, v206
	v_add_u32_e32 v193, s7, v206
	global_load_dwordx4 v[32:35], v220, s[44:45]
	global_load_dwordx4 v[36:39], v221, s[44:45]
	global_load_dwordx4 v[40:43], v192, s[44:45]
	global_load_dwordx4 v[44:47], v193, s[44:45]
	s_add_u32 s4, s53, 44
	s_cmp_ge_u32 s4, s52
	s_cbranch_scc1 .Lpv_sw11

; #define PV_DO(R, gi) do { PV_SWITCH(gi) peer3_axpy(R, acc, hwv, (gi)); } while (0)
; #define PV_ROWS(R, gi) do { __builtin_amdgcn_sched_barrier(0); peer3_rows<true>(R, PV, ev, (gi), lane); __builtin_amdgcn_sched_barrier(0); } while (0)
; #define PV_ROWS_N(R, gi) do { __builtin_amdgcn_sched_barrier(0); peer3_rows<true>(R, PV, evn, (gi), lane); __builtin_amdgcn_sched_barrier(0); } while (0)
; __device__ __forceinline__ void phase_peer_bucket(const Params& P, unsigned char* ws, int l, LAS unsigned char* lds, int bid, int G, int lane, int wave) {
;     ...
;                     if (ng == 16) {
;                         const bool nextfull = false;
;                         if (!pre) { PV_ROWS(Rb0, 0); PV_ROWS(Rb1, 1); PV_ROWS(Rb2, 2); PV_ROWS(Rb3, 3); PV_ROWS(Rb4, 4); PV_ROWS(Rb5, 5); PV_ROWS(Rb6, 6); }
;                         PV_ROWS(Rb7, 7); PV_DO(Rb0, 0); PV_ROWS(Rb0, 8); PV_DO(Rb1, 1); PV_ROWS(Rb1, 9); PV_DO(Rb2, 2); PV_ROWS(Rb2, 10); PV_DO(Rb3, 3); PV_ROWS(Rb3, 11); PV_DO(Rb4, 4); PV_ROWS(Rb4, 12); PV_DO(Rb5, 5); PV_ROWS(Rb5, 13); PV_DO(Rb6, 6); PV_ROWS(Rb6, 14); PV_DO(Rb7, 7);
;                         PV_ROWS(Rb7, 15); PV_DO(Rb0, 8);
;                         if (nextfull) { PV_ROWS_N(Rb0, 0); PV_DO(Rb1, 9); PV_ROWS_N(Rb1, 1); PV_DO(Rb2, 10); PV_ROWS_N(Rb2, 2); PV_DO(Rb3, 11); PV_ROWS_N(Rb3, 3); PV_DO(Rb4, 12); PV_ROWS_N(Rb4, 4); PV_DO(Rb5, 13); PV_ROWS_N(Rb5, 5); PV_DO(Rb6, 14); PV_ROWS_N(Rb6, 6); PV_DO(Rb7, 15); }
;                         else { PV_DO(Rb1, 9); PV_DO(Rb2, 10); PV_DO(Rb3, 11); PV_DO(Rb4, 12); PV_DO(Rb5, 13); PV_DO(Rb6, 14); PV_DO(Rb7, 15); }
.Lpv_g12:
	v_readlane_b32 s36, v209, 12
	v_readlane_b32 s5, v209, 13
	v_readlane_b32 s6, v209, 14
	v_readlane_b32 s7, v209, 15
	v_add_u32_e32 v220, s36, v206
	v_add_u32_e32 v221, s5, v206
	v_add_u32_e32 v192, s6, v206
	v_add_u32_e32 v193, s7, v206
	global_load_dwordx4 v[48:51], v220, s[44:45]
	global_load_dwordx4 v[52:55], v221, s[44:45]
	global_load_dwordx4 v[56:59], v192, s[44:45]
	global_load_dwordx4 v[60:63], v193, s[44:45]
	s_add_u32 s4, s53, 48
	s_cmp_ge_u32 s4, s52
	s_cbranch_scc1 .Lpv_sw12

; #define PV_DO(R, gi) do { PV_SWITCH(gi) peer3_axpy(R, acc, hwv, (gi)); } while (0)
; #define PV_ROWS(R, gi) do { __builtin_amdgcn_sched_barrier(0); peer3_rows<true>(R, PV, ev, (gi), lane); __builtin_amdgcn_sched_barrier(0); } while (0)
; #define PV_ROWS_N(R, gi) do { __builtin_amdgcn_sched_barrier(0); peer3_rows<true>(R, PV, evn, (gi), lane); __builtin_amdgcn_sched_barrier(0); } while (0)
; __device__ __forceinline__ void phase_peer_bucket(const Params& P, unsigned char* ws, int l, LAS unsigned char* lds, int bid, int G, int lane, int wave) {
;     ...
;                     if (ng == 16) {
;                         const bool nextfull = false;
;                         if (!pre) { PV_ROWS(Rb0, 0); PV_ROWS(Rb1, 1); PV_ROWS(Rb2, 2); PV_ROWS(Rb3, 3); PV_ROWS(Rb4, 4); PV_ROWS(Rb5, 5); PV_ROWS(Rb6, 6); }
;                         PV_ROWS(Rb7, 7); PV_DO(Rb0, 0); PV_ROWS(Rb0, 8); PV_DO(Rb1, 1); PV_ROWS(Rb1, 9); PV_DO(Rb2, 2); PV_ROWS(Rb2, 10); PV_DO(Rb3, 3); PV_ROWS(Rb3, 11); PV_DO(Rb4, 4); PV_ROWS(Rb4, 12); PV_DO(Rb5, 5); PV_ROWS(Rb5, 13); PV_DO(Rb6, 6); PV_ROWS(Rb6, 14); PV_DO(Rb7, 7);
;                         PV_ROWS(Rb7, 15); PV_DO(Rb0, 8);
;                         if (nextfull) { PV_ROWS_N(Rb0, 0); PV_DO(Rb1, 9); PV_ROWS_N(Rb1, 1); PV_DO(Rb2, 10); PV_ROWS_N(Rb2, 2); PV_DO(Rb3, 11); PV_ROWS_N(Rb3, 3); PV_DO(Rb4, 12); PV_ROWS_N(Rb4, 4); PV_DO(Rb5, 13); PV_ROWS_N(Rb5, 5); PV_DO(Rb6, 14); PV_ROWS_N(Rb6, 6); PV_DO(Rb7, 15); }
;                         else { PV_DO(Rb1, 9); PV_DO(Rb2, 10); PV_DO(Rb3, 11); PV_DO(Rb4, 12); PV_DO(Rb5, 13); PV_DO(Rb6, 14); PV_DO(Rb7, 15); }
.Lpv_g13:
	v_readlane_b32 s36, v209, 16
	v_readlane_b32 s5, v209, 17
	v_readlane_b32 s6, v209, 18
	v_readlane_b32 s7, v209, 19
	v_add_u32_e32 v220, s36, v206
	v_add_u32_e32 v221, s5, v206
	v_add_u32_e32 v192, s6, v206
	v_add_u32_e32 v193, s7, v206
	global_load_dwordx4 v[64:67], v220, s[44:45]
	global_load_dwordx4 v[68:71], v221, s[44:45]
	global_load_dwordx4 v[72:75], v192, s[44:45]
	global_load_dwordx4 v[76:79], v193, s[44:45]
	s_add_u32 s4, s53, 52
	s_cmp_ge_u32 s4, s52
	s_cbranch_scc1 .Lpv_sw13

; #define PV_DO(R, gi) do { PV_SWITCH(gi) peer3_axpy(R, acc, hwv, (gi)); } while (0)
; #define PV_ROWS(R, gi) do { __builtin_amdgcn_sched_barrier(0); peer3_rows<true>(R, PV, ev, (gi), lane); __builtin_amdgcn_sched_barrier(0); } while (0)
; #define PV_ROWS_N(R, gi) do { __builtin_amdgcn_sched_barrier(0); peer3_rows<true>(R, PV, evn, (gi), lane); __builtin_amdgcn_sched_barrier(0); } while (0)
; __device__ __forceinline__ void phase_peer_bucket(const Params& P, unsigned char* ws, int l, LAS unsigned char* lds, int bid, int G, int lane, int wave) {
;     ...
;                     if (ng == 16) {
;                         const bool nextfull = false;
;                         if (!pre) { PV_ROWS(Rb0, 0); PV_ROWS(Rb1, 1); PV_ROWS(Rb2, 2); PV_ROWS(Rb3, 3); PV_ROWS(Rb4, 4); PV_ROWS(Rb5, 5); PV_ROWS(Rb6, 6); }
;                         PV_ROWS(Rb7, 7); PV_DO(Rb0, 0); PV_ROWS(Rb0, 8); PV_DO(Rb1, 1); PV_ROWS(Rb1, 9); PV_DO(Rb2, 2); PV_ROWS(Rb2, 10); PV_DO(Rb3, 3); PV_ROWS(Rb3, 11); PV_DO(Rb4, 4); PV_ROWS(Rb4, 12); PV_DO(Rb5, 5); PV_ROWS(Rb5, 13); PV_DO(Rb6, 6); PV_ROWS(Rb6, 14); PV_DO(Rb7, 7);
;                         PV_ROWS(Rb7, 15); PV_DO(Rb0, 8);
;                         if (nextfull) { PV_ROWS_N(Rb0, 0); PV_DO(Rb1, 9); PV_ROWS_N(Rb1, 1); PV_DO(Rb2, 10); PV_ROWS_N(Rb2, 2); PV_DO(Rb3, 11); PV_ROWS_N(Rb3, 3); PV_DO(Rb4, 12); PV_ROWS_N(Rb4, 4); PV_DO(Rb5, 13); PV_ROWS_N(Rb5, 5); PV_DO(Rb6, 14); PV_ROWS_N(Rb6, 6); PV_DO(Rb7, 15); }
;                         else { PV_DO(Rb1, 9); PV_DO(Rb2, 10); PV_DO(Rb3, 11); PV_DO(Rb4, 12); PV_DO(Rb5, 13); PV_DO(Rb6, 14); PV_DO(Rb7, 15); }
.Lpv_g14:
	v_readlane_b32 s36, v209, 20
	v_readlane_b32 s5, v209, 21
	v_readlane_b32 s6, v209, 22
	v_readlane_b32 s7, v209, 23
	v_add_u32_e32 v220, s36, v206
	v_add_u32_e32 v221, s5, v206
	v_add_u32_e32 v192, s6, v206
	v_add_u32_e32 v193, s7, v206
	global_load_dwordx4 v[82:85], v220, s[44:45]
	global_load_dwordx4 v[86:89], v221, s[44:45]
	global_load_dwordx4 v[90:93], v192, s[44:45]
	global_load_dwordx4 v[94:97], v193, s[44:45]
	s_add_u32 s4, s53, 56
	s_cmp_ge_u32 s4, s52
	s_cbranch_scc1 .Lpv_sw14

; #define PV_DO(R, gi) do { PV_SWITCH(gi) peer3_axpy(R, acc, hwv, (gi)); } while (0)
; #define PV_ROWS(R, gi) do { __builtin_amdgcn_sched_barrier(0); peer3_rows<true>(R, PV, ev, (gi), lane); __builtin_amdgcn_sched_barrier(0); } while (0)
; #define PV_ROWS_N(R, gi) do { __builtin_amdgcn_sched_barrier(0); peer3_rows<true>(R, PV, evn, (gi), lane); __builtin_amdgcn_sched_barrier(0); } while (0)
; __device__ __forceinline__ void phase_peer_bucket(const Params& P, unsigned char* ws, int l, LAS unsigned char* lds, int bid, int G, int lane, int wave) {
;     ...
;                     if (ng == 16) {
;                         const bool nextfull = false;
;                         if (!pre) { PV_ROWS(Rb0, 0); PV_ROWS(Rb1, 1); PV_ROWS(Rb2, 2); PV_ROWS(Rb3, 3); PV_ROWS(Rb4, 4); PV_ROWS(Rb5, 5); PV_ROWS(Rb6, 6); }
;                         PV_ROWS(Rb7, 7); PV_DO(Rb0, 0); PV_ROWS(Rb0, 8); PV_DO(Rb1, 1); PV_ROWS(Rb1, 9); PV_DO(Rb2, 2); PV_ROWS(Rb2, 10); PV_DO(Rb3, 3); PV_ROWS(Rb3, 11); PV_DO(Rb4, 4); PV_ROWS(Rb4, 12); PV_DO(Rb5, 5); PV_ROWS(Rb5, 13); PV_DO(Rb6, 6); PV_ROWS(Rb6, 14); PV_DO(Rb7, 7);
;                         PV_ROWS(Rb7, 15); PV_DO(Rb0, 8);
;                         if (nextfull) { PV_ROWS_N(Rb0, 0); PV_DO(Rb1, 9); PV_ROWS_N(Rb1, 1); PV_DO(Rb2, 10); PV_ROWS_N(Rb2, 2); PV_DO(Rb3, 11); PV_ROWS_N(Rb3, 3); PV_DO(Rb4, 12); PV_ROWS_N(Rb4, 4); PV_DO(Rb5, 13); PV_ROWS_N(Rb5, 5); PV_DO(Rb6, 14); PV_ROWS_N(Rb6, 6); PV_DO(Rb7, 15); }
;                         else { PV_DO(Rb1, 9); PV_DO(Rb2, 10); PV_DO(Rb3, 11); PV_DO(Rb4, 12); PV_DO(Rb5, 13); PV_DO(Rb6, 14); PV_DO(Rb7, 15); }
.Lpv_g15:
	v_readlane_b32 s36, v209, 24
	v_readlane_b32 s5, v209, 25
	v_readlane_b32 s6, v209, 26
	v_readlane_b32 s7, v209, 27
	v_add_u32_e32 v220, s36, v206
	v_add_u32_e32 v221, s5, v206
	v_add_u32_e32 v192, s6, v206
	v_add_u32_e32 v193, s7, v206
	global_load_dwordx4 v[98:101], v220, s[44:45]
	global_load_dwordx4 v[102:105], v221, s[44:45]
	global_load_dwordx4 v[106:109], v192, s[44:45]
	global_load_dwordx4 v[110:113], v193, s[44:45]
	s_add_u32 s4, s53, 60
	s_cmp_ge_u32 s4, s52
	s_cbranch_scc1 .Lpv_sw15

; __device__ __forceinline__ void peer3_rowstore(unsigned char* __restrict__ base, float* __restrict__ scl, unsigned n, int lane, const h2 (&acch)[16], float hinv, unsigned rskew) {
;     f2 acc[16]; float am = 0.f;
; #pragma unroll
;     for (int i = 0; i < 16; ++i) { acc[i].x = (float)acch[i].x; acc[i].y = (float)acch[i].y; am = fmaxf(am, fmaxf(fabsf(acc[i].x), fabsf(acc[i].y))); }
;     am = wave_max_dpp(am);
;     const float sc = (am > 0.f) ? 6.f / am : 1.f;
;     if (lane == 0) scl[n] = (am > 0.f) ? am * hinv * (1.f / 6.f) : 0.f;
;     u4 w;
; #pragma unroll
;     for (int d = 0; d < 4; ++d) { unsigned r = 0u;
;         r = __builtin_amdgcn_cvt_scalef32_pk_fp4_f32(r, acc[4 * d].x * sc, acc[4 * d].y * sc, 1.0f, 0); r = __builtin_amdgcn_cvt_scalef32_pk_fp4_f32(r, acc[4 * d + 1].x * sc, acc[4 * d + 1].y * sc, 1.0f, 1);
;         r = __builtin_amdgcn_cvt_scalef32_pk_fp4_f32(r, acc[4 * d + 2].x * sc, acc[4 * d + 2].y * sc, 1.0f, 2); r = __builtin_amdgcn_cvt_scalef32_pk_fp4_f32(r, acc[4 * d + 3].x * sc, acc[4 * d + 3].y * sc, 1.0f, 3);
;         w[d] = r; }
;     __builtin_nontemporal_store(w, (u4*)(base + ((size_t)((n + rskew) & (unsigned)(NTOK - 1)) * 1024u + (unsigned)(16 * lane))));
; }
.Lpv_sw0:
	s_cmp_gt_u32 s51, 31
	s_cbranch_scc1 .Lpv_done
	v_pk_add_f32 v[136:137], v[136:137], v[138:139]
	v_pk_add_f32 v[140:141], v[140:141], v[142:143]
	v_pk_add_f32 v[144:145], v[144:145], v[146:147]
	v_pk_add_f32 v[148:149], v[148:149], v[150:151]
	v_pk_add_f32 v[152:153], v[152:153], v[154:155]
	v_pk_add_f32 v[156:157], v[156:157], v[158:159]
	v_pk_add_f32 v[160:161], v[160:161], v[162:163]
	v_pk_add_f32 v[164:165], v[164:165], v[166:167]
	v_pk_add_f32 v[168:169], v[168:169], v[170:171]
	v_pk_add_f32 v[172:173], v[172:173], v[174:175]
	v_pk_add_f32 v[176:177], v[176:177], v[178:179]
	v_pk_add_f32 v[180:181], v[180:181], v[182:183]
	v_pk_add_f32 v[184:185], v[184:185], v[186:187]
	v_pk_add_f32 v[188:189], v[188:189], v[190:191]
	v_pk_add_f32 v[234:235], v[234:235], v[236:237]
	v_pk_add_f32 v[238:239], v[238:239], v[240:241]
	v_max_f32_e64 v242, |v136|, |v137|
	v_max3_f32 v242, v242, |v140|, |v141|
	v_max3_f32 v242, v242, |v144|, |v145|
	v_max3_f32 v242, v242, |v148|, |v149|
	v_max3_f32 v242, v242, |v152|, |v153|
	v_max3_f32 v242, v242, |v156|, |v157|
	v_max3_f32 v242, v242, |v160|, |v161|
	v_max3_f32 v242, v242, |v164|, |v165|
	v_max3_f32 v242, v242, |v168|, |v169|
	v_max3_f32 v242, v242, |v172|, |v173|
	v_max3_f32 v242, v242, |v176|, |v177|
	v_max3_f32 v242, v242, |v180|, |v181|
	v_max3_f32 v242, v242, |v184|, |v185|
	v_max3_f32 v242, v242, |v188|, |v189|
	v_max3_f32 v242, v242, |v234|, |v235|
	v_max3_f32 v242, v242, |v238|, |v239|
	s_nop 1
	v_mov_b32_dpp v243, v242 quad_perm:[1,0,3,2] row_mask:0xf bank_mask:0xf bound_ctrl:1
	v_max_f32_e32 v243, v243, v243
	v_max_f32_e32 v242, v242, v243
	s_nop 1
	v_mov_b32_dpp v243, v242 quad_perm:[2,3,0,1] row_mask:0xf bank_mask:0xf bound_ctrl:1
	v_max_f32_e32 v243, v243, v243
	v_max_f32_e32 v242, v242, v243
	s_nop 1
	v_mov_b32_dpp v243, v242 row_half_mirror row_mask:0xf bank_mask:0xf bound_ctrl:1
	v_max_f32_e32 v243, v243, v243
	v_max_f32_e32 v242, v242, v243
	s_nop 1
	v_mov_b32_dpp v243, v242 row_mirror row_mask:0xf bank_mask:0xf bound_ctrl:1
	v_max_f32_e32 v243, v243, v243
	v_max_f32_e32 v242, v242, v243
	s_nop 1
	v_readlane_b32 s6, v242, 32
	v_readlane_b32 s7, v242, 48
	v_readlane_b32 s4, v242, 0
	v_readlane_b32 s5, v242, 16
	s_nop 1
	v_max_f32_e64 v242, s7, s7
	v_max_f32_e64 v243, s6, s6
	v_max_f32_e32 v242, v243, v242
	v_mov_b32_e32 v243, s5
	v_max3_f32 v242, s4, v243, v242
	v_cmp_lt_f32_e64 s[4:5], 0, v242
	s_add_u32 s36, s8, s50
	v_mul_f32_e32 v243, 0x3e2aaaab, v242
	s_lshl_b64 s[6:7], s[36:37], 2
	s_add_u32 s6, s46, s6
	s_addc_u32 s7, s47, s7
	v_cndmask_b32_e64 v243, 0, v243, s[4:5]
	s_and_saveexec_b64 s[54:55], s[38:39]
	global_store_dword v80, v243, s[6:7]
	s_or_b64 exec, exec, s[54:55]
	v_div_scale_f32 v243, s[6:7], v242, v242, s60
	v_rcp_f32_e32 v244, v243
	v_div_scale_f32 v245, vcc, s60, v242, s60
	v_fma_f32 v220, -v243, v244, 1.0
	v_fmac_f32_e32 v244, v220, v244
	v_mul_f32_e32 v220, v245, v244
	v_fma_f32 v221, -v243, v220, v245
	v_fmac_f32_e32 v220, v221, v244
	v_fma_f32 v243, -v243, v220, v245
	v_div_fmas_f32 v243, v243, v244, v220
	v_div_fixup_f32 v244, v243, v242, s60
	v_cndmask_b32_e64 v244, 1.0, v244, s[4:5]
	v_mov_b32_e32 v245, v244
	v_mov_b32_e32 v246, v80
	v_pk_mul_f32 v[220:221], v[244:245], v[136:137]
	v_cvt_scalef32_pk_fp4_f32 v246, v220, v221, 1.0
	v_pk_mul_f32 v[220:221], v[244:245], v[140:141]
	v_cvt_scalef32_pk_fp4_f32 v246, v220, v221, 1.0 op_sel:[0,0,1,0]
	v_pk_mul_f32 v[220:221], v[244:245], v[144:145]
	v_cvt_scalef32_pk_fp4_f32 v246, v220, v221, 1.0 op_sel:[0,0,0,1]
	v_pk_mul_f32 v[220:221], v[244:245], v[148:149]
	v_cvt_scalef32_pk_fp4_f32 v246, v220, v221, 1.0 op_sel:[0,0,1,1]
	v_mov_b32_e32 v247, v80
	v_pk_mul_f32 v[220:221], v[244:245], v[152:153]
	v_cvt_scalef32_pk_fp4_f32 v247, v220, v221, 1.0
	v_pk_mul_f32 v[220:221], v[244:245], v[156:157]
	v_cvt_scalef32_pk_fp4_f32 v247, v220, v221, 1.0 op_sel:[0,0,1,0]
	v_pk_mul_f32 v[220:221], v[244:245], v[160:161]
	v_cvt_scalef32_pk_fp4_f32 v247, v220, v221, 1.0 op_sel:[0,0,0,1]
	v_pk_mul_f32 v[220:221], v[244:245], v[164:165]
	v_cvt_scalef32_pk_fp4_f32 v247, v220, v221, 1.0 op_sel:[0,0,1,1]
	v_mov_b32_e32 v248, v80
	v_pk_mul_f32 v[220:221], v[244:245], v[168:169]
	v_cvt_scalef32_pk_fp4_f32 v248, v220, v221, 1.0
	v_pk_mul_f32 v[220:221], v[244:245], v[172:173]
	v_cvt_scalef32_pk_fp4_f32 v248, v220, v221, 1.0 op_sel:[0,0,1,0]
	v_pk_mul_f32 v[220:221], v[244:245], v[176:177]
	v_cvt_scalef32_pk_fp4_f32 v248, v220, v221, 1.0 op_sel:[0,0,0,1]
	v_pk_mul_f32 v[220:221], v[244:245], v[180:181]
	v_cvt_scalef32_pk_fp4_f32 v248, v220, v221, 1.0 op_sel:[0,0,1,1]
	v_mov_b32_e32 v249, v80
	v_pk_mul_f32 v[220:221], v[244:245], v[184:185]
	v_cvt_scalef32_pk_fp4_f32 v249, v220, v221, 1.0
	v_pk_mul_f32 v[220:221], v[244:245], v[188:189]
	v_cvt_scalef32_pk_fp4_f32 v249, v220, v221, 1.0 op_sel:[0,0,1,0]
	v_pk_mul_f32 v[220:221], v[244:245], v[234:235]
	v_cvt_scalef32_pk_fp4_f32 v249, v220, v221, 1.0 op_sel:[0,0,0,1]
	v_pk_mul_f32 v[220:221], v[244:245], v[238:239]
	v_cvt_scalef32_pk_fp4_f32 v249, v220, v221, 1.0 op_sel:[0,0,1,1]
	s_add_i32 s4, s36, s66
	s_lshl_b32 s4, s4, 10
	s_and_b32 s4, s4, 0x7ffc00
	v_or_b32_e32 v220, s4, v206
	s_nop 0
	global_store_dwordx4 v220, v[246:249], s[10:11] nt
	v_mov_b64_e32 v[136:137], 0
	v_mov_b64_e32 v[138:139], 0
	v_mov_b64_e32 v[140:141], 0
	v_mov_b64_e32 v[142:143], 0
	v_mov_b64_e32 v[144:145], 0
	v_mov_b64_e32 v[146:147], 0
	v_mov_b64_e32 v[148:149], 0
	v_mov_b64_e32 v[150:151], 0
	v_mov_b64_e32 v[152:153], 0
	v_mov_b64_e32 v[154:155], 0
	v_mov_b64_e32 v[156:157], 0
	v_mov_b64_e32 v[158:159], 0
	v_mov_b64_e32 v[160:161], 0
	v_mov_b64_e32 v[162:163], 0
	v_mov_b64_e32 v[164:165], 0
	v_mov_b64_e32 v[166:167], 0
	v_mov_b64_e32 v[168:169], 0
	v_mov_b64_e32 v[170:171], 0
	v_mov_b64_e32 v[172:173], 0
	v_mov_b64_e32 v[174:175], 0
	v_mov_b64_e32 v[176:177], 0
	v_mov_b64_e32 v[178:179], 0
	v_mov_b64_e32 v[180:181], 0
	v_mov_b64_e32 v[182:183], 0
	v_mov_b64_e32 v[184:185], 0
	v_mov_b64_e32 v[186:187], 0
	v_mov_b64_e32 v[188:189], 0
	v_mov_b64_e32 v[190:191], 0
	v_mov_b64_e32 v[234:235], 0
	v_mov_b64_e32 v[236:237], 0
	v_mov_b64_e32 v[238:239], 0
	v_mov_b64_e32 v[240:241], 0
	s_mov_b32 s50, s51
	s_add_u32 s4, s50, 1
	v_readlane_b32 s52, v81, s4
	s_add_u32 s51, s50, 1

; __device__ __forceinline__ void peer3_rowstore(unsigned char* __restrict__ base, float* __restrict__ scl, unsigned n, int lane, const h2 (&acch)[16], float hinv, unsigned rskew) {
;     f2 acc[16]; float am = 0.f;
; #pragma unroll
;     for (int i = 0; i < 16; ++i) { acc[i].x = (float)acch[i].x; acc[i].y = (float)acch[i].y; am = fmaxf(am, fmaxf(fabsf(acc[i].x), fabsf(acc[i].y))); }
;     am = wave_max_dpp(am);
;     const float sc = (am > 0.f) ? 6.f / am : 1.f;
;     if (lane == 0) scl[n] = (am > 0.f) ? am * hinv * (1.f / 6.f) : 0.f;
;     u4 w;
; #pragma unroll
;     for (int d = 0; d < 4; ++d) { unsigned r = 0u;
;         r = __builtin_amdgcn_cvt_scalef32_pk_fp4_f32(r, acc[4 * d].x * sc, acc[4 * d].y * sc, 1.0f, 0); r = __builtin_amdgcn_cvt_scalef32_pk_fp4_f32(r, acc[4 * d + 1].x * sc, acc[4 * d + 1].y * sc, 1.0f, 1);
;         r = __builtin_amdgcn_cvt_scalef32_pk_fp4_f32(r, acc[4 * d + 2].x * sc, acc[4 * d + 2].y * sc, 1.0f, 2); r = __builtin_amdgcn_cvt_scalef32_pk_fp4_f32(r, acc[4 * d + 3].x * sc, acc[4 * d + 3].y * sc, 1.0f, 3);
;         w[d] = r; }
;     __builtin_nontemporal_store(w, (u4*)(base + ((size_t)((n + rskew) & (unsigned)(NTOK - 1)) * 1024u + (unsigned)(16 * lane))));
; }
; __device__ __forceinline__ void phase_peer_bucket(const Params& P, unsigned char* ws, int l, LAS unsigned char* lds, int bid, int G, int lane, int wave) {
;     ...
;                 peer3_rowstore(PART, PSCL, nbase + tcur, lane, acc, hinv, 5u * (unsigned)x);
.Lpv_done:
	v_pk_add_f32 v[136:137], v[136:137], v[138:139]
	v_pk_add_f32 v[140:141], v[140:141], v[142:143]
	v_pk_add_f32 v[144:145], v[144:145], v[146:147]
	v_pk_add_f32 v[148:149], v[148:149], v[150:151]
	v_pk_add_f32 v[152:153], v[152:153], v[154:155]
	v_pk_add_f32 v[156:157], v[156:157], v[158:159]
	v_pk_add_f32 v[160:161], v[160:161], v[162:163]
	v_pk_add_f32 v[164:165], v[164:165], v[166:167]
	v_pk_add_f32 v[168:169], v[168:169], v[170:171]
	v_pk_add_f32 v[172:173], v[172:173], v[174:175]
	v_pk_add_f32 v[176:177], v[176:177], v[178:179]
	v_pk_add_f32 v[180:181], v[180:181], v[182:183]
	v_pk_add_f32 v[184:185], v[184:185], v[186:187]
	v_pk_add_f32 v[188:189], v[188:189], v[190:191]
	v_pk_add_f32 v[234:235], v[234:235], v[236:237]
	v_pk_add_f32 v[238:239], v[238:239], v[240:241]
	v_max_f32_e64 v242, |v136|, |v137|
	v_max3_f32 v242, v242, |v140|, |v141|
	v_max3_f32 v242, v242, |v144|, |v145|
	v_max3_f32 v242, v242, |v148|, |v149|
	v_max3_f32 v242, v242, |v152|, |v153|
	v_max3_f32 v242, v242, |v156|, |v157|
	v_max3_f32 v242, v242, |v160|, |v161|
	v_max3_f32 v242, v242, |v164|, |v165|
	v_max3_f32 v242, v242, |v168|, |v169|
	v_max3_f32 v242, v242, |v172|, |v173|
	v_max3_f32 v242, v242, |v176|, |v177|
	v_max3_f32 v242, v242, |v180|, |v181|
	v_max3_f32 v242, v242, |v184|, |v185|
	v_max3_f32 v242, v242, |v188|, |v189|
	v_max3_f32 v242, v242, |v234|, |v235|
	v_max3_f32 v242, v242, |v238|, |v239|
	s_nop 1
	v_mov_b32_dpp v243, v242 quad_perm:[1,0,3,2] row_mask:0xf bank_mask:0xf bound_ctrl:1
	v_max_f32_e32 v243, v243, v243
	v_max_f32_e32 v242, v242, v243
	s_nop 1
	v_mov_b32_dpp v243, v242 quad_perm:[2,3,0,1] row_mask:0xf bank_mask:0xf bound_ctrl:1
	v_max_f32_e32 v243, v243, v243
	v_max_f32_e32 v242, v242, v243
	s_nop 1
	v_mov_b32_dpp v243, v242 row_half_mirror row_mask:0xf bank_mask:0xf bound_ctrl:1
	v_max_f32_e32 v243, v243, v243
	v_max_f32_e32 v242, v242, v243
	s_nop 1
	v_mov_b32_dpp v243, v242 row_mirror row_mask:0xf bank_mask:0xf bound_ctrl:1
	v_max_f32_e32 v243, v243, v243
	v_max_f32_e32 v242, v242, v243
	s_nop 1
	v_readlane_b32 s6, v242, 32
	v_readlane_b32 s7, v242, 48
	v_readlane_b32 s4, v242, 0
	v_readlane_b32 s5, v242, 16
	s_nop 1
	v_max_f32_e64 v242, s7, s7
	v_max_f32_e64 v243, s6, s6
	v_max_f32_e32 v242, v243, v242
	v_mov_b32_e32 v243, s5
	v_max3_f32 v242, s4, v243, v242
	v_cmp_lt_f32_e64 s[4:5], 0, v242
	s_add_u32 s36, s8, s50
	v_mul_f32_e32 v243, 0x3e2aaaab, v242
	s_lshl_b64 s[6:7], s[36:37], 2
	s_add_u32 s6, s46, s6
	s_addc_u32 s7, s47, s7
	v_cndmask_b32_e64 v243, 0, v243, s[4:5]
	s_and_saveexec_b64 s[54:55], s[38:39]
	global_store_dword v80, v243, s[6:7]
	s_or_b64 exec, exec, s[54:55]
	v_div_scale_f32 v243, s[6:7], v242, v242, s60
	v_rcp_f32_e32 v244, v243
	v_div_scale_f32 v245, vcc, s60, v242, s60
	v_fma_f32 v220, -v243, v244, 1.0
	v_fmac_f32_e32 v244, v220, v244
	v_mul_f32_e32 v220, v245, v244
	v_fma_f32 v221, -v243, v220, v245
	v_fmac_f32_e32 v220, v221, v244
	v_fma_f32 v243, -v243, v220, v245
	v_div_fmas_f32 v243, v243, v244, v220
	v_div_fixup_f32 v244, v243, v242, s60
	v_cndmask_b32_e64 v244, 1.0, v244, s[4:5]
	v_mov_b32_e32 v245, v244
	v_mov_b32_e32 v246, v80
	v_pk_mul_f32 v[220:221], v[244:245], v[136:137]
	v_cvt_scalef32_pk_fp4_f32 v246, v220, v221, 1.0
	v_pk_mul_f32 v[220:221], v[244:245], v[140:141]
	v_cvt_scalef32_pk_fp4_f32 v246, v220, v221, 1.0 op_sel:[0,0,1,0]
	v_pk_mul_f32 v[220:221], v[244:245], v[144:145]
	v_cvt_scalef32_pk_fp4_f32 v246, v220, v221, 1.0 op_sel:[0,0,0,1]
	v_pk_mul_f32 v[220:221], v[244:245], v[148:149]
	v_cvt_scalef32_pk_fp4_f32 v246, v220, v221, 1.0 op_sel:[0,0,1,1]
	v_mov_b32_e32 v247, v80
	v_pk_mul_f32 v[220:221], v[244:245], v[152:153]
	v_cvt_scalef32_pk_fp4_f32 v247, v220, v221, 1.0
	v_pk_mul_f32 v[220:221], v[244:245], v[156:157]
	v_cvt_scalef32_pk_fp4_f32 v247, v220, v221, 1.0 op_sel:[0,0,1,0]
	v_pk_mul_f32 v[220:221], v[244:245], v[160:161]
	v_cvt_scalef32_pk_fp4_f32 v247, v220, v221, 1.0 op_sel:[0,0,0,1]
	v_pk_mul_f32 v[220:221], v[244:245], v[164:165]
	v_cvt_scalef32_pk_fp4_f32 v247, v220, v221, 1.0 op_sel:[0,0,1,1]
	v_mov_b32_e32 v248, v80
	v_pk_mul_f32 v[220:221], v[244:245], v[168:169]
	v_cvt_scalef32_pk_fp4_f32 v248, v220, v221, 1.0
	v_pk_mul_f32 v[220:221], v[244:245], v[172:173]
	v_cvt_scalef32_pk_fp4_f32 v248, v220, v221, 1.0 op_sel:[0,0,1,0]
	v_pk_mul_f32 v[220:221], v[244:245], v[176:177]
	v_cvt_scalef32_pk_fp4_f32 v248, v220, v221, 1.0 op_sel:[0,0,0,1]
	v_pk_mul_f32 v[220:221], v[244:245], v[180:181]
	v_cvt_scalef32_pk_fp4_f32 v248, v220, v221, 1.0 op_sel:[0,0,1,1]
	v_mov_b32_e32 v249, v80
	v_pk_mul_f32 v[220:221], v[244:245], v[184:185]
	v_cvt_scalef32_pk_fp4_f32 v249, v220, v221, 1.0
	v_pk_mul_f32 v[220:221], v[244:245], v[188:189]
	v_cvt_scalef32_pk_fp4_f32 v249, v220, v221, 1.0 op_sel:[0,0,1,0]
	v_pk_mul_f32 v[220:221], v[244:245], v[234:235]
	v_cvt_scalef32_pk_fp4_f32 v249, v220, v221, 1.0 op_sel:[0,0,0,1]
	v_pk_mul_f32 v[220:221], v[244:245], v[238:239]
	v_cvt_scalef32_pk_fp4_f32 v249, v220, v221, 1.0 op_sel:[0,0,1,1]
	s_add_i32 s4, s36, s66
	s_lshl_b32 s4, s4, 10
	s_and_b32 s4, s4, 0x7ffc00
	v_or_b32_e32 v220, s4, v206
	s_nop 0
	global_store_dwordx4 v220, v[246:249], s[10:11] nt
	v_mov_b64_e32 v[136:137], 0
	v_mov_b64_e32 v[138:139], 0
	v_mov_b64_e32 v[140:141], 0
	v_mov_b64_e32 v[142:143], 0
	v_mov_b64_e32 v[144:145], 0
	v_mov_b64_e32 v[146:147], 0
	v_mov_b64_e32 v[148:149], 0
	v_mov_b64_e32 v[150:151], 0
	v_mov_b64_e32 v[152:153], 0
	v_mov_b64_e32 v[154:155], 0
	v_mov_b64_e32 v[156:157], 0
	v_mov_b64_e32 v[158:159], 0
	v_mov_b64_e32 v[160:161], 0
	v_mov_b64_e32 v[162:163], 0
	v_mov_b64_e32 v[164:165], 0
	v_mov_b64_e32 v[166:167], 0
	v_mov_b64_e32 v[168:169], 0
	v_mov_b64_e32 v[170:171], 0
	v_mov_b64_e32 v[172:173], 0
	v_mov_b64_e32 v[174:175], 0
	v_mov_b64_e32 v[176:177], 0
	v_mov_b64_e32 v[178:179], 0
	v_mov_b64_e32 v[180:181], 0
	v_mov_b64_e32 v[182:183], 0
	v_mov_b64_e32 v[184:185], 0
	v_mov_b64_e32 v[186:187], 0
	v_mov_b64_e32 v[188:189], 0
	v_mov_b64_e32 v[190:191], 0
	v_mov_b64_e32 v[234:235], 0
	v_mov_b64_e32 v[236:237], 0
	v_mov_b64_e32 v[238:239], 0
	v_mov_b64_e32 v[240:241], 0
	s_mov_b32 s51, 0x5040100
	s_mov_b64 s[54:55], 0x40000
	s_mov_b32 s57, 0x800000
	s_branch .LBB0_1530
